# baseline (speedup 1.0000x reference)
.LBB0_2:
	s_or_b64 exec, exec, s[80:81]
	v_lshl_add_u32 v1, v206, 2, s22
	s_add_i32 s19, s19, 0x22200
	ds_write_b32 v1, v72
	v_lshl_or_b32 v1, v124, 3, s19
	v_lshl_add_u32 v187, v67, 2, s22
	s_movk_i32 s22, 0x110
	v_mad_u32_u24 v186, v67, s22, v1
	s_add_i32 s22, s7, 0x180
	v_and_b32_e32 v102, 15, v0
	s_lshl_b32 s27, s34, 8
	s_and_b32 s25, s22, 0x380
	s_add_i32 s22, s7, 0x280
	v_lshlrev_b32_e32 v66, 2, v124
	v_mul_u32_u24_e32 v1, 0x110, v102
	v_and_b32_e32 v209, 48, v0
	s_and_b32 s23, s22, 0x380
	s_add_i32 s22, s7, 0x300
	v_mov_b32_e32 v67, 0x200
	s_addk_i32 s27, 0x380
	v_or_b32_e32 v133, s7, v66
	v_add3_u32 v1, s19, v1, v209
	s_lshl_b32 s19, s35, 15
	v_lshlrev_b32_e32 v210, 4, v206
	v_or_b32_e32 v189, s24, v66
	s_xor_b32 s24, s7, 0x200
	s_and_b32 s22, s22, 0x300
	v_bitop3_b32 v197, s7, v66, v67 bitop3:0xde
	s_and_b32 s7, s27, 0x380
	v_lshrrev_b32_e32 v185, 4, v206
	s_ashr_i32 s11, s10, 31
	v_or_b32_e32 v184, s19, v210
	v_or_b32_e32 v188, s26, v66
	v_or_b32_e32 v198, s25, v66
	v_or_b32_e32 v196, s23, v66
	v_or_b32_e32 v195, s22, v66
	v_or_b32_e32 v194, s7, v66
	v_mov_b32_e32 v102, v133
	v_and_b32_e32 v248, 2, v206
	v_cmp_ne_u32_e32 vcc, 0, v248
	v_mov_b32_e32 v249, 0x44444444
	v_mov_b32_e32 v250, 0xeeeeeeee
	s_nop 1
	v_cndmask_b32_e32 v223, v249, v250, vcc
	v_lshrrev_b32_e32 v248, 4, v206
	v_lshl_add_u32 v248, v248, 4, 1
	v_add_u32_e32 v249, 0, v248
	v_cvt_f32_u32_e32 v249, v249
	v_add_u32_e32 v250, 1, v248
	v_cvt_f32_u32_e32 v250, v250
	v_cvt_pk_bf16_f32 v232, v249, v250
	v_add_u32_e32 v249, 2, v248
	v_cvt_f32_u32_e32 v249, v249
	v_add_u32_e32 v250, 3, v248
	v_cvt_f32_u32_e32 v250, v250
	v_cvt_pk_bf16_f32 v233, v249, v250
	v_add_u32_e32 v249, 4, v248
	v_cvt_f32_u32_e32 v249, v249
	v_add_u32_e32 v250, 5, v248
	v_cvt_f32_u32_e32 v250, v250
	v_cvt_pk_bf16_f32 v234, v249, v250
	v_add_u32_e32 v249, 6, v248
	v_cvt_f32_u32_e32 v249, v249
	v_add_u32_e32 v250, 7, v248
	v_cvt_f32_u32_e32 v250, v250
	v_cvt_pk_bf16_f32 v235, v249, v250
	v_add_u32_e32 v249, 8, v248
	v_cvt_f32_u32_e32 v249, v249
	v_add_u32_e32 v250, 9, v248
	v_cvt_f32_u32_e32 v250, v250
	v_cvt_pk_bf16_f32 v236, v249, v250
	v_add_u32_e32 v249, 10, v248
	v_cvt_f32_u32_e32 v249, v249
	v_add_u32_e32 v250, 11, v248
	v_cvt_f32_u32_e32 v250, v250
	v_cvt_pk_bf16_f32 v237, v249, v250
	v_add_u32_e32 v249, 12, v248
	v_cvt_f32_u32_e32 v249, v249
	v_add_u32_e32 v250, 13, v248
	v_cvt_f32_u32_e32 v250, v250
	v_cvt_pk_bf16_f32 v238, v249, v250
	v_add_u32_e32 v249, 14, v248
	v_cvt_f32_u32_e32 v249, v249
	v_add_u32_e32 v250, 15, v248
	v_cvt_f32_u32_e32 v250, v250
	v_cvt_pk_bf16_f32 v239, v249, v250
	v_and_b32_e32 v248, 15, v206
	v_lshrrev_b32_e32 v249, 2, v248
	v_and_b32_e32 v250, 1, v248
	v_lshl_add_u32 v249, v249, 1, v250
	v_and_b32_e32 v250, 3, v249
	v_lshrrev_b32_e32 v251, 4, v206
	v_cmp_eq_u32_e32 vcc, v250, v251
	v_lshrrev_b32_e32 v249, 2, v249
	v_cmp_ne_u32_e64 s[78:79], 0, v249
	v_mov_b32_e32 v250, 0x3f80
	v_mov_b32_e32 v251, 0x3f800000
	s_nop 1
	v_cndmask_b32_e64 v250, v250, v251, s[78:79]
	v_cndmask_b32_e32 v252, 0, v250, vcc
	s_lshr_b32 s77, s19, 15
	s_mulk_i32 s77, 0x1100
	s_add_i32 s77, s77, 0x22200
	v_lshrrev_b32_e32 v248, 4, v206
	v_and_b32_e32 v249, 1, v248
	v_lshrrev_b32_e32 v250, 1, v248
	v_lshlrev_b32_e32 v249, 6, v249
	v_lshl_add_u32 v253, v250, 1, v249
	v_and_b32_e32 v248, 15, v206
	v_cmp_eq_u32_e64 s[78:79], 0, v248
	v_mov_b32_e32 v244, v252
	v_mov_b32_e32 v245, 0
	v_mov_b32_e32 v246, 0
	v_mov_b32_e32 v247, 0
	v_mov_b64_e32 v[240:241], 0
	v_mov_b64_e32 v[242:243], 0
	s_nop 1
	v_smfmac_f32_16x16x64_bf16 v[240:243], v[244:247], v[232:239], v223
	s_nop 15
	s_nop 3
	s_and_saveexec_b64 s[80:81], s[78:79]
	v_cvt_u32_f32_e32 v248, v240
	v_add_u32_e32 v248, -1, v248
	v_lshl_add_u32 v248, v248, 2, s77
	v_add_u32_e32 v249, 0, v253
	ds_write_b32 v248, v249
	v_cvt_u32_f32_e32 v248, v241
	v_add_u32_e32 v248, -1, v248
	v_lshl_add_u32 v248, v248, 2, s77
	v_add_u32_e32 v249, 32, v253
	ds_write_b32 v248, v249
	v_cvt_u32_f32_e32 v248, v242
	v_add_u32_e32 v248, -1, v248
	v_lshl_add_u32 v248, v248, 2, s77
	v_add_u32_e32 v249, 16, v253
	ds_write_b32 v248, v249
	v_cvt_u32_f32_e32 v248, v243
	v_add_u32_e32 v248, -1, v248
	v_lshl_add_u32 v248, v248, 2, s77
	v_add_u32_e32 v249, 48, v253
	ds_write_b32 v248, v249
	s_or_b64 exec, exec, s[80:81]
	v_mov_b32_e32 v244, 0
	v_mov_b32_e32 v245, v252
	v_mov_b32_e32 v246, 0
	v_mov_b32_e32 v247, 0
	v_mov_b64_e32 v[240:241], 0
	v_mov_b64_e32 v[242:243], 0
	s_nop 1
	v_smfmac_f32_16x16x64_bf16 v[240:243], v[244:247], v[232:239], v223
	s_nop 15
	s_nop 3
	s_and_saveexec_b64 s[80:81], s[78:79]
	v_cvt_u32_f32_e32 v248, v240
	v_add_u32_e32 v248, -1, v248
	v_lshl_add_u32 v248, v248, 2, s77
	v_add_u32_e32 v249, 4, v253
	ds_write_b32 v248, v249
	v_cvt_u32_f32_e32 v248, v241
	v_add_u32_e32 v248, -1, v248
	v_lshl_add_u32 v248, v248, 2, s77
	v_add_u32_e32 v249, 36, v253
	ds_write_b32 v248, v249
	v_cvt_u32_f32_e32 v248, v242
	v_add_u32_e32 v248, -1, v248
	v_lshl_add_u32 v248, v248, 2, s77
	v_add_u32_e32 v249, 20, v253
	ds_write_b32 v248, v249
	v_cvt_u32_f32_e32 v248, v243
	v_add_u32_e32 v248, -1, v248
	v_lshl_add_u32 v248, v248, 2, s77
	v_add_u32_e32 v249, 52, v253
	ds_write_b32 v248, v249
	s_or_b64 exec, exec, s[80:81]
	v_mov_b32_e32 v244, 0
	v_mov_b32_e32 v245, 0
	v_mov_b32_e32 v246, v252
	v_mov_b32_e32 v247, 0
	v_mov_b64_e32 v[240:241], 0
	v_mov_b64_e32 v[242:243], 0
	s_nop 1
	v_smfmac_f32_16x16x64_bf16 v[240:243], v[244:247], v[232:239], v223
	s_nop 15
	s_nop 3
	s_and_saveexec_b64 s[80:81], s[78:79]
	v_cvt_u32_f32_e32 v248, v240
	v_add_u32_e32 v248, -1, v248
	v_lshl_add_u32 v248, v248, 2, s77
	v_add_u32_e32 v249, 8, v253
	ds_write_b32 v248, v249
	v_cvt_u32_f32_e32 v248, v241
	v_add_u32_e32 v248, -1, v248
	v_lshl_add_u32 v248, v248, 2, s77
	v_add_u32_e32 v249, 40, v253
	ds_write_b32 v248, v249
	v_cvt_u32_f32_e32 v248, v242
	v_add_u32_e32 v248, -1, v248
	v_lshl_add_u32 v248, v248, 2, s77
	v_add_u32_e32 v249, 24, v253
	ds_write_b32 v248, v249
	v_cvt_u32_f32_e32 v248, v243
	v_add_u32_e32 v248, -1, v248
	v_lshl_add_u32 v248, v248, 2, s77
	v_add_u32_e32 v249, 56, v253
	ds_write_b32 v248, v249
	s_or_b64 exec, exec, s[80:81]
	v_mov_b32_e32 v244, 0
	v_mov_b32_e32 v245, 0
	v_mov_b32_e32 v246, 0
	v_mov_b32_e32 v247, v252
	v_mov_b64_e32 v[240:241], 0
	v_mov_b64_e32 v[242:243], 0
	s_nop 1
	v_smfmac_f32_16x16x64_bf16 v[240:243], v[244:247], v[232:239], v223
	s_nop 15
	s_nop 3
	s_and_saveexec_b64 s[80:81], s[78:79]
	v_cvt_u32_f32_e32 v248, v240
	v_add_u32_e32 v248, -1, v248
	v_lshl_add_u32 v248, v248, 2, s77
	v_add_u32_e32 v249, 12, v253
	ds_write_b32 v248, v249
	v_cvt_u32_f32_e32 v248, v241
	v_add_u32_e32 v248, -1, v248
	v_lshl_add_u32 v248, v248, 2, s77
	v_add_u32_e32 v249, 44, v253
	ds_write_b32 v248, v249
	v_cvt_u32_f32_e32 v248, v242
	v_add_u32_e32 v248, -1, v248
	v_lshl_add_u32 v248, v248, 2, s77
	v_add_u32_e32 v249, 28, v253
	ds_write_b32 v248, v249
	v_cvt_u32_f32_e32 v248, v243
	v_add_u32_e32 v248, -1, v248
	v_lshl_add_u32 v248, v248, 2, s77
	v_add_u32_e32 v249, 60, v253
	ds_write_b32 v248, v249
	s_or_b64 exec, exec, s[80:81]
	v_bfe_u32 v248, v206, 3, 2
	v_lshrrev_b32_e32 v249, 5, v206
	v_lshlrev_b32_e32 v248, 4, v248
	v_lshl_or_b32 v248, v249, 3, v248
	v_and_b32_e32 v249, 7, v206
	v_or_b32_e32 v248, v248, v249
	v_lshl_add_u32 v248, v248, 2, s77
	s_waitcnt lgkmcnt(0)
	ds_read_b32 v254, v248
	v_and_b32_e32 v248, 15, v206
	v_bfe_u32 v249, v248, 1, 2
	v_lshrrev_b32_e32 v250, 3, v248
	v_lshlrev_b32_e32 v249, 4, v249
	v_lshl_or_b32 v249, v250, 3, v249
	v_and_b32_e32 v250, 1, v248
	v_lshl_or_b32 v249, v250, 2, v249
	v_lshl_add_u32 v249, v249, 2, s77
	ds_read_b128 v[248:251], v249
	s_lshr_b32 s76, s19, 6
	s_add_i32 s76, s76, 0x20000
	v_lshrrev_b32_e32 v252, 4, v206
	v_lshl_add_u32 v252, v252, 7, s76
	s_waitcnt lgkmcnt(0)
	v_add_u32_e32 v248, v252, v248
	v_add_u32_e32 v249, v252, v249
	v_add_u32_e32 v250, v252, v250
	v_add_u32_e32 v251, v252, v251
	v_cvt_pk_bf16_f32 v236, v224, v225
	v_cvt_pk_bf16_f32 v237, v226, v227
	v_lshlrev_b32_e32 v238, 16, v236
	v_and_b32_e32 v239, 0xffff0000, v236
	v_lshlrev_b32_e32 v240, 16, v237
	v_and_b32_e32 v241, 0xffff0000, v237
	v_sub_f32_e32 v238, v224, v238
	v_sub_f32_e32 v239, v225, v239
	v_sub_f32_e32 v240, v226, v240
	v_sub_f32_e32 v241, v227, v241
	v_cvt_pk_bf16_f32 v238, v238, v239
	v_cvt_pk_bf16_f32 v239, v240, v241
	ds_write_b16 v248, v236
	ds_write_b16_d16_hi v249, v236
	ds_write_b16 v250, v237
	ds_write_b16_d16_hi v251, v237
	ds_write_b16 v248, v238 offset:2176
	ds_write_b16_d16_hi v249, v238 offset:2176
	ds_write_b16 v250, v239 offset:2176
	ds_write_b16_d16_hi v251, v239 offset:2176
	s_waitcnt vmcnt(23)
	s_waitcnt vmcnt(22)
	s_waitcnt vmcnt(21)
	s_waitcnt vmcnt(20)
	s_waitcnt vmcnt(19)
	s_waitcnt vmcnt(18)
	s_waitcnt vmcnt(17)
	s_waitcnt vmcnt(16)
	ds_read_b32 v232, v187 offset:192
	ds_read_b32 v234, v187 offset:200
	ds_read_b32 v236, v187 offset:208
	ds_read_b32 v238, v187 offset:216
	ds_read_b32 v240, v187 offset:224
	ds_read_b32 v242, v187 offset:232
	ds_read_b32 v244, v187 offset:240
	ds_read_b32 v246, v187 offset:248
	v_or_b32_e32 v103, 48, v132
	v_add_u32_e32 v104, 1, v102
	v_cmp_eq_u32_e32 vcc, v102, v103
	v_add_u32_e32 v105, 3, v102
	v_add_u32_e32 v106, 2, v102
	v_cndmask_b32_e64 v72, 0, 1.0, vcc
	v_cmp_eq_u32_e32 vcc, v104, v103
	v_or_b32_e32 v107, 50, v132
	v_or_b32_e32 v108, 52, v132
	v_cndmask_b32_e64 v73, 0, 1.0, vcc
	v_cmp_eq_u32_e32 vcc, v105, v103
	s_waitcnt lgkmcnt(0)
	v_pk_fma_f32 v[68:69], v[232:233], v[68:69], v[72:73] op_sel_hi:[0,1,1] neg_lo:[1,0,0] neg_hi:[1,0,0]
	v_cvt_pk_bf16_f32 v68, v68, v69
	v_cndmask_b32_e64 v73, 0, 1.0, vcc
	v_cmp_eq_u32_e32 vcc, v106, v103
	v_or_b32_e32 v109, 54, v132
	v_or_b32_e32 v110, 56, v132
	v_cndmask_b32_e64 v72, 0, 1.0, vcc
	v_pk_fma_f32 v[66:67], v[232:233], v[70:71], v[72:73] op_sel_hi:[0,1,1] neg_lo:[1,0,0] neg_hi:[1,0,0]
	v_cvt_pk_bf16_f32 v69, v66, v67
	ds_write_b64 v186, v[68:69]
	v_cmp_eq_u32_e32 vcc, v102, v107
	v_or_b32_e32 v111, 58, v132
	v_or_b32_e32 v112, 60, v132
	v_cndmask_b32_e64 v68, 0, 1.0, vcc
	v_cmp_eq_u32_e32 vcc, v104, v107
	v_or_b32_e32 v113, 62, v132
	v_or_b32_e32 v193, 2, v132
	v_cndmask_b32_e64 v69, 0, 1.0, vcc
	v_cmp_eq_u32_e32 vcc, v105, v107
	v_pk_fma_f32 v[68:69], v[234:235], v[78:79], v[68:69] op_sel_hi:[0,1,1] neg_lo:[1,0,0] neg_hi:[1,0,0]
	v_cvt_pk_bf16_f32 v68, v68, v69
	v_cndmask_b32_e64 v71, 0, 1.0, vcc
	v_cmp_eq_u32_e32 vcc, v106, v107
	v_or_b32_e32 v192, 4, v132
	v_or_b32_e32 v190, 6, v132
	v_cndmask_b32_e64 v70, 0, 1.0, vcc
	v_pk_fma_f32 v[66:67], v[234:235], v[80:81], v[70:71] op_sel_hi:[0,1,1] neg_lo:[1,0,0] neg_hi:[1,0,0]
	v_cvt_pk_bf16_f32 v69, v66, v67
	ds_write_b64 v186, v[68:69] offset:544
	v_cmp_eq_u32_e32 vcc, v102, v108
	v_or_b32_e32 v149, 8, v132
	v_or_b32_e32 v148, 10, v132
	v_cndmask_b32_e64 v68, 0, 1.0, vcc
	v_cmp_eq_u32_e32 vcc, v104, v108
	v_or_b32_e32 v147, 12, v132
	v_or_b32_e32 v146, 14, v132
	v_cndmask_b32_e64 v69, 0, 1.0, vcc
	v_cmp_eq_u32_e32 vcc, v105, v108
	v_pk_fma_f32 v[68:69], v[236:237], v[82:83], v[68:69] op_sel_hi:[0,1,1] neg_lo:[1,0,0] neg_hi:[1,0,0]
	v_cvt_pk_bf16_f32 v68, v68, v69
	v_cndmask_b32_e64 v71, 0, 1.0, vcc
	v_cmp_eq_u32_e32 vcc, v106, v108
	s_nop 1
	v_cndmask_b32_e64 v70, 0, 1.0, vcc
	v_pk_fma_f32 v[66:67], v[236:237], v[84:85], v[70:71] op_sel_hi:[0,1,1] neg_lo:[1,0,0] neg_hi:[1,0,0]
	v_cvt_pk_bf16_f32 v69, v66, v67
	ds_write_b64 v186, v[68:69] offset:1088
	v_cmp_eq_u32_e32 vcc, v102, v109
	s_nop 1
	v_cndmask_b32_e64 v68, 0, 1.0, vcc
	v_cmp_eq_u32_e32 vcc, v104, v109
	s_nop 1
	v_cndmask_b32_e64 v69, 0, 1.0, vcc
	v_cmp_eq_u32_e32 vcc, v105, v109
	v_pk_fma_f32 v[68:69], v[238:239], v[90:91], v[68:69] op_sel_hi:[0,1,1] neg_lo:[1,0,0] neg_hi:[1,0,0]
	v_cvt_pk_bf16_f32 v68, v68, v69
	v_cndmask_b32_e64 v71, 0, 1.0, vcc
	v_cmp_eq_u32_e32 vcc, v106, v109
	s_nop 1
	v_cndmask_b32_e64 v70, 0, 1.0, vcc
	v_pk_fma_f32 v[66:67], v[238:239], v[92:93], v[70:71] op_sel_hi:[0,1,1] neg_lo:[1,0,0] neg_hi:[1,0,0]
	v_cvt_pk_bf16_f32 v69, v66, v67
	ds_write_b64 v186, v[68:69] offset:1632
	v_cmp_eq_u32_e32 vcc, v102, v110
	s_nop 1
	v_cndmask_b32_e64 v68, 0, 1.0, vcc
	v_cmp_eq_u32_e32 vcc, v104, v110
	s_nop 1
	v_cndmask_b32_e64 v69, 0, 1.0, vcc
	v_cmp_eq_u32_e32 vcc, v105, v110
	v_pk_fma_f32 v[68:69], v[240:241], v[98:99], v[68:69] op_sel_hi:[0,1,1] neg_lo:[1,0,0] neg_hi:[1,0,0]
	v_cvt_pk_bf16_f32 v68, v68, v69
	v_cndmask_b32_e64 v71, 0, 1.0, vcc
	v_cmp_eq_u32_e32 vcc, v106, v110
	s_nop 1
	v_cndmask_b32_e64 v70, 0, 1.0, vcc
	v_pk_fma_f32 v[66:67], v[240:241], v[100:101], v[70:71] op_sel_hi:[0,1,1] neg_lo:[1,0,0] neg_hi:[1,0,0]
	v_cvt_pk_bf16_f32 v69, v66, v67
	ds_write_b64 v186, v[68:69] offset:2176
	v_cmp_eq_u32_e32 vcc, v102, v111
	s_nop 1
	v_cndmask_b32_e64 v68, 0, 1.0, vcc
	v_cmp_eq_u32_e32 vcc, v104, v111
	s_nop 1
	v_cndmask_b32_e64 v69, 0, 1.0, vcc
	v_cmp_eq_u32_e32 vcc, v105, v111
	v_pk_fma_f32 v[62:63], v[242:243], v[62:63], v[68:69] op_sel_hi:[0,1,1] neg_lo:[1,0,0] neg_hi:[1,0,0]
	v_cvt_pk_bf16_f32 v62, v62, v63
	v_cndmask_b32_e64 v69, 0, 1.0, vcc
	v_cmp_eq_u32_e32 vcc, v106, v111
	s_nop 1
	v_cndmask_b32_e64 v68, 0, 1.0, vcc
	v_pk_fma_f32 v[64:65], v[242:243], v[64:65], v[68:69] op_sel_hi:[0,1,1] neg_lo:[1,0,0] neg_hi:[1,0,0]
	v_cvt_pk_bf16_f32 v63, v64, v65
	ds_write_b64 v186, v[62:63] offset:2720
	v_cmp_eq_u32_e32 vcc, v102, v112
	s_nop 1
	v_cndmask_b32_e64 v64, 0, 1.0, vcc
	v_cmp_eq_u32_e32 vcc, v104, v112
	s_nop 1
	v_cndmask_b32_e64 v65, 0, 1.0, vcc
	v_cmp_eq_u32_e32 vcc, v105, v112
	v_pk_fma_f32 v[54:55], v[244:245], v[54:55], v[64:65] op_sel_hi:[0,1,1] neg_lo:[1,0,0] neg_hi:[1,0,0]
	v_cvt_pk_bf16_f32 v54, v54, v55
	v_cndmask_b32_e64 v65, 0, 1.0, vcc
	v_cmp_eq_u32_e32 vcc, v106, v112
	s_nop 1
	v_cndmask_b32_e64 v64, 0, 1.0, vcc
	v_pk_fma_f32 v[56:57], v[244:245], v[56:57], v[64:65] op_sel_hi:[0,1,1] neg_lo:[1,0,0] neg_hi:[1,0,0]
	v_cvt_pk_bf16_f32 v55, v56, v57
	ds_write_b64 v186, v[54:55] offset:3264
	v_cmp_eq_u32_e32 vcc, v102, v113
	s_nop 1
	v_cndmask_b32_e64 v56, 0, 1.0, vcc
	v_cmp_eq_u32_e32 vcc, v104, v113
	s_nop 1
	v_cndmask_b32_e64 v57, 0, 1.0, vcc
	v_cmp_eq_u32_e32 vcc, v105, v113
	v_pk_fma_f32 v[46:47], v[246:247], v[46:47], v[56:57] op_sel_hi:[0,1,1] neg_lo:[1,0,0] neg_hi:[1,0,0]
	v_cvt_pk_bf16_f32 v46, v46, v47
	v_cndmask_b32_e64 v57, 0, 1.0, vcc
	v_cmp_eq_u32_e32 vcc, v106, v113
	s_nop 1
	v_cndmask_b32_e64 v56, 0, 1.0, vcc
	v_pk_fma_f32 v[48:49], v[246:247], v[48:49], v[56:57] op_sel_hi:[0,1,1] neg_lo:[1,0,0] neg_hi:[1,0,0]
	v_cvt_pk_bf16_f32 v47, v48, v49
	ds_write_b64 v186, v[46:47] offset:3808
	ds_read_b128 v[232:235], v1
	ds_read_b128 v[236:239], v1 offset:64
	ds_read_b128 v[240:243], v1 offset:128
	ds_read_b128 v[244:247], v1 offset:192
	s_waitcnt lgkmcnt(0)
	ds_write_b128 v184, v[232:235]
	ds_write_b128 v184, v[236:239] offset:1024
	ds_write_b128 v184, v[240:243] offset:2048
	ds_write_b128 v184, v[244:247] offset:3072
	ds_read_b32 v232, v187 offset:192
	ds_read_b32 v234, v187 offset:200
	ds_read_b32 v236, v187 offset:208
	ds_read_b32 v238, v187 offset:216
	ds_read_b32 v240, v187 offset:224
	ds_read_b32 v242, v187 offset:232
	ds_read_b32 v244, v187 offset:240
	ds_read_b32 v246, v187 offset:248
	s_lshl_b32 s30, s25, 2
	s_mov_b32 s31, s21
	v_lshl_add_u64 v[46:47], v[126:127], 0, s[30:31]
	v_lshl_add_u64 v[48:49], v[128:129], 0, s[30:31]
	v_lshl_add_u64 v[54:55], v[134:135], 0, s[30:31]
	v_lshl_add_u64 v[56:57], v[136:137], 0, s[30:31]
	v_lshl_add_u64 v[62:63], v[138:139], 0, s[30:31]
	v_lshl_add_u64 v[64:65], v[140:141], 0, s[30:31]
	v_lshl_add_u64 v[98:99], v[142:143], 0, s[30:31]
	v_lshl_add_u64 v[100:101], v[144:145], 0, s[30:31]
	global_load_dwordx4 v[90:93], v[46:47], off nt
	global_load_dwordx4 v[82:85], v[48:49], off nt
	global_load_dwordx4 v[78:81], v[54:55], off nt
	global_load_dwordx4 v[70:73], v[56:57], off nt
	global_load_dwordx4 v[66:69], v[62:63], off nt
	s_nop 0
	global_load_dwordx4 v[62:65], v[64:65], off nt
	s_nop 0
	global_load_dwordx4 v[54:57], v[98:99], off nt
	global_load_dwordx4 v[46:49], v[100:101], off nt
	v_mov_b32_e32 v99, v189
	s_waitcnt vmcnt(23)
	s_waitcnt vmcnt(22)
	s_waitcnt vmcnt(21)
	s_waitcnt vmcnt(20)
	s_waitcnt vmcnt(19)
	s_waitcnt vmcnt(18)
	s_waitcnt vmcnt(17)
	s_waitcnt vmcnt(16)
	v_add_u32_e32 v102, 1, v99
	v_cmp_eq_u32_e32 vcc, v99, v103
	v_add_u32_e32 v104, 3, v99
	v_add_u32_e32 v105, 2, v99
	v_cndmask_b32_e64 v100, 0, 1.0, vcc
	v_cmp_eq_u32_e32 vcc, v102, v103
	s_nop 1
	v_cndmask_b32_e64 v101, 0, 1.0, vcc
	v_cmp_eq_u32_e32 vcc, v104, v103
	s_waitcnt lgkmcnt(0)
	v_pk_fma_f32 v[94:95], v[232:233], v[94:95], v[100:101] op_sel_hi:[0,1,1] neg_lo:[1,0,0] neg_hi:[1,0,0]
	v_cvt_pk_bf16_f32 v94, v94, v95
	v_cndmask_b32_e64 v101, 0, 1.0, vcc
	v_cmp_eq_u32_e32 vcc, v105, v103
	s_nop 1
	v_cndmask_b32_e64 v100, 0, 1.0, vcc
	v_pk_fma_f32 v[96:97], v[232:233], v[96:97], v[100:101] op_sel_hi:[0,1,1] neg_lo:[1,0,0] neg_hi:[1,0,0]
	v_cvt_pk_bf16_f32 v95, v96, v97
	ds_write_b64 v186, v[94:95]
	v_cmp_eq_u32_e32 vcc, v99, v107
	s_nop 1
	v_cndmask_b32_e64 v96, 0, 1.0, vcc
	v_cmp_eq_u32_e32 vcc, v102, v107
	s_nop 1
	v_cndmask_b32_e64 v97, 0, 1.0, vcc
	v_cmp_eq_u32_e32 vcc, v104, v107
	v_pk_fma_f32 v[86:87], v[234:235], v[86:87], v[96:97] op_sel_hi:[0,1,1] neg_lo:[1,0,0] neg_hi:[1,0,0]
	v_cvt_pk_bf16_f32 v86, v86, v87
	v_cndmask_b32_e64 v97, 0, 1.0, vcc
	v_cmp_eq_u32_e32 vcc, v105, v107
	s_nop 1
	v_cndmask_b32_e64 v96, 0, 1.0, vcc
	v_pk_fma_f32 v[88:89], v[234:235], v[88:89], v[96:97] op_sel_hi:[0,1,1] neg_lo:[1,0,0] neg_hi:[1,0,0]
	v_cvt_pk_bf16_f32 v87, v88, v89
	ds_write_b64 v186, v[86:87] offset:544
	v_cmp_eq_u32_e32 vcc, v99, v108
	s_nop 1
	v_cndmask_b32_e64 v88, 0, 1.0, vcc
	v_cmp_eq_u32_e32 vcc, v102, v108
	s_nop 1
	v_cndmask_b32_e64 v89, 0, 1.0, vcc
	v_cmp_eq_u32_e32 vcc, v104, v108
	v_pk_fma_f32 v[74:75], v[236:237], v[74:75], v[88:89] op_sel_hi:[0,1,1] neg_lo:[1,0,0] neg_hi:[1,0,0]
	v_cvt_pk_bf16_f32 v74, v74, v75
	v_cndmask_b32_e64 v89, 0, 1.0, vcc
	v_cmp_eq_u32_e32 vcc, v105, v108
	s_nop 1
	v_cndmask_b32_e64 v88, 0, 1.0, vcc
	v_pk_fma_f32 v[76:77], v[236:237], v[76:77], v[88:89] op_sel_hi:[0,1,1] neg_lo:[1,0,0] neg_hi:[1,0,0]
	v_cvt_pk_bf16_f32 v75, v76, v77
	ds_write_b64 v186, v[74:75] offset:1088
	v_cmp_eq_u32_e32 vcc, v99, v109
	s_nop 1
	v_cndmask_b32_e64 v76, 0, 1.0, vcc
	v_cmp_eq_u32_e32 vcc, v102, v109
	s_nop 1
	v_cndmask_b32_e64 v77, 0, 1.0, vcc
	v_cmp_eq_u32_e32 vcc, v104, v109
	v_pk_fma_f32 v[58:59], v[238:239], v[58:59], v[76:77] op_sel_hi:[0,1,1] neg_lo:[1,0,0] neg_hi:[1,0,0]
	v_cvt_pk_bf16_f32 v58, v58, v59
	v_cndmask_b32_e64 v77, 0, 1.0, vcc
	v_cmp_eq_u32_e32 vcc, v105, v109
	s_nop 1
	v_cndmask_b32_e64 v76, 0, 1.0, vcc
	v_pk_fma_f32 v[60:61], v[238:239], v[60:61], v[76:77] op_sel_hi:[0,1,1] neg_lo:[1,0,0] neg_hi:[1,0,0]
	v_cvt_pk_bf16_f32 v59, v60, v61
	ds_write_b64 v186, v[58:59] offset:1632
	v_cmp_eq_u32_e32 vcc, v99, v110
	s_nop 1
	v_cndmask_b32_e64 v60, 0, 1.0, vcc
	v_cmp_eq_u32_e32 vcc, v102, v110
	s_nop 1
	v_cndmask_b32_e64 v61, 0, 1.0, vcc
	v_cmp_eq_u32_e32 vcc, v104, v110
	v_pk_fma_f32 v[50:51], v[240:241], v[50:51], v[60:61] op_sel_hi:[0,1,1] neg_lo:[1,0,0] neg_hi:[1,0,0]
	v_cvt_pk_bf16_f32 v50, v50, v51
	v_cndmask_b32_e64 v61, 0, 1.0, vcc
	v_cmp_eq_u32_e32 vcc, v105, v110
	s_nop 1
	v_cndmask_b32_e64 v60, 0, 1.0, vcc
	v_pk_fma_f32 v[52:53], v[240:241], v[52:53], v[60:61] op_sel_hi:[0,1,1] neg_lo:[1,0,0] neg_hi:[1,0,0]
	v_cvt_pk_bf16_f32 v51, v52, v53
	ds_write_b64 v186, v[50:51] offset:2176
	v_cmp_eq_u32_e32 vcc, v99, v111
	s_nop 1
	v_cndmask_b32_e64 v52, 0, 1.0, vcc
	v_cmp_eq_u32_e32 vcc, v102, v111
	s_nop 1
	v_cndmask_b32_e64 v53, 0, 1.0, vcc
	v_cmp_eq_u32_e32 vcc, v104, v111
	v_pk_fma_f32 v[42:43], v[242:243], v[42:43], v[52:53] op_sel_hi:[0,1,1] neg_lo:[1,0,0] neg_hi:[1,0,0]
	v_cvt_pk_bf16_f32 v42, v42, v43
	v_cndmask_b32_e64 v53, 0, 1.0, vcc
	v_cmp_eq_u32_e32 vcc, v105, v111
	s_nop 1
	v_cndmask_b32_e64 v52, 0, 1.0, vcc
	v_pk_fma_f32 v[44:45], v[242:243], v[44:45], v[52:53] op_sel_hi:[0,1,1] neg_lo:[1,0,0] neg_hi:[1,0,0]
	v_cvt_pk_bf16_f32 v43, v44, v45
	ds_write_b64 v186, v[42:43] offset:2720
	v_cmp_eq_u32_e32 vcc, v99, v112
	s_nop 1
	v_cndmask_b32_e64 v44, 0, 1.0, vcc
	v_cmp_eq_u32_e32 vcc, v102, v112
	s_nop 1
	v_cndmask_b32_e64 v45, 0, 1.0, vcc
	v_cmp_eq_u32_e32 vcc, v104, v112
	v_pk_fma_f32 v[38:39], v[244:245], v[38:39], v[44:45] op_sel_hi:[0,1,1] neg_lo:[1,0,0] neg_hi:[1,0,0]
	v_cvt_pk_bf16_f32 v38, v38, v39
	v_cndmask_b32_e64 v45, 0, 1.0, vcc
	v_cmp_eq_u32_e32 vcc, v105, v112
	s_nop 1
	v_cndmask_b32_e64 v44, 0, 1.0, vcc
	v_pk_fma_f32 v[40:41], v[244:245], v[40:41], v[44:45] op_sel_hi:[0,1,1] neg_lo:[1,0,0] neg_hi:[1,0,0]
	v_cvt_pk_bf16_f32 v39, v40, v41
	ds_write_b64 v186, v[38:39] offset:3264
	v_cmp_eq_u32_e32 vcc, v99, v113
	s_nop 1
	v_cndmask_b32_e64 v40, 0, 1.0, vcc
	v_cmp_eq_u32_e32 vcc, v102, v113
	s_nop 1
	v_cndmask_b32_e64 v41, 0, 1.0, vcc
	v_cmp_eq_u32_e32 vcc, v104, v113
	v_pk_fma_f32 v[34:35], v[246:247], v[34:35], v[40:41] op_sel_hi:[0,1,1] neg_lo:[1,0,0] neg_hi:[1,0,0]
	v_cvt_pk_bf16_f32 v34, v34, v35
	v_cndmask_b32_e64 v41, 0, 1.0, vcc
	v_cmp_eq_u32_e32 vcc, v105, v113
	s_nop 1
	v_cndmask_b32_e64 v40, 0, 1.0, vcc
	v_pk_fma_f32 v[36:37], v[246:247], v[36:37], v[40:41] op_sel_hi:[0,1,1] neg_lo:[1,0,0] neg_hi:[1,0,0]
	v_cvt_pk_bf16_f32 v35, v36, v37
	ds_write_b64 v186, v[34:35] offset:3808
	ds_read_b128 v[232:235], v1
	ds_read_b128 v[236:239], v1 offset:64
	ds_read_b128 v[240:243], v1 offset:128
	ds_read_b128 v[244:247], v1 offset:192
	s_waitcnt lgkmcnt(0)
	ds_write_b128 v184, v[232:235] offset:4096
	ds_write_b128 v184, v[236:239] offset:5120
	ds_write_b128 v184, v[240:243] offset:6144
	ds_write_b128 v184, v[244:247] offset:7168
	ds_read_b32 v232, v187 offset:192
	ds_read_b32 v234, v187 offset:200
	ds_read_b32 v236, v187 offset:208
	ds_read_b32 v238, v187 offset:216
	ds_read_b32 v240, v187 offset:224
	ds_read_b32 v242, v187 offset:232
	ds_read_b32 v244, v187 offset:240
	ds_read_b32 v246, v187 offset:248
	s_lshl_b32 s28, s24, 2
	s_mov_b32 s29, s21
	v_lshl_add_u64 v[34:35], v[126:127], 0, s[28:29]
	v_lshl_add_u64 v[36:37], v[128:129], 0, s[28:29]
	v_lshl_add_u64 v[38:39], v[134:135], 0, s[28:29]
	v_lshl_add_u64 v[40:41], v[136:137], 0, s[28:29]
	v_lshl_add_u64 v[42:43], v[138:139], 0, s[28:29]
	v_lshl_add_u64 v[44:45], v[140:141], 0, s[28:29]
	v_lshl_add_u64 v[50:51], v[142:143], 0, s[28:29]
	v_lshl_add_u64 v[52:53], v[144:145], 0, s[28:29]
	global_load_dwordx4 v[122:125], v[34:35], off nt
	global_load_dwordx4 v[114:117], v[36:37], off nt
	global_load_dwordx4 v[106:109], v[38:39], off nt
	global_load_dwordx4 v[86:89], v[40:41], off nt
	global_load_dwordx4 v[74:77], v[42:43], off nt
	s_nop 0
	global_load_dwordx4 v[42:45], v[44:45], off nt
	s_nop 0
	global_load_dwordx4 v[38:41], v[50:51], off nt
	global_load_dwordx4 v[34:37], v[52:53], off nt
	v_mov_b32_e32 v50, v188
	s_waitcnt vmcnt(23)
	s_waitcnt vmcnt(22)
	s_waitcnt vmcnt(21)
	s_waitcnt vmcnt(20)
	s_waitcnt vmcnt(19)
	s_waitcnt vmcnt(18)
	s_waitcnt vmcnt(17)
	s_waitcnt vmcnt(16)
	s_waitcnt lgkmcnt(0)
	v_pk_fma_f32 v[30:31], v[232:233], v[30:31], 0 op_sel_hi:[0,1,0] neg_lo:[1,0,0] neg_hi:[1,0,0]
	v_pk_fma_f32 v[32:33], v[232:233], v[32:33], 0 op_sel_hi:[0,1,0] neg_lo:[1,0,0] neg_hi:[1,0,0]
	v_cvt_pk_bf16_f32 v30, v30, v31
	v_cvt_pk_bf16_f32 v31, v32, v33
	ds_write_b64 v186, v[30:31]
	v_pk_fma_f32 v[26:27], v[234:235], v[26:27], 0 op_sel_hi:[0,1,0] neg_lo:[1,0,0] neg_hi:[1,0,0]
	v_pk_fma_f32 v[28:29], v[234:235], v[28:29], 0 op_sel_hi:[0,1,0] neg_lo:[1,0,0] neg_hi:[1,0,0]
	v_cvt_pk_bf16_f32 v26, v26, v27
	v_cvt_pk_bf16_f32 v27, v28, v29
	ds_write_b64 v186, v[26:27] offset:544
	v_pk_fma_f32 v[22:23], v[236:237], v[22:23], 0 op_sel_hi:[0,1,0] neg_lo:[1,0,0] neg_hi:[1,0,0]
	v_pk_fma_f32 v[24:25], v[236:237], v[24:25], 0 op_sel_hi:[0,1,0] neg_lo:[1,0,0] neg_hi:[1,0,0]
	v_cvt_pk_bf16_f32 v22, v22, v23
	v_cvt_pk_bf16_f32 v23, v24, v25
	ds_write_b64 v186, v[22:23] offset:1088
	v_pk_fma_f32 v[18:19], v[238:239], v[18:19], 0 op_sel_hi:[0,1,0] neg_lo:[1,0,0] neg_hi:[1,0,0]
	v_pk_fma_f32 v[20:21], v[238:239], v[20:21], 0 op_sel_hi:[0,1,0] neg_lo:[1,0,0] neg_hi:[1,0,0]
	v_cvt_pk_bf16_f32 v18, v18, v19
	v_cvt_pk_bf16_f32 v19, v20, v21
	ds_write_b64 v186, v[18:19] offset:1632
	v_pk_fma_f32 v[14:15], v[240:241], v[14:15], 0 op_sel_hi:[0,1,0] neg_lo:[1,0,0] neg_hi:[1,0,0]
	v_pk_fma_f32 v[16:17], v[240:241], v[16:17], 0 op_sel_hi:[0,1,0] neg_lo:[1,0,0] neg_hi:[1,0,0]
	v_cvt_pk_bf16_f32 v14, v14, v15
	v_cvt_pk_bf16_f32 v15, v16, v17
	ds_write_b64 v186, v[14:15] offset:2176
	v_pk_fma_f32 v[10:11], v[242:243], v[10:11], 0 op_sel_hi:[0,1,0] neg_lo:[1,0,0] neg_hi:[1,0,0]
	v_pk_fma_f32 v[12:13], v[242:243], v[12:13], 0 op_sel_hi:[0,1,0] neg_lo:[1,0,0] neg_hi:[1,0,0]
	v_cvt_pk_bf16_f32 v10, v10, v11
	v_cvt_pk_bf16_f32 v11, v12, v13
	ds_write_b64 v186, v[10:11] offset:2720
	v_pk_fma_f32 v[6:7], v[244:245], v[6:7], 0 op_sel_hi:[0,1,0] neg_lo:[1,0,0] neg_hi:[1,0,0]
	v_pk_fma_f32 v[8:9], v[244:245], v[8:9], 0 op_sel_hi:[0,1,0] neg_lo:[1,0,0] neg_hi:[1,0,0]
	v_cvt_pk_bf16_f32 v6, v6, v7
	v_cvt_pk_bf16_f32 v7, v8, v9
	ds_write_b64 v186, v[6:7] offset:3264
	v_pk_fma_f32 v[2:3], v[246:247], v[2:3], 0 op_sel_hi:[0,1,0] neg_lo:[1,0,0] neg_hi:[1,0,0]
	v_pk_fma_f32 v[4:5], v[246:247], v[4:5], 0 op_sel_hi:[0,1,0] neg_lo:[1,0,0] neg_hi:[1,0,0]
	v_cvt_pk_bf16_f32 v2, v2, v3
	v_cvt_pk_bf16_f32 v3, v4, v5
	ds_write_b64 v186, v[2:3] offset:3808
	ds_read_b128 v[232:235], v1
	ds_read_b128 v[236:239], v1 offset:64
	ds_read_b128 v[240:243], v1 offset:128
	ds_read_b128 v[244:247], v1 offset:192
	s_waitcnt lgkmcnt(0)
	ds_write_b128 v184, v[232:235] offset:8192
	ds_write_b128 v184, v[236:239] offset:9216
	ds_write_b128 v184, v[240:243] offset:10240
	ds_write_b128 v184, v[244:247] offset:11264
	ds_read_b32 v232, v187 offset:192
	ds_read_b32 v234, v187 offset:200
	ds_read_b32 v236, v187 offset:208
	ds_read_b32 v238, v187 offset:216
	ds_read_b32 v240, v187 offset:224
	ds_read_b32 v242, v187 offset:232
	ds_read_b32 v244, v187 offset:240
	ds_read_b32 v246, v187 offset:248
	s_lshl_b32 s26, s23, 2
	s_mov_b32 s27, s21
	v_lshl_add_u64 v[2:3], v[126:127], 0, s[26:27]
	v_lshl_add_u64 v[4:5], v[128:129], 0, s[26:27]
	v_lshl_add_u64 v[6:7], v[134:135], 0, s[26:27]
	v_lshl_add_u64 v[8:9], v[136:137], 0, s[26:27]
	v_lshl_add_u64 v[10:11], v[138:139], 0, s[26:27]
	v_lshl_add_u64 v[12:13], v[140:141], 0, s[26:27]
	v_lshl_add_u64 v[14:15], v[142:143], 0, s[26:27]
	v_lshl_add_u64 v[16:17], v[144:145], 0, s[26:27]
	global_load_dwordx4 v[118:121], v[2:3], off nt
	global_load_dwordx4 v[110:113], v[4:5], off nt
	global_load_dwordx4 v[102:105], v[6:7], off nt
	global_load_dwordx4 v[98:101], v[8:9], off nt
	global_load_dwordx4 v[58:61], v[10:11], off nt
	global_load_dwordx4 v[50:53], v[12:13], off nt
	global_load_dwordx4 v[30:33], v[14:15], off nt
	global_load_dwordx4 v[22:25], v[16:17], off nt
	v_mov_b32_e32 v2, v198
	s_waitcnt vmcnt(23)
	s_waitcnt vmcnt(22)
	s_waitcnt vmcnt(21)
	s_waitcnt vmcnt(20)
	s_waitcnt vmcnt(19)
	s_waitcnt vmcnt(18)
	s_waitcnt vmcnt(17)
	s_waitcnt vmcnt(16)
	s_waitcnt lgkmcnt(0)
	v_pk_fma_f32 v[4:5], v[232:233], v[90:91], 0 op_sel_hi:[0,1,0] neg_lo:[1,0,0] neg_hi:[1,0,0]
	v_pk_fma_f32 v[2:3], v[232:233], v[92:93], 0 op_sel_hi:[0,1,0] neg_lo:[1,0,0] neg_hi:[1,0,0]
	v_cvt_pk_bf16_f32 v4, v4, v5
	v_cvt_pk_bf16_f32 v5, v2, v3
	ds_write_b64 v186, v[4:5]
	v_pk_fma_f32 v[4:5], v[234:235], v[82:83], 0 op_sel_hi:[0,1,0] neg_lo:[1,0,0] neg_hi:[1,0,0]
	v_pk_fma_f32 v[2:3], v[234:235], v[84:85], 0 op_sel_hi:[0,1,0] neg_lo:[1,0,0] neg_hi:[1,0,0]
	v_cvt_pk_bf16_f32 v4, v4, v5
	v_cvt_pk_bf16_f32 v5, v2, v3
	ds_write_b64 v186, v[4:5] offset:544
	v_pk_fma_f32 v[4:5], v[236:237], v[78:79], 0 op_sel_hi:[0,1,0] neg_lo:[1,0,0] neg_hi:[1,0,0]
	v_pk_fma_f32 v[2:3], v[236:237], v[80:81], 0 op_sel_hi:[0,1,0] neg_lo:[1,0,0] neg_hi:[1,0,0]
	v_cvt_pk_bf16_f32 v4, v4, v5
	v_cvt_pk_bf16_f32 v5, v2, v3
	ds_write_b64 v186, v[4:5] offset:1088
	v_pk_fma_f32 v[4:5], v[238:239], v[70:71], 0 op_sel_hi:[0,1,0] neg_lo:[1,0,0] neg_hi:[1,0,0]
	v_pk_fma_f32 v[2:3], v[238:239], v[72:73], 0 op_sel_hi:[0,1,0] neg_lo:[1,0,0] neg_hi:[1,0,0]
	v_cvt_pk_bf16_f32 v4, v4, v5
	v_cvt_pk_bf16_f32 v5, v2, v3
	ds_write_b64 v186, v[4:5] offset:1632
	v_pk_fma_f32 v[4:5], v[240:241], v[66:67], 0 op_sel_hi:[0,1,0] neg_lo:[1,0,0] neg_hi:[1,0,0]
	v_pk_fma_f32 v[2:3], v[240:241], v[68:69], 0 op_sel_hi:[0,1,0] neg_lo:[1,0,0] neg_hi:[1,0,0]
	v_cvt_pk_bf16_f32 v4, v4, v5
	v_cvt_pk_bf16_f32 v5, v2, v3
	ds_write_b64 v186, v[4:5] offset:2176
	v_pk_fma_f32 v[4:5], v[242:243], v[62:63], 0 op_sel_hi:[0,1,0] neg_lo:[1,0,0] neg_hi:[1,0,0]
	v_pk_fma_f32 v[2:3], v[242:243], v[64:65], 0 op_sel_hi:[0,1,0] neg_lo:[1,0,0] neg_hi:[1,0,0]
	v_cvt_pk_bf16_f32 v4, v4, v5
	v_cvt_pk_bf16_f32 v5, v2, v3
	ds_write_b64 v186, v[4:5] offset:2720
	v_pk_fma_f32 v[4:5], v[244:245], v[54:55], 0 op_sel_hi:[0,1,0] neg_lo:[1,0,0] neg_hi:[1,0,0]
	v_pk_fma_f32 v[2:3], v[244:245], v[56:57], 0 op_sel_hi:[0,1,0] neg_lo:[1,0,0] neg_hi:[1,0,0]
	v_cvt_pk_bf16_f32 v4, v4, v5
	v_cvt_pk_bf16_f32 v5, v2, v3
	ds_write_b64 v186, v[4:5] offset:3264
	v_pk_fma_f32 v[4:5], v[246:247], v[46:47], 0 op_sel_hi:[0,1,0] neg_lo:[1,0,0] neg_hi:[1,0,0]
	v_pk_fma_f32 v[2:3], v[246:247], v[48:49], 0 op_sel_hi:[0,1,0] neg_lo:[1,0,0] neg_hi:[1,0,0]
	v_cvt_pk_bf16_f32 v4, v4, v5
	v_cvt_pk_bf16_f32 v5, v2, v3
	ds_write_b64 v186, v[4:5] offset:3808
	ds_read_b128 v[232:235], v1
	ds_read_b128 v[236:239], v1 offset:64
	ds_read_b128 v[240:243], v1 offset:128
	ds_read_b128 v[244:247], v1 offset:192
	s_waitcnt lgkmcnt(0)
	ds_write_b128 v184, v[232:235] offset:12288
	ds_write_b128 v184, v[236:239] offset:13312
	ds_write_b128 v184, v[240:243] offset:14336
	ds_write_b128 v184, v[244:247] offset:15360
	ds_read_b32 v232, v187 offset:192
	ds_read_b32 v234, v187 offset:200
	ds_read_b32 v236, v187 offset:208
	ds_read_b32 v238, v187 offset:216
	ds_read_b32 v240, v187 offset:224
	ds_read_b32 v242, v187 offset:232
	ds_read_b32 v244, v187 offset:240
	ds_read_b32 v246, v187 offset:248
	s_lshl_b32 s24, s22, 2
	s_mov_b32 s25, s21
	v_lshl_add_u64 v[2:3], v[126:127], 0, s[24:25]
	v_lshl_add_u64 v[6:7], v[134:135], 0, s[24:25]
	v_lshl_add_u64 v[8:9], v[136:137], 0, s[24:25]
	v_lshl_add_u64 v[14:15], v[142:143], 0, s[24:25]
	v_lshl_add_u64 v[4:5], v[128:129], 0, s[24:25]
	v_lshl_add_u64 v[10:11], v[138:139], 0, s[24:25]
	v_lshl_add_u64 v[12:13], v[140:141], 0, s[24:25]
	v_lshl_add_u64 v[18:19], v[144:145], 0, s[24:25]
	global_load_dwordx4 v[94:97], v[2:3], off nt
	global_load_dwordx4 v[90:93], v[4:5], off nt
	global_load_dwordx4 v[82:85], v[6:7], off nt
	global_load_dwordx4 v[70:73], v[8:9], off nt
	global_load_dwordx4 v[54:57], v[10:11], off nt
	global_load_dwordx4 v[26:29], v[12:13], off nt
	s_nop 0
	global_load_dwordx4 v[14:17], v[14:15], off nt
	s_nop 0
	global_load_dwordx4 v[6:9], v[18:19], off nt
	v_mov_b32_e32 v2, v197
	s_waitcnt vmcnt(23)
	s_waitcnt vmcnt(22)
	s_waitcnt vmcnt(21)
	s_waitcnt vmcnt(20)
	s_waitcnt vmcnt(19)
	s_waitcnt vmcnt(18)
	s_waitcnt vmcnt(17)
	s_waitcnt vmcnt(16)
	s_waitcnt lgkmcnt(0)
	v_pk_fma_f32 v[4:5], v[232:233], v[122:123], 0 op_sel_hi:[0,1,0] neg_lo:[1,0,0] neg_hi:[1,0,0]
	v_pk_fma_f32 v[2:3], v[232:233], v[124:125], 0 op_sel_hi:[0,1,0] neg_lo:[1,0,0] neg_hi:[1,0,0]
	v_cvt_pk_bf16_f32 v4, v4, v5
	v_cvt_pk_bf16_f32 v5, v2, v3
	ds_write_b64 v186, v[4:5]
	v_pk_fma_f32 v[4:5], v[234:235], v[114:115], 0 op_sel_hi:[0,1,0] neg_lo:[1,0,0] neg_hi:[1,0,0]
	v_pk_fma_f32 v[2:3], v[234:235], v[116:117], 0 op_sel_hi:[0,1,0] neg_lo:[1,0,0] neg_hi:[1,0,0]
	v_cvt_pk_bf16_f32 v4, v4, v5
	v_cvt_pk_bf16_f32 v5, v2, v3
	ds_write_b64 v186, v[4:5] offset:544
	v_pk_fma_f32 v[4:5], v[236:237], v[106:107], 0 op_sel_hi:[0,1,0] neg_lo:[1,0,0] neg_hi:[1,0,0]
	v_pk_fma_f32 v[2:3], v[236:237], v[108:109], 0 op_sel_hi:[0,1,0] neg_lo:[1,0,0] neg_hi:[1,0,0]
	v_cvt_pk_bf16_f32 v4, v4, v5
	v_cvt_pk_bf16_f32 v5, v2, v3
	ds_write_b64 v186, v[4:5] offset:1088
	v_pk_fma_f32 v[4:5], v[238:239], v[86:87], 0 op_sel_hi:[0,1,0] neg_lo:[1,0,0] neg_hi:[1,0,0]
	v_pk_fma_f32 v[2:3], v[238:239], v[88:89], 0 op_sel_hi:[0,1,0] neg_lo:[1,0,0] neg_hi:[1,0,0]
	v_cvt_pk_bf16_f32 v4, v4, v5
	v_cvt_pk_bf16_f32 v5, v2, v3
	ds_write_b64 v186, v[4:5] offset:1632
	v_pk_fma_f32 v[4:5], v[240:241], v[74:75], 0 op_sel_hi:[0,1,0] neg_lo:[1,0,0] neg_hi:[1,0,0]
	v_pk_fma_f32 v[2:3], v[240:241], v[76:77], 0 op_sel_hi:[0,1,0] neg_lo:[1,0,0] neg_hi:[1,0,0]
	v_cvt_pk_bf16_f32 v4, v4, v5
	v_cvt_pk_bf16_f32 v5, v2, v3
	ds_write_b64 v186, v[4:5] offset:2176
	v_pk_fma_f32 v[4:5], v[242:243], v[42:43], 0 op_sel_hi:[0,1,0] neg_lo:[1,0,0] neg_hi:[1,0,0]
	v_pk_fma_f32 v[2:3], v[242:243], v[44:45], 0 op_sel_hi:[0,1,0] neg_lo:[1,0,0] neg_hi:[1,0,0]
	v_cvt_pk_bf16_f32 v4, v4, v5
	v_cvt_pk_bf16_f32 v5, v2, v3
	ds_write_b64 v186, v[4:5] offset:2720
	v_pk_fma_f32 v[4:5], v[244:245], v[38:39], 0 op_sel_hi:[0,1,0] neg_lo:[1,0,0] neg_hi:[1,0,0]
	v_pk_fma_f32 v[2:3], v[244:245], v[40:41], 0 op_sel_hi:[0,1,0] neg_lo:[1,0,0] neg_hi:[1,0,0]
	v_cvt_pk_bf16_f32 v4, v4, v5
	v_cvt_pk_bf16_f32 v5, v2, v3
	ds_write_b64 v186, v[4:5] offset:3264
	v_pk_fma_f32 v[4:5], v[246:247], v[34:35], 0 op_sel_hi:[0,1,0] neg_lo:[1,0,0] neg_hi:[1,0,0]
	v_pk_fma_f32 v[2:3], v[246:247], v[36:37], 0 op_sel_hi:[0,1,0] neg_lo:[1,0,0] neg_hi:[1,0,0]
	v_cvt_pk_bf16_f32 v4, v4, v5
	v_cvt_pk_bf16_f32 v5, v2, v3
	ds_write_b64 v186, v[4:5] offset:3808
	ds_read_b128 v[232:235], v1
	ds_read_b128 v[236:239], v1 offset:64
	ds_read_b128 v[240:243], v1 offset:128
	ds_read_b128 v[244:247], v1 offset:192
	s_waitcnt lgkmcnt(0)
	ds_write_b128 v184, v[232:235] offset:16384
	ds_write_b128 v184, v[236:239] offset:17408
	ds_write_b128 v184, v[240:243] offset:18432
	ds_write_b128 v184, v[244:247] offset:19456
	ds_read_b32 v232, v187 offset:192
	ds_read_b32 v234, v187 offset:200
	ds_read_b32 v236, v187 offset:208
	ds_read_b32 v238, v187 offset:216
	ds_read_b32 v240, v187 offset:224
	ds_read_b32 v242, v187 offset:232
	ds_read_b32 v244, v187 offset:240
	ds_read_b32 v246, v187 offset:248
	s_lshl_b32 s22, s7, 2
	s_mov_b32 s23, s21
	v_lshl_add_u64 v[2:3], v[126:127], 0, s[22:23]
	v_lshl_add_u64 v[4:5], v[128:129], 0, s[22:23]
	v_lshl_add_u64 v[10:11], v[134:135], 0, s[22:23]
	v_lshl_add_u64 v[12:13], v[136:137], 0, s[22:23]
	v_lshl_add_u64 v[34:35], v[138:139], 0, s[22:23]
	v_lshl_add_u64 v[36:37], v[140:141], 0, s[22:23]
	v_lshl_add_u64 v[46:47], v[142:143], 0, s[22:23]
	v_lshl_add_u64 v[48:49], v[144:145], 0, s[22:23]
	global_load_dwordx4 v[86:89], v[2:3], off nt
	global_load_dwordx4 v[78:81], v[4:5], off nt
	global_load_dwordx4 v[66:69], v[10:11], off nt
	global_load_dwordx4 v[42:45], v[12:13], off nt
	global_load_dwordx4 v[38:41], v[34:35], off nt
	global_load_dwordx4 v[18:21], v[36:37], off nt
	s_nop 0
	global_load_dwordx4 v[10:13], v[46:47], off nt
	global_load_dwordx4 v[2:5], v[48:49], off nt
	v_mov_b32_e32 v34, v196
	s_waitcnt vmcnt(23)
	s_waitcnt vmcnt(22)
	s_waitcnt vmcnt(21)
	s_waitcnt vmcnt(20)
	s_waitcnt vmcnt(19)
	s_waitcnt vmcnt(18)
	s_waitcnt vmcnt(17)
	s_waitcnt vmcnt(16)
	s_waitcnt lgkmcnt(0)
	v_pk_fma_f32 v[36:37], v[232:233], v[118:119], 0 op_sel_hi:[0,1,0] neg_lo:[1,0,0] neg_hi:[1,0,0]
	v_pk_fma_f32 v[34:35], v[232:233], v[120:121], 0 op_sel_hi:[0,1,0] neg_lo:[1,0,0] neg_hi:[1,0,0]
	v_cvt_pk_bf16_f32 v36, v36, v37
	v_cvt_pk_bf16_f32 v37, v34, v35
	ds_write_b64 v186, v[36:37]
	v_pk_fma_f32 v[36:37], v[234:235], v[110:111], 0 op_sel_hi:[0,1,0] neg_lo:[1,0,0] neg_hi:[1,0,0]
	v_pk_fma_f32 v[34:35], v[234:235], v[112:113], 0 op_sel_hi:[0,1,0] neg_lo:[1,0,0] neg_hi:[1,0,0]
	v_cvt_pk_bf16_f32 v36, v36, v37
	v_cvt_pk_bf16_f32 v37, v34, v35
	ds_write_b64 v186, v[36:37] offset:544
	v_pk_fma_f32 v[36:37], v[236:237], v[102:103], 0 op_sel_hi:[0,1,0] neg_lo:[1,0,0] neg_hi:[1,0,0]
	v_pk_fma_f32 v[34:35], v[236:237], v[104:105], 0 op_sel_hi:[0,1,0] neg_lo:[1,0,0] neg_hi:[1,0,0]
	v_cvt_pk_bf16_f32 v36, v36, v37
	v_cvt_pk_bf16_f32 v37, v34, v35
	ds_write_b64 v186, v[36:37] offset:1088
	v_pk_fma_f32 v[36:37], v[238:239], v[98:99], 0 op_sel_hi:[0,1,0] neg_lo:[1,0,0] neg_hi:[1,0,0]
	v_pk_fma_f32 v[34:35], v[238:239], v[100:101], 0 op_sel_hi:[0,1,0] neg_lo:[1,0,0] neg_hi:[1,0,0]
	v_cvt_pk_bf16_f32 v36, v36, v37
	v_cvt_pk_bf16_f32 v37, v34, v35
	ds_write_b64 v186, v[36:37] offset:1632
	v_pk_fma_f32 v[36:37], v[240:241], v[58:59], 0 op_sel_hi:[0,1,0] neg_lo:[1,0,0] neg_hi:[1,0,0]
	v_pk_fma_f32 v[34:35], v[240:241], v[60:61], 0 op_sel_hi:[0,1,0] neg_lo:[1,0,0] neg_hi:[1,0,0]
	v_cvt_pk_bf16_f32 v36, v36, v37
	v_cvt_pk_bf16_f32 v37, v34, v35
	ds_write_b64 v186, v[36:37] offset:2176
	v_pk_fma_f32 v[36:37], v[242:243], v[50:51], 0 op_sel_hi:[0,1,0] neg_lo:[1,0,0] neg_hi:[1,0,0]
	v_pk_fma_f32 v[34:35], v[242:243], v[52:53], 0 op_sel_hi:[0,1,0] neg_lo:[1,0,0] neg_hi:[1,0,0]
	v_cvt_pk_bf16_f32 v36, v36, v37
	v_cvt_pk_bf16_f32 v37, v34, v35
	ds_write_b64 v186, v[36:37] offset:2720
	v_pk_fma_f32 v[30:31], v[244:245], v[30:31], 0 op_sel_hi:[0,1,0] neg_lo:[1,0,0] neg_hi:[1,0,0]
	v_pk_fma_f32 v[32:33], v[244:245], v[32:33], 0 op_sel_hi:[0,1,0] neg_lo:[1,0,0] neg_hi:[1,0,0]
	v_cvt_pk_bf16_f32 v30, v30, v31
	v_cvt_pk_bf16_f32 v31, v32, v33
	ds_write_b64 v186, v[30:31] offset:3264
	v_pk_fma_f32 v[22:23], v[246:247], v[22:23], 0 op_sel_hi:[0,1,0] neg_lo:[1,0,0] neg_hi:[1,0,0]
	v_pk_fma_f32 v[24:25], v[246:247], v[24:25], 0 op_sel_hi:[0,1,0] neg_lo:[1,0,0] neg_hi:[1,0,0]
	v_cvt_pk_bf16_f32 v22, v22, v23
	v_cvt_pk_bf16_f32 v23, v24, v25
	ds_write_b64 v186, v[22:23] offset:3808
	ds_read_b128 v[232:235], v1
	ds_read_b128 v[236:239], v1 offset:64
	ds_read_b128 v[240:243], v1 offset:128
	ds_read_b128 v[244:247], v1 offset:192
	s_waitcnt lgkmcnt(0)
	ds_write_b128 v184, v[232:235] offset:20480
	ds_write_b128 v184, v[236:239] offset:21504
	ds_write_b128 v184, v[240:243] offset:22528
	ds_write_b128 v184, v[244:247] offset:23552
	ds_read_b32 v232, v187 offset:192
	ds_read_b32 v234, v187 offset:200
	ds_read_b32 v236, v187 offset:208
	ds_read_b32 v238, v187 offset:216
	ds_read_b32 v240, v187 offset:224
	ds_read_b32 v242, v187 offset:232
	ds_read_b32 v244, v187 offset:240
	ds_read_b32 v246, v187 offset:248
	v_lshl_add_u64 v[22:23], v[130:131], 0, s[30:31]
	s_movk_i32 s7, 0x2000
	v_add_co_u32_e32 v24, vcc, s7, v22
	s_movk_i32 s36, 0x4000
	s_nop 0
	v_addc_co_u32_e32 v25, vcc, 0, v23, vcc
	global_load_dwordx4 v[74:77], v[22:23], off nt
	global_load_dwordx4 v[62:65], v[24:25], off nt
	v_add_co_u32_e32 v24, vcc, s36, v22
	s_movk_i32 s37, 0x6000
	s_nop 0
	v_addc_co_u32_e32 v25, vcc, 0, v23, vcc
	v_add_co_u32_e32 v30, vcc, s37, v22
	s_mov_b32 s38, 0x8000
	s_nop 0
	v_addc_co_u32_e32 v31, vcc, 0, v23, vcc
	global_load_dwordx4 v[58:61], v[24:25], off nt
	global_load_dwordx4 v[46:49], v[30:31], off nt
	v_add_co_u32_e32 v24, vcc, s38, v22
	s_mov_b32 s39, 0xa000
	s_nop 0
	v_addc_co_u32_e32 v25, vcc, 0, v23, vcc
	v_add_co_u32_e32 v34, vcc, s39, v22
	s_mov_b32 s41, 0xc000
	s_nop 0
	v_addc_co_u32_e32 v35, vcc, 0, v23, vcc
	global_load_dwordx4 v[50:53], v[24:25], off nt
	global_load_dwordx4 v[30:33], v[34:35], off nt
	v_add_co_u32_e32 v24, vcc, s41, v22
	s_mov_b32 s42, 0xe000
	s_nop 0
	v_addc_co_u32_e32 v25, vcc, 0, v23, vcc
	v_add_co_u32_e32 v22, vcc, s42, v22
	s_nop 1
	v_addc_co_u32_e32 v23, vcc, 0, v23, vcc
	global_load_dwordx4 v[34:37], v[24:25], off nt
	s_nop 0
	global_load_dwordx4 v[22:25], v[22:23], off nt
	v_mov_b32_e32 v98, v195
	s_waitcnt vmcnt(23)
	s_waitcnt vmcnt(22)
	s_waitcnt vmcnt(21)
	s_waitcnt vmcnt(20)
	s_waitcnt vmcnt(19)
	s_waitcnt vmcnt(18)
	s_waitcnt vmcnt(17)
	s_waitcnt vmcnt(16)
	s_waitcnt lgkmcnt(0)
	v_pk_fma_f32 v[94:95], v[232:233], v[94:95], 0 op_sel_hi:[0,1,0] neg_lo:[1,0,0] neg_hi:[1,0,0]
	v_pk_fma_f32 v[96:97], v[232:233], v[96:97], 0 op_sel_hi:[0,1,0] neg_lo:[1,0,0] neg_hi:[1,0,0]
	v_cvt_pk_bf16_f32 v94, v94, v95
	v_cvt_pk_bf16_f32 v95, v96, v97
	ds_write_b64 v186, v[94:95]
	v_pk_fma_f32 v[90:91], v[234:235], v[90:91], 0 op_sel_hi:[0,1,0] neg_lo:[1,0,0] neg_hi:[1,0,0]
	v_pk_fma_f32 v[92:93], v[234:235], v[92:93], 0 op_sel_hi:[0,1,0] neg_lo:[1,0,0] neg_hi:[1,0,0]
	v_cvt_pk_bf16_f32 v90, v90, v91
	v_cvt_pk_bf16_f32 v91, v92, v93
	ds_write_b64 v186, v[90:91] offset:544
	v_pk_fma_f32 v[82:83], v[236:237], v[82:83], 0 op_sel_hi:[0,1,0] neg_lo:[1,0,0] neg_hi:[1,0,0]
	v_pk_fma_f32 v[84:85], v[236:237], v[84:85], 0 op_sel_hi:[0,1,0] neg_lo:[1,0,0] neg_hi:[1,0,0]
	v_cvt_pk_bf16_f32 v82, v82, v83
	v_cvt_pk_bf16_f32 v83, v84, v85
	ds_write_b64 v186, v[82:83] offset:1088
	v_pk_fma_f32 v[70:71], v[238:239], v[70:71], 0 op_sel_hi:[0,1,0] neg_lo:[1,0,0] neg_hi:[1,0,0]
	v_pk_fma_f32 v[72:73], v[238:239], v[72:73], 0 op_sel_hi:[0,1,0] neg_lo:[1,0,0] neg_hi:[1,0,0]
	v_cvt_pk_bf16_f32 v70, v70, v71
	v_cvt_pk_bf16_f32 v71, v72, v73
	ds_write_b64 v186, v[70:71] offset:1632
	v_pk_fma_f32 v[54:55], v[240:241], v[54:55], 0 op_sel_hi:[0,1,0] neg_lo:[1,0,0] neg_hi:[1,0,0]
	v_pk_fma_f32 v[56:57], v[240:241], v[56:57], 0 op_sel_hi:[0,1,0] neg_lo:[1,0,0] neg_hi:[1,0,0]
	v_cvt_pk_bf16_f32 v54, v54, v55
	v_cvt_pk_bf16_f32 v55, v56, v57
	ds_write_b64 v186, v[54:55] offset:2176
	v_pk_fma_f32 v[26:27], v[242:243], v[26:27], 0 op_sel_hi:[0,1,0] neg_lo:[1,0,0] neg_hi:[1,0,0]
	v_pk_fma_f32 v[28:29], v[242:243], v[28:29], 0 op_sel_hi:[0,1,0] neg_lo:[1,0,0] neg_hi:[1,0,0]
	v_cvt_pk_bf16_f32 v26, v26, v27
	v_cvt_pk_bf16_f32 v27, v28, v29
	ds_write_b64 v186, v[26:27] offset:2720
	v_pk_fma_f32 v[14:15], v[244:245], v[14:15], 0 op_sel_hi:[0,1,0] neg_lo:[1,0,0] neg_hi:[1,0,0]
	v_pk_fma_f32 v[16:17], v[244:245], v[16:17], 0 op_sel_hi:[0,1,0] neg_lo:[1,0,0] neg_hi:[1,0,0]
	v_cvt_pk_bf16_f32 v14, v14, v15
	v_cvt_pk_bf16_f32 v15, v16, v17
	ds_write_b64 v186, v[14:15] offset:3264
	v_pk_fma_f32 v[6:7], v[246:247], v[6:7], 0 op_sel_hi:[0,1,0] neg_lo:[1,0,0] neg_hi:[1,0,0]
	v_pk_fma_f32 v[8:9], v[246:247], v[8:9], 0 op_sel_hi:[0,1,0] neg_lo:[1,0,0] neg_hi:[1,0,0]
	v_cvt_pk_bf16_f32 v6, v6, v7
	v_cvt_pk_bf16_f32 v7, v8, v9
	ds_write_b64 v186, v[6:7] offset:3808
	ds_read_b128 v[232:235], v1
	ds_read_b128 v[236:239], v1 offset:64
	ds_read_b128 v[240:243], v1 offset:128
	ds_read_b128 v[244:247], v1 offset:192
	s_waitcnt lgkmcnt(0)
	ds_write_b128 v184, v[232:235] offset:24576
	ds_write_b128 v184, v[236:239] offset:25600
	ds_write_b128 v184, v[240:243] offset:26624
	ds_write_b128 v184, v[244:247] offset:27648
	ds_read_b32 v232, v187 offset:192
	ds_read_b32 v234, v187 offset:200
	ds_read_b32 v236, v187 offset:208
	ds_read_b32 v238, v187 offset:216
	ds_read_b32 v240, v187 offset:224
	ds_read_b32 v242, v187 offset:232
	ds_read_b32 v244, v187 offset:240
	ds_read_b32 v246, v187 offset:248
	s_mov_b64 s[44:45], 0x10000
	v_lshl_add_u64 v[150:151], v[130:131], 0, s[44:45]
	s_mov_b64 s[44:45], 0x12000
	v_lshl_add_u64 v[152:153], v[130:131], 0, s[44:45]
	s_mov_b64 s[44:45], 0x14000
	v_lshl_add_u64 v[156:157], v[130:131], 0, s[44:45]
	s_mov_b64 s[44:45], 0x16000
	v_lshl_add_u64 v[158:159], v[130:131], 0, s[44:45]
	s_mov_b64 s[44:45], 0x18000
	v_lshl_add_u64 v[160:161], v[130:131], 0, s[44:45]
	s_mov_b64 s[44:45], 0x1a000
	v_lshl_add_u64 v[162:163], v[130:131], 0, s[44:45]
	s_mov_b64 s[44:45], 0x1c000
	v_lshl_add_u64 v[164:165], v[130:131], 0, s[44:45]
	s_mov_b64 s[44:45], 0x1e000
	v_lshl_add_u64 v[6:7], v[150:151], 0, s[30:31]
	v_lshl_add_u64 v[8:9], v[152:153], 0, s[30:31]
	v_lshl_add_u64 v[14:15], v[156:157], 0, s[30:31]
	v_lshl_add_u64 v[16:17], v[158:159], 0, s[30:31]
	v_lshl_add_u64 v[26:27], v[160:161], 0, s[30:31]
	v_lshl_add_u64 v[28:29], v[162:163], 0, s[30:31]
	v_lshl_add_u64 v[166:167], v[130:131], 0, s[44:45]
	v_lshl_add_u64 v[98:99], v[164:165], 0, s[30:31]
	v_lshl_add_u64 v[100:101], v[166:167], 0, s[30:31]
	global_load_dwordx4 v[94:97], v[6:7], off nt
	global_load_dwordx4 v[90:93], v[8:9], off nt
	global_load_dwordx4 v[82:85], v[14:15], off nt
	global_load_dwordx4 v[70:73], v[16:17], off nt
	global_load_dwordx4 v[54:57], v[26:27], off nt
	s_nop 0
	global_load_dwordx4 v[26:29], v[28:29], off nt
	s_nop 0
	global_load_dwordx4 v[14:17], v[98:99], off nt
	global_load_dwordx4 v[6:9], v[100:101], off nt
	v_mov_b32_e32 v98, v194
	s_waitcnt vmcnt(23)
	s_waitcnt vmcnt(22)
	s_waitcnt vmcnt(21)
	s_waitcnt vmcnt(20)
	s_waitcnt vmcnt(19)
	s_waitcnt vmcnt(18)
	s_waitcnt vmcnt(17)
	s_waitcnt vmcnt(16)
	s_waitcnt lgkmcnt(0)
	v_pk_fma_f32 v[86:87], v[232:233], v[86:87], 0 op_sel_hi:[0,1,0] neg_lo:[1,0,0] neg_hi:[1,0,0]
	v_pk_fma_f32 v[88:89], v[232:233], v[88:89], 0 op_sel_hi:[0,1,0] neg_lo:[1,0,0] neg_hi:[1,0,0]
	v_cvt_pk_bf16_f32 v86, v86, v87
	v_cvt_pk_bf16_f32 v87, v88, v89
	ds_write_b64 v186, v[86:87]
	v_pk_fma_f32 v[78:79], v[234:235], v[78:79], 0 op_sel_hi:[0,1,0] neg_lo:[1,0,0] neg_hi:[1,0,0]
	v_pk_fma_f32 v[80:81], v[234:235], v[80:81], 0 op_sel_hi:[0,1,0] neg_lo:[1,0,0] neg_hi:[1,0,0]
	v_cvt_pk_bf16_f32 v78, v78, v79
	v_cvt_pk_bf16_f32 v79, v80, v81
	ds_write_b64 v186, v[78:79] offset:544
	v_pk_fma_f32 v[66:67], v[236:237], v[66:67], 0 op_sel_hi:[0,1,0] neg_lo:[1,0,0] neg_hi:[1,0,0]
	v_pk_fma_f32 v[68:69], v[236:237], v[68:69], 0 op_sel_hi:[0,1,0] neg_lo:[1,0,0] neg_hi:[1,0,0]
	v_cvt_pk_bf16_f32 v66, v66, v67
	v_cvt_pk_bf16_f32 v67, v68, v69
	ds_write_b64 v186, v[66:67] offset:1088
	v_pk_fma_f32 v[42:43], v[238:239], v[42:43], 0 op_sel_hi:[0,1,0] neg_lo:[1,0,0] neg_hi:[1,0,0]
	v_pk_fma_f32 v[44:45], v[238:239], v[44:45], 0 op_sel_hi:[0,1,0] neg_lo:[1,0,0] neg_hi:[1,0,0]
	v_cvt_pk_bf16_f32 v42, v42, v43
	v_cvt_pk_bf16_f32 v43, v44, v45
	ds_write_b64 v186, v[42:43] offset:1632
	v_pk_fma_f32 v[38:39], v[240:241], v[38:39], 0 op_sel_hi:[0,1,0] neg_lo:[1,0,0] neg_hi:[1,0,0]
	v_pk_fma_f32 v[40:41], v[240:241], v[40:41], 0 op_sel_hi:[0,1,0] neg_lo:[1,0,0] neg_hi:[1,0,0]
	v_cvt_pk_bf16_f32 v38, v38, v39
	v_cvt_pk_bf16_f32 v39, v40, v41
	ds_write_b64 v186, v[38:39] offset:2176
	v_pk_fma_f32 v[18:19], v[242:243], v[18:19], 0 op_sel_hi:[0,1,0] neg_lo:[1,0,0] neg_hi:[1,0,0]
	v_pk_fma_f32 v[20:21], v[242:243], v[20:21], 0 op_sel_hi:[0,1,0] neg_lo:[1,0,0] neg_hi:[1,0,0]
	v_cvt_pk_bf16_f32 v18, v18, v19
	v_cvt_pk_bf16_f32 v19, v20, v21
	ds_write_b64 v186, v[18:19] offset:2720
	v_pk_fma_f32 v[10:11], v[244:245], v[10:11], 0 op_sel_hi:[0,1,0] neg_lo:[1,0,0] neg_hi:[1,0,0]
	v_pk_fma_f32 v[12:13], v[244:245], v[12:13], 0 op_sel_hi:[0,1,0] neg_lo:[1,0,0] neg_hi:[1,0,0]
	v_cvt_pk_bf16_f32 v10, v10, v11
	v_cvt_pk_bf16_f32 v11, v12, v13
	ds_write_b64 v186, v[10:11] offset:3264
	v_pk_fma_f32 v[2:3], v[246:247], v[2:3], 0 op_sel_hi:[0,1,0] neg_lo:[1,0,0] neg_hi:[1,0,0]
	v_pk_fma_f32 v[4:5], v[246:247], v[4:5], 0 op_sel_hi:[0,1,0] neg_lo:[1,0,0] neg_hi:[1,0,0]
	v_cvt_pk_bf16_f32 v2, v2, v3
	v_cvt_pk_bf16_f32 v3, v4, v5
	ds_write_b64 v186, v[2:3] offset:3808
	ds_read_b128 v[232:235], v1
	ds_read_b128 v[236:239], v1 offset:64
	ds_read_b128 v[240:243], v1 offset:128
	ds_read_b128 v[244:247], v1 offset:192
	s_waitcnt lgkmcnt(0)
	ds_write_b128 v184, v[232:235] offset:28672
	ds_write_b128 v184, v[236:239] offset:29696
	ds_write_b128 v184, v[240:243] offset:30720
	ds_write_b128 v184, v[244:247] offset:31744
	ds_read_b32 v232, v187 offset:0
	ds_read_b32 v234, v187 offset:8
	ds_read_b32 v236, v187 offset:16
	ds_read_b32 v238, v187 offset:24
	ds_read_b32 v240, v187 offset:32
	ds_read_b32 v242, v187 offset:40
	ds_read_b32 v244, v187 offset:48
	ds_read_b32 v246, v187 offset:56
	s_mov_b64 s[44:45], 0x20000
	v_lshl_add_u64 v[168:169], v[130:131], 0, s[44:45]
	s_mov_b64 s[44:45], 0x22000
	v_lshl_add_u64 v[170:171], v[130:131], 0, s[44:45]
	s_mov_b64 s[44:45], 0x24000
	v_lshl_add_u64 v[172:173], v[130:131], 0, s[44:45]
	s_mov_b64 s[44:45], 0x26000
	v_lshl_add_u64 v[174:175], v[130:131], 0, s[44:45]
	s_mov_b64 s[44:45], 0x28000
	v_lshl_add_u64 v[176:177], v[130:131], 0, s[44:45]
	s_mov_b64 s[44:45], 0x2a000
	v_lshl_add_u64 v[178:179], v[130:131], 0, s[44:45]
	s_mov_b64 s[44:45], 0x2c000
	v_lshl_add_u64 v[180:181], v[130:131], 0, s[44:45]
	s_mov_b64 s[44:45], 0x2e000
	v_lshl_add_u64 v[2:3], v[168:169], 0, s[30:31]
	v_lshl_add_u64 v[4:5], v[170:171], 0, s[30:31]
	v_lshl_add_u64 v[10:11], v[172:173], 0, s[30:31]
	v_lshl_add_u64 v[12:13], v[174:175], 0, s[30:31]
	v_lshl_add_u64 v[18:19], v[176:177], 0, s[30:31]
	v_lshl_add_u64 v[20:21], v[178:179], 0, s[30:31]
	v_lshl_add_u64 v[182:183], v[130:131], 0, s[44:45]
	v_lshl_add_u64 v[42:43], v[180:181], 0, s[30:31]
	v_lshl_add_u64 v[44:45], v[182:183], 0, s[30:31]
	global_load_dwordx4 v[106:109], v[2:3], off nt
	global_load_dwordx4 v[98:101], v[4:5], off nt
	global_load_dwordx4 v[78:81], v[10:11], off nt
	global_load_dwordx4 v[66:69], v[12:13], off nt
	global_load_dwordx4 v[38:41], v[18:19], off nt
	s_nop 0
	global_load_dwordx4 v[18:21], v[20:21], off nt
	s_nop 0
	global_load_dwordx4 v[10:13], v[42:43], off nt
	global_load_dwordx4 v[2:5], v[44:45], off nt
	v_mov_b32_e32 v42, v198
	s_waitcnt vmcnt(23)
	s_waitcnt vmcnt(22)
	s_waitcnt vmcnt(21)
	s_waitcnt vmcnt(20)
	s_waitcnt vmcnt(19)
	s_waitcnt vmcnt(18)
	s_waitcnt vmcnt(17)
	s_waitcnt vmcnt(16)
	s_waitcnt lgkmcnt(0)
	v_pk_fma_f32 v[44:45], v[232:233], v[74:75], 0 op_sel_hi:[0,1,0] neg_lo:[1,0,0] neg_hi:[1,0,0]
	v_pk_fma_f32 v[42:43], v[232:233], v[76:77], 0 op_sel_hi:[0,1,0] neg_lo:[1,0,0] neg_hi:[1,0,0]
	v_cvt_pk_bf16_f32 v44, v44, v45
	v_cvt_pk_bf16_f32 v45, v42, v43
	ds_write_b64 v186, v[44:45]
	v_pk_fma_f32 v[44:45], v[234:235], v[62:63], 0 op_sel_hi:[0,1,0] neg_lo:[1,0,0] neg_hi:[1,0,0]
	v_pk_fma_f32 v[42:43], v[234:235], v[64:65], 0 op_sel_hi:[0,1,0] neg_lo:[1,0,0] neg_hi:[1,0,0]
	v_cvt_pk_bf16_f32 v44, v44, v45
	v_cvt_pk_bf16_f32 v45, v42, v43
	ds_write_b64 v186, v[44:45] offset:544
	v_pk_fma_f32 v[44:45], v[236:237], v[58:59], 0 op_sel_hi:[0,1,0] neg_lo:[1,0,0] neg_hi:[1,0,0]
	v_pk_fma_f32 v[42:43], v[236:237], v[60:61], 0 op_sel_hi:[0,1,0] neg_lo:[1,0,0] neg_hi:[1,0,0]
	v_cvt_pk_bf16_f32 v44, v44, v45
	v_cvt_pk_bf16_f32 v45, v42, v43
	ds_write_b64 v186, v[44:45] offset:1088
	v_pk_fma_f32 v[44:45], v[238:239], v[46:47], 0 op_sel_hi:[0,1,0] neg_lo:[1,0,0] neg_hi:[1,0,0]
	v_pk_fma_f32 v[42:43], v[238:239], v[48:49], 0 op_sel_hi:[0,1,0] neg_lo:[1,0,0] neg_hi:[1,0,0]
	v_cvt_pk_bf16_f32 v44, v44, v45
	v_cvt_pk_bf16_f32 v45, v42, v43
	ds_write_b64 v186, v[44:45] offset:1632
	v_pk_fma_f32 v[44:45], v[240:241], v[50:51], 0 op_sel_hi:[0,1,0] neg_lo:[1,0,0] neg_hi:[1,0,0]
	v_pk_fma_f32 v[42:43], v[240:241], v[52:53], 0 op_sel_hi:[0,1,0] neg_lo:[1,0,0] neg_hi:[1,0,0]
	v_cvt_pk_bf16_f32 v44, v44, v45
	v_cvt_pk_bf16_f32 v45, v42, v43
	ds_write_b64 v186, v[44:45] offset:2176
	v_pk_fma_f32 v[30:31], v[242:243], v[30:31], 0 op_sel_hi:[0,1,0] neg_lo:[1,0,0] neg_hi:[1,0,0]
	v_pk_fma_f32 v[32:33], v[242:243], v[32:33], 0 op_sel_hi:[0,1,0] neg_lo:[1,0,0] neg_hi:[1,0,0]
	v_cvt_pk_bf16_f32 v30, v30, v31
	v_cvt_pk_bf16_f32 v31, v32, v33
	ds_write_b64 v186, v[30:31] offset:2720
	v_pk_fma_f32 v[32:33], v[244:245], v[34:35], 0 op_sel_hi:[0,1,0] neg_lo:[1,0,0] neg_hi:[1,0,0]
	v_pk_fma_f32 v[30:31], v[244:245], v[36:37], 0 op_sel_hi:[0,1,0] neg_lo:[1,0,0] neg_hi:[1,0,0]
	v_cvt_pk_bf16_f32 v32, v32, v33
	v_cvt_pk_bf16_f32 v33, v30, v31
	ds_write_b64 v186, v[32:33] offset:3264
	v_pk_fma_f32 v[22:23], v[246:247], v[22:23], 0 op_sel_hi:[0,1,0] neg_lo:[1,0,0] neg_hi:[1,0,0]
	v_pk_fma_f32 v[24:25], v[246:247], v[24:25], 0 op_sel_hi:[0,1,0] neg_lo:[1,0,0] neg_hi:[1,0,0]
	v_cvt_pk_bf16_f32 v22, v22, v23
	v_cvt_pk_bf16_f32 v23, v24, v25
	ds_write_b64 v186, v[22:23] offset:3808
	ds_read_b32 v232, v187 offset:64
	ds_read_b32 v234, v187 offset:72
	ds_read_b32 v236, v187 offset:80
	ds_read_b32 v238, v187 offset:88
	ds_read_b32 v240, v187 offset:96
	ds_read_b32 v242, v187 offset:104
	ds_read_b32 v244, v187 offset:112
	ds_read_b32 v246, v187 offset:120
	ds_read_b128 a[0:3], v1
	ds_read_b128 a[4:7], v1 offset:64
	ds_read_b128 a[8:11], v1 offset:128
	ds_read_b128 a[12:15], v1 offset:192
	v_lshl_add_u64 v[22:23], v[130:131], 0, s[28:29]
	v_add_co_u32_e32 v24, vcc, s7, v22
	s_nop 1
	v_addc_co_u32_e32 v25, vcc, 0, v23, vcc
	global_load_dwordx4 v[102:105], v[22:23], off nt
	global_load_dwordx4 v[86:89], v[24:25], off nt
	v_add_co_u32_e32 v24, vcc, s36, v22
	s_nop 1
	v_addc_co_u32_e32 v25, vcc, 0, v23, vcc
	v_add_co_u32_e32 v30, vcc, s37, v22
	s_nop 1
	v_addc_co_u32_e32 v31, vcc, 0, v23, vcc
	global_load_dwordx4 v[74:77], v[24:25], off nt
	global_load_dwordx4 v[62:65], v[30:31], off nt
	v_add_co_u32_e32 v24, vcc, s38, v22
	s_nop 1
	v_addc_co_u32_e32 v25, vcc, 0, v23, vcc
	v_add_co_u32_e32 v30, vcc, s39, v22
	s_nop 1
	v_addc_co_u32_e32 v31, vcc, 0, v23, vcc
	global_load_dwordx4 v[58:61], v[24:25], off nt
	global_load_dwordx4 v[46:49], v[30:31], off nt
	v_add_co_u32_e32 v24, vcc, s41, v22
	s_nop 1
	v_addc_co_u32_e32 v25, vcc, 0, v23, vcc
	v_add_co_u32_e32 v22, vcc, s42, v22
	s_nop 1
	v_addc_co_u32_e32 v23, vcc, 0, v23, vcc
	global_load_dwordx4 v[42:45], v[24:25], off nt
	global_load_dwordx4 v[30:33], v[22:23], off nt
	v_mov_b32_e32 v22, v198
	s_waitcnt vmcnt(23)
	s_waitcnt vmcnt(22)
	s_waitcnt vmcnt(21)
	s_waitcnt vmcnt(20)
	s_waitcnt vmcnt(19)
	s_waitcnt vmcnt(18)
	s_waitcnt vmcnt(17)
	s_waitcnt vmcnt(16)
	s_waitcnt lgkmcnt(0)
	v_pk_fma_f32 v[24:25], v[232:233], v[94:95], 0 op_sel_hi:[0,1,0] neg_lo:[1,0,0] neg_hi:[1,0,0]
	v_pk_fma_f32 v[22:23], v[232:233], v[96:97], 0 op_sel_hi:[0,1,0] neg_lo:[1,0,0] neg_hi:[1,0,0]
	v_cvt_pk_bf16_f32 v24, v24, v25
	v_cvt_pk_bf16_f32 v25, v22, v23
	ds_write_b64 v186, v[24:25]
	v_pk_fma_f32 v[24:25], v[234:235], v[90:91], 0 op_sel_hi:[0,1,0] neg_lo:[1,0,0] neg_hi:[1,0,0]
	v_pk_fma_f32 v[22:23], v[234:235], v[92:93], 0 op_sel_hi:[0,1,0] neg_lo:[1,0,0] neg_hi:[1,0,0]
	v_cvt_pk_bf16_f32 v24, v24, v25
	v_cvt_pk_bf16_f32 v25, v22, v23
	ds_write_b64 v186, v[24:25] offset:544
	v_pk_fma_f32 v[24:25], v[236:237], v[82:83], 0 op_sel_hi:[0,1,0] neg_lo:[1,0,0] neg_hi:[1,0,0]
	v_pk_fma_f32 v[22:23], v[236:237], v[84:85], 0 op_sel_hi:[0,1,0] neg_lo:[1,0,0] neg_hi:[1,0,0]
	v_cvt_pk_bf16_f32 v24, v24, v25
	v_cvt_pk_bf16_f32 v25, v22, v23
	ds_write_b64 v186, v[24:25] offset:1088
	v_pk_fma_f32 v[24:25], v[238:239], v[70:71], 0 op_sel_hi:[0,1,0] neg_lo:[1,0,0] neg_hi:[1,0,0]
	v_pk_fma_f32 v[22:23], v[238:239], v[72:73], 0 op_sel_hi:[0,1,0] neg_lo:[1,0,0] neg_hi:[1,0,0]
	v_cvt_pk_bf16_f32 v24, v24, v25
	v_cvt_pk_bf16_f32 v25, v22, v23
	ds_write_b64 v186, v[24:25] offset:1632
	v_pk_fma_f32 v[24:25], v[240:241], v[54:55], 0 op_sel_hi:[0,1,0] neg_lo:[1,0,0] neg_hi:[1,0,0]
	v_pk_fma_f32 v[22:23], v[240:241], v[56:57], 0 op_sel_hi:[0,1,0] neg_lo:[1,0,0] neg_hi:[1,0,0]
	v_cvt_pk_bf16_f32 v24, v24, v25
	v_cvt_pk_bf16_f32 v25, v22, v23
	ds_write_b64 v186, v[24:25] offset:2176
	v_pk_fma_f32 v[24:25], v[242:243], v[26:27], 0 op_sel_hi:[0,1,0] neg_lo:[1,0,0] neg_hi:[1,0,0]
	v_pk_fma_f32 v[22:23], v[242:243], v[28:29], 0 op_sel_hi:[0,1,0] neg_lo:[1,0,0] neg_hi:[1,0,0]
	v_cvt_pk_bf16_f32 v24, v24, v25
	v_cvt_pk_bf16_f32 v25, v22, v23
	ds_write_b64 v186, v[24:25] offset:2720
	v_pk_fma_f32 v[14:15], v[244:245], v[14:15], 0 op_sel_hi:[0,1,0] neg_lo:[1,0,0] neg_hi:[1,0,0]
	v_pk_fma_f32 v[16:17], v[244:245], v[16:17], 0 op_sel_hi:[0,1,0] neg_lo:[1,0,0] neg_hi:[1,0,0]
	v_cvt_pk_bf16_f32 v14, v14, v15
	v_cvt_pk_bf16_f32 v15, v16, v17
	ds_write_b64 v186, v[14:15] offset:3264
	v_pk_fma_f32 v[6:7], v[246:247], v[6:7], 0 op_sel_hi:[0,1,0] neg_lo:[1,0,0] neg_hi:[1,0,0]
	v_pk_fma_f32 v[8:9], v[246:247], v[8:9], 0 op_sel_hi:[0,1,0] neg_lo:[1,0,0] neg_hi:[1,0,0]
	v_cvt_pk_bf16_f32 v6, v6, v7
	v_cvt_pk_bf16_f32 v7, v8, v9
	ds_write_b64 v186, v[6:7] offset:3808
	ds_read_b32 v232, v187 offset:128
	ds_read_b32 v234, v187 offset:136
	ds_read_b32 v236, v187 offset:144
	ds_read_b32 v238, v187 offset:152
	ds_read_b32 v240, v187 offset:160
	ds_read_b32 v242, v187 offset:168
	ds_read_b32 v244, v187 offset:176
	ds_read_b32 v246, v187 offset:184
	ds_read_b128 a[16:19], v1
	ds_read_b128 a[20:23], v1 offset:64
	ds_read_b128 a[24:27], v1 offset:128
	ds_read_b128 a[28:31], v1 offset:192
	v_lshl_add_u64 v[6:7], v[150:151], 0, s[28:29]
	v_lshl_add_u64 v[8:9], v[152:153], 0, s[28:29]
	v_lshl_add_u64 v[14:15], v[156:157], 0, s[28:29]
	v_lshl_add_u64 v[16:17], v[158:159], 0, s[28:29]
	v_lshl_add_u64 v[22:23], v[160:161], 0, s[28:29]
	v_lshl_add_u64 v[24:25], v[162:163], 0, s[28:29]
	v_lshl_add_u64 v[26:27], v[164:165], 0, s[28:29]
	v_lshl_add_u64 v[28:29], v[166:167], 0, s[28:29]
	global_load_dwordx4 v[110:113], v[6:7], off nt
	global_load_dwordx4 v[90:93], v[8:9], off nt
	global_load_dwordx4 v[70:73], v[14:15], off nt
	global_load_dwordx4 v[50:53], v[16:17], off nt
	global_load_dwordx4 v[34:37], v[22:23], off nt
	s_nop 0
	global_load_dwordx4 v[22:25], v[24:25], off nt
	s_nop 0
	global_load_dwordx4 v[14:17], v[26:27], off nt
	global_load_dwordx4 v[6:9], v[28:29], off nt
	s_waitcnt vmcnt(23)
	s_waitcnt vmcnt(22)
	s_waitcnt vmcnt(21)
	s_waitcnt vmcnt(20)
	s_waitcnt vmcnt(19)
	s_waitcnt vmcnt(18)
	s_waitcnt vmcnt(17)
	s_waitcnt vmcnt(16)
	s_waitcnt lgkmcnt(0)
	v_pk_fma_f32 v[28:29], v[232:233], v[106:107], 0 op_sel_hi:[0,1,0] neg_lo:[1,0,0] neg_hi:[1,0,0]
	v_pk_fma_f32 v[26:27], v[232:233], v[108:109], 0 op_sel_hi:[0,1,0] neg_lo:[1,0,0] neg_hi:[1,0,0]
	v_cvt_pk_bf16_f32 v28, v28, v29
	v_cvt_pk_bf16_f32 v29, v26, v27
	ds_write_b64 v186, v[28:29]
	v_pk_fma_f32 v[28:29], v[234:235], v[98:99], 0 op_sel_hi:[0,1,0] neg_lo:[1,0,0] neg_hi:[1,0,0]
	v_pk_fma_f32 v[26:27], v[234:235], v[100:101], 0 op_sel_hi:[0,1,0] neg_lo:[1,0,0] neg_hi:[1,0,0]
	v_cvt_pk_bf16_f32 v28, v28, v29
	v_cvt_pk_bf16_f32 v29, v26, v27
	ds_write_b64 v186, v[28:29] offset:544
	v_pk_fma_f32 v[28:29], v[236:237], v[78:79], 0 op_sel_hi:[0,1,0] neg_lo:[1,0,0] neg_hi:[1,0,0]
	v_pk_fma_f32 v[26:27], v[236:237], v[80:81], 0 op_sel_hi:[0,1,0] neg_lo:[1,0,0] neg_hi:[1,0,0]
	v_cvt_pk_bf16_f32 v28, v28, v29
	v_cvt_pk_bf16_f32 v29, v26, v27
	ds_write_b64 v186, v[28:29] offset:1088
	v_pk_fma_f32 v[28:29], v[238:239], v[66:67], 0 op_sel_hi:[0,1,0] neg_lo:[1,0,0] neg_hi:[1,0,0]
	v_pk_fma_f32 v[26:27], v[238:239], v[68:69], 0 op_sel_hi:[0,1,0] neg_lo:[1,0,0] neg_hi:[1,0,0]
	v_cvt_pk_bf16_f32 v28, v28, v29
	v_cvt_pk_bf16_f32 v29, v26, v27
	ds_write_b64 v186, v[28:29] offset:1632
	v_pk_fma_f32 v[28:29], v[240:241], v[38:39], 0 op_sel_hi:[0,1,0] neg_lo:[1,0,0] neg_hi:[1,0,0]
	v_pk_fma_f32 v[26:27], v[240:241], v[40:41], 0 op_sel_hi:[0,1,0] neg_lo:[1,0,0] neg_hi:[1,0,0]
	v_cvt_pk_bf16_f32 v28, v28, v29
	v_cvt_pk_bf16_f32 v29, v26, v27
	ds_write_b64 v186, v[28:29] offset:2176
	v_pk_fma_f32 v[18:19], v[242:243], v[18:19], 0 op_sel_hi:[0,1,0] neg_lo:[1,0,0] neg_hi:[1,0,0]
	v_pk_fma_f32 v[20:21], v[242:243], v[20:21], 0 op_sel_hi:[0,1,0] neg_lo:[1,0,0] neg_hi:[1,0,0]
	v_cvt_pk_bf16_f32 v18, v18, v19
	v_cvt_pk_bf16_f32 v19, v20, v21
	ds_write_b64 v186, v[18:19] offset:2720
	v_pk_fma_f32 v[10:11], v[244:245], v[10:11], 0 op_sel_hi:[0,1,0] neg_lo:[1,0,0] neg_hi:[1,0,0]
	v_pk_fma_f32 v[12:13], v[244:245], v[12:13], 0 op_sel_hi:[0,1,0] neg_lo:[1,0,0] neg_hi:[1,0,0]
	v_cvt_pk_bf16_f32 v10, v10, v11
	v_cvt_pk_bf16_f32 v11, v12, v13
	ds_write_b64 v186, v[10:11] offset:3264
	v_pk_fma_f32 v[2:3], v[246:247], v[2:3], 0 op_sel_hi:[0,1,0] neg_lo:[1,0,0] neg_hi:[1,0,0]
	v_pk_fma_f32 v[4:5], v[246:247], v[4:5], 0 op_sel_hi:[0,1,0] neg_lo:[1,0,0] neg_hi:[1,0,0]
	v_cvt_pk_bf16_f32 v2, v2, v3
	v_cvt_pk_bf16_f32 v3, v4, v5
	ds_write_b64 v186, v[2:3] offset:3808
	ds_read_b32 v232, v187 offset:0
	ds_read_b32 v234, v187 offset:8
	ds_read_b32 v236, v187 offset:16
	ds_read_b32 v238, v187 offset:24
	ds_read_b32 v240, v187 offset:32
	ds_read_b32 v242, v187 offset:40
	ds_read_b32 v244, v187 offset:48
	ds_read_b32 v246, v187 offset:56
	ds_read_b128 a[32:35], v1
	ds_read_b128 a[36:39], v1 offset:64
	ds_read_b128 a[40:43], v1 offset:128
	ds_read_b128 a[44:47], v1 offset:192
	v_lshl_add_u64 v[2:3], v[168:169], 0, s[28:29]
	v_lshl_add_u64 v[4:5], v[170:171], 0, s[28:29]
	v_lshl_add_u64 v[10:11], v[172:173], 0, s[28:29]
	v_lshl_add_u64 v[12:13], v[174:175], 0, s[28:29]
	v_lshl_add_u64 v[18:19], v[176:177], 0, s[28:29]
	v_lshl_add_u64 v[20:21], v[178:179], 0, s[28:29]
	v_lshl_add_u64 v[26:27], v[180:181], 0, s[28:29]
	v_lshl_add_u64 v[28:29], v[182:183], 0, s[28:29]
	global_load_dwordx4 v[106:109], v[2:3], off nt
	global_load_dwordx4 v[94:97], v[4:5], off nt
	global_load_dwordx4 v[66:69], v[10:11], off nt
	global_load_dwordx4 v[54:57], v[12:13], off nt
	global_load_dwordx4 v[38:41], v[18:19], off nt
	s_nop 0
	global_load_dwordx4 v[18:21], v[20:21], off nt
	s_nop 0
	global_load_dwordx4 v[10:13], v[26:27], off nt
	global_load_dwordx4 v[2:5], v[28:29], off nt
	v_mov_b32_e32 v26, v197
	s_waitcnt vmcnt(23)
	s_waitcnt vmcnt(22)
	s_waitcnt vmcnt(21)
	s_waitcnt vmcnt(20)
	s_waitcnt vmcnt(19)
	s_waitcnt vmcnt(18)
	s_waitcnt vmcnt(17)
	s_waitcnt vmcnt(16)
	s_waitcnt lgkmcnt(0)
	v_pk_fma_f32 v[28:29], v[232:233], v[102:103], 0 op_sel_hi:[0,1,0] neg_lo:[1,0,0] neg_hi:[1,0,0]
	v_pk_fma_f32 v[26:27], v[232:233], v[104:105], 0 op_sel_hi:[0,1,0] neg_lo:[1,0,0] neg_hi:[1,0,0]
	v_cvt_pk_bf16_f32 v28, v28, v29
	v_cvt_pk_bf16_f32 v29, v26, v27
	ds_write_b64 v186, v[28:29]
	v_pk_fma_f32 v[28:29], v[234:235], v[86:87], 0 op_sel_hi:[0,1,0] neg_lo:[1,0,0] neg_hi:[1,0,0]
	v_pk_fma_f32 v[26:27], v[234:235], v[88:89], 0 op_sel_hi:[0,1,0] neg_lo:[1,0,0] neg_hi:[1,0,0]
	v_cvt_pk_bf16_f32 v28, v28, v29
	v_cvt_pk_bf16_f32 v29, v26, v27
	ds_write_b64 v186, v[28:29] offset:544
	v_pk_fma_f32 v[28:29], v[236:237], v[74:75], 0 op_sel_hi:[0,1,0] neg_lo:[1,0,0] neg_hi:[1,0,0]
	v_pk_fma_f32 v[26:27], v[236:237], v[76:77], 0 op_sel_hi:[0,1,0] neg_lo:[1,0,0] neg_hi:[1,0,0]
	v_cvt_pk_bf16_f32 v28, v28, v29
	v_cvt_pk_bf16_f32 v29, v26, v27
	ds_write_b64 v186, v[28:29] offset:1088
	v_pk_fma_f32 v[28:29], v[238:239], v[62:63], 0 op_sel_hi:[0,1,0] neg_lo:[1,0,0] neg_hi:[1,0,0]
	v_pk_fma_f32 v[26:27], v[238:239], v[64:65], 0 op_sel_hi:[0,1,0] neg_lo:[1,0,0] neg_hi:[1,0,0]
	v_cvt_pk_bf16_f32 v28, v28, v29
	v_cvt_pk_bf16_f32 v29, v26, v27
	ds_write_b64 v186, v[28:29] offset:1632
	v_pk_fma_f32 v[28:29], v[240:241], v[58:59], 0 op_sel_hi:[0,1,0] neg_lo:[1,0,0] neg_hi:[1,0,0]
	v_pk_fma_f32 v[26:27], v[240:241], v[60:61], 0 op_sel_hi:[0,1,0] neg_lo:[1,0,0] neg_hi:[1,0,0]
	v_cvt_pk_bf16_f32 v28, v28, v29
	v_cvt_pk_bf16_f32 v29, v26, v27
	ds_write_b64 v186, v[28:29] offset:2176
	v_pk_fma_f32 v[28:29], v[242:243], v[46:47], 0 op_sel_hi:[0,1,0] neg_lo:[1,0,0] neg_hi:[1,0,0]
	v_pk_fma_f32 v[26:27], v[242:243], v[48:49], 0 op_sel_hi:[0,1,0] neg_lo:[1,0,0] neg_hi:[1,0,0]
	v_cvt_pk_bf16_f32 v28, v28, v29
	v_cvt_pk_bf16_f32 v29, v26, v27
	ds_write_b64 v186, v[28:29] offset:2720
	v_pk_fma_f32 v[28:29], v[244:245], v[42:43], 0 op_sel_hi:[0,1,0] neg_lo:[1,0,0] neg_hi:[1,0,0]
	v_pk_fma_f32 v[26:27], v[244:245], v[44:45], 0 op_sel_hi:[0,1,0] neg_lo:[1,0,0] neg_hi:[1,0,0]
	v_cvt_pk_bf16_f32 v28, v28, v29
	v_cvt_pk_bf16_f32 v29, v26, v27
	ds_write_b64 v186, v[28:29] offset:3264
	v_pk_fma_f32 v[28:29], v[246:247], v[30:31], 0 op_sel_hi:[0,1,0] neg_lo:[1,0,0] neg_hi:[1,0,0]
	v_pk_fma_f32 v[26:27], v[246:247], v[32:33], 0 op_sel_hi:[0,1,0] neg_lo:[1,0,0] neg_hi:[1,0,0]
	v_cvt_pk_bf16_f32 v28, v28, v29
	v_cvt_pk_bf16_f32 v29, v26, v27
	ds_write_b64 v186, v[28:29] offset:3808
	ds_read_b32 v232, v187 offset:64
	ds_read_b32 v234, v187 offset:72
	ds_read_b32 v236, v187 offset:80
	ds_read_b32 v238, v187 offset:88
	ds_read_b32 v240, v187 offset:96
	ds_read_b32 v242, v187 offset:104
	ds_read_b32 v244, v187 offset:112
	ds_read_b32 v246, v187 offset:120
	ds_read_b128 a[48:51], v1
	ds_read_b128 a[52:55], v1 offset:64
	ds_read_b128 a[56:59], v1 offset:128
	ds_read_b128 a[60:63], v1 offset:192
	v_lshl_add_u64 v[26:27], v[130:131], 0, s[26:27]
	v_add_co_u32_e32 v28, vcc, s7, v26
	s_nop 1
	v_addc_co_u32_e32 v29, vcc, 0, v27, vcc
	global_load_dwordx4 v[86:89], v[26:27], off nt
	global_load_dwordx4 v[82:85], v[28:29], off nt
	v_add_co_u32_e32 v28, vcc, s36, v26
	s_nop 1
	v_addc_co_u32_e32 v29, vcc, 0, v27, vcc
	v_add_co_u32_e32 v30, vcc, s37, v26
	s_nop 1
	v_addc_co_u32_e32 v31, vcc, 0, v27, vcc
	global_load_dwordx4 v[78:81], v[28:29], off nt
	global_load_dwordx4 v[58:61], v[30:31], off nt
	v_add_co_u32_e32 v28, vcc, s38, v26
	s_nop 1
	v_addc_co_u32_e32 v29, vcc, 0, v27, vcc
	v_add_co_u32_e32 v30, vcc, s39, v26
	s_nop 1
	v_addc_co_u32_e32 v31, vcc, 0, v27, vcc
	global_load_dwordx4 v[46:49], v[28:29], off nt
	global_load_dwordx4 v[42:45], v[30:31], off nt
	v_add_co_u32_e32 v28, vcc, s41, v26
	s_nop 1
	v_addc_co_u32_e32 v29, vcc, 0, v27, vcc
	v_add_co_u32_e32 v26, vcc, s42, v26
	s_nop 1
	v_addc_co_u32_e32 v27, vcc, 0, v27, vcc
	global_load_dwordx4 v[30:33], v[28:29], off nt
	s_nop 0
	global_load_dwordx4 v[26:29], v[26:27], off nt
	v_mov_b32_e32 v62, v197
	s_waitcnt vmcnt(23)
	s_waitcnt vmcnt(22)
	s_waitcnt vmcnt(21)
	s_waitcnt vmcnt(20)
	s_waitcnt vmcnt(19)
	s_waitcnt vmcnt(18)
	s_waitcnt vmcnt(17)
	s_waitcnt vmcnt(16)
	s_waitcnt lgkmcnt(0)
	v_pk_fma_f32 v[64:65], v[232:233], v[110:111], 0 op_sel_hi:[0,1,0] neg_lo:[1,0,0] neg_hi:[1,0,0]
	v_pk_fma_f32 v[62:63], v[232:233], v[112:113], 0 op_sel_hi:[0,1,0] neg_lo:[1,0,0] neg_hi:[1,0,0]
	v_cvt_pk_bf16_f32 v64, v64, v65
	v_cvt_pk_bf16_f32 v65, v62, v63
	ds_write_b64 v186, v[64:65]
	v_pk_fma_f32 v[64:65], v[234:235], v[90:91], 0 op_sel_hi:[0,1,0] neg_lo:[1,0,0] neg_hi:[1,0,0]
	v_pk_fma_f32 v[62:63], v[234:235], v[92:93], 0 op_sel_hi:[0,1,0] neg_lo:[1,0,0] neg_hi:[1,0,0]
	v_cvt_pk_bf16_f32 v64, v64, v65
	v_cvt_pk_bf16_f32 v65, v62, v63
	ds_write_b64 v186, v[64:65] offset:544
	v_pk_fma_f32 v[64:65], v[236:237], v[70:71], 0 op_sel_hi:[0,1,0] neg_lo:[1,0,0] neg_hi:[1,0,0]
	v_pk_fma_f32 v[62:63], v[236:237], v[72:73], 0 op_sel_hi:[0,1,0] neg_lo:[1,0,0] neg_hi:[1,0,0]
	v_cvt_pk_bf16_f32 v64, v64, v65
	v_cvt_pk_bf16_f32 v65, v62, v63
	ds_write_b64 v186, v[64:65] offset:1088
	v_pk_fma_f32 v[50:51], v[238:239], v[50:51], 0 op_sel_hi:[0,1,0] neg_lo:[1,0,0] neg_hi:[1,0,0]
	v_pk_fma_f32 v[52:53], v[238:239], v[52:53], 0 op_sel_hi:[0,1,0] neg_lo:[1,0,0] neg_hi:[1,0,0]
	v_cvt_pk_bf16_f32 v50, v50, v51
	v_cvt_pk_bf16_f32 v51, v52, v53
	ds_write_b64 v186, v[50:51] offset:1632
	v_pk_fma_f32 v[34:35], v[240:241], v[34:35], 0 op_sel_hi:[0,1,0] neg_lo:[1,0,0] neg_hi:[1,0,0]
	v_pk_fma_f32 v[36:37], v[240:241], v[36:37], 0 op_sel_hi:[0,1,0] neg_lo:[1,0,0] neg_hi:[1,0,0]
	v_cvt_pk_bf16_f32 v34, v34, v35
	v_cvt_pk_bf16_f32 v35, v36, v37
	ds_write_b64 v186, v[34:35] offset:2176
	v_pk_fma_f32 v[22:23], v[242:243], v[22:23], 0 op_sel_hi:[0,1,0] neg_lo:[1,0,0] neg_hi:[1,0,0]
	v_pk_fma_f32 v[24:25], v[242:243], v[24:25], 0 op_sel_hi:[0,1,0] neg_lo:[1,0,0] neg_hi:[1,0,0]
	v_cvt_pk_bf16_f32 v22, v22, v23
	v_cvt_pk_bf16_f32 v23, v24, v25
	ds_write_b64 v186, v[22:23] offset:2720
	v_pk_fma_f32 v[14:15], v[244:245], v[14:15], 0 op_sel_hi:[0,1,0] neg_lo:[1,0,0] neg_hi:[1,0,0]
	v_pk_fma_f32 v[16:17], v[244:245], v[16:17], 0 op_sel_hi:[0,1,0] neg_lo:[1,0,0] neg_hi:[1,0,0]
	v_cvt_pk_bf16_f32 v14, v14, v15
	v_cvt_pk_bf16_f32 v15, v16, v17
	ds_write_b64 v186, v[14:15] offset:3264
	v_pk_fma_f32 v[6:7], v[246:247], v[6:7], 0 op_sel_hi:[0,1,0] neg_lo:[1,0,0] neg_hi:[1,0,0]
	v_pk_fma_f32 v[8:9], v[246:247], v[8:9], 0 op_sel_hi:[0,1,0] neg_lo:[1,0,0] neg_hi:[1,0,0]
	v_cvt_pk_bf16_f32 v6, v6, v7
	v_cvt_pk_bf16_f32 v7, v8, v9
	ds_write_b64 v186, v[6:7] offset:3808
	ds_read_b32 v232, v187 offset:128
	ds_read_b32 v234, v187 offset:136
	ds_read_b32 v236, v187 offset:144
	ds_read_b32 v238, v187 offset:152
	ds_read_b32 v240, v187 offset:160
	ds_read_b32 v242, v187 offset:168
	ds_read_b32 v244, v187 offset:176
	ds_read_b32 v246, v187 offset:184
	ds_read_b128 a[64:67], v1
	ds_read_b128 a[68:71], v1 offset:64
	ds_read_b128 a[72:75], v1 offset:128
	ds_read_b128 a[76:79], v1 offset:192
	v_lshl_add_u64 v[6:7], v[150:151], 0, s[26:27]
	v_lshl_add_u64 v[8:9], v[152:153], 0, s[26:27]
	v_lshl_add_u64 v[14:15], v[156:157], 0, s[26:27]
	v_lshl_add_u64 v[16:17], v[158:159], 0, s[26:27]
	v_lshl_add_u64 v[22:23], v[160:161], 0, s[26:27]
	v_lshl_add_u64 v[24:25], v[162:163], 0, s[26:27]
	v_lshl_add_u64 v[70:71], v[164:165], 0, s[26:27]
	v_lshl_add_u64 v[72:73], v[166:167], 0, s[26:27]
	global_load_dwordx4 v[110:113], v[6:7], off nt
	global_load_dwordx4 v[98:101], v[8:9], off nt
	global_load_dwordx4 v[62:65], v[14:15], off nt
	global_load_dwordx4 v[50:53], v[16:17], off nt
	global_load_dwordx4 v[34:37], v[22:23], off nt
	s_nop 0
	global_load_dwordx4 v[22:25], v[24:25], off nt
	s_nop 0
	global_load_dwordx4 v[14:17], v[70:71], off nt
	global_load_dwordx4 v[6:9], v[72:73], off nt
	s_waitcnt vmcnt(23)
	s_waitcnt vmcnt(22)
	s_waitcnt vmcnt(21)
	s_waitcnt vmcnt(20)
	s_waitcnt vmcnt(19)
	s_waitcnt vmcnt(18)
	s_waitcnt vmcnt(17)
	s_waitcnt vmcnt(16)
	s_waitcnt lgkmcnt(0)
	v_pk_fma_f32 v[72:73], v[232:233], v[106:107], 0 op_sel_hi:[0,1,0] neg_lo:[1,0,0] neg_hi:[1,0,0]
	v_pk_fma_f32 v[70:71], v[232:233], v[108:109], 0 op_sel_hi:[0,1,0] neg_lo:[1,0,0] neg_hi:[1,0,0]
	v_cvt_pk_bf16_f32 v72, v72, v73
	v_cvt_pk_bf16_f32 v73, v70, v71
	ds_write_b64 v186, v[72:73]
	v_pk_fma_f32 v[72:73], v[234:235], v[94:95], 0 op_sel_hi:[0,1,0] neg_lo:[1,0,0] neg_hi:[1,0,0]
	v_pk_fma_f32 v[70:71], v[234:235], v[96:97], 0 op_sel_hi:[0,1,0] neg_lo:[1,0,0] neg_hi:[1,0,0]
	v_cvt_pk_bf16_f32 v72, v72, v73
	v_cvt_pk_bf16_f32 v73, v70, v71
	ds_write_b64 v186, v[72:73] offset:544
	v_pk_fma_f32 v[66:67], v[236:237], v[66:67], 0 op_sel_hi:[0,1,0] neg_lo:[1,0,0] neg_hi:[1,0,0]
	v_pk_fma_f32 v[68:69], v[236:237], v[68:69], 0 op_sel_hi:[0,1,0] neg_lo:[1,0,0] neg_hi:[1,0,0]
	v_cvt_pk_bf16_f32 v66, v66, v67
	v_cvt_pk_bf16_f32 v67, v68, v69
	ds_write_b64 v186, v[66:67] offset:1088
	v_pk_fma_f32 v[54:55], v[238:239], v[54:55], 0 op_sel_hi:[0,1,0] neg_lo:[1,0,0] neg_hi:[1,0,0]
	v_pk_fma_f32 v[56:57], v[238:239], v[56:57], 0 op_sel_hi:[0,1,0] neg_lo:[1,0,0] neg_hi:[1,0,0]
	v_cvt_pk_bf16_f32 v54, v54, v55
	v_cvt_pk_bf16_f32 v55, v56, v57
	ds_write_b64 v186, v[54:55] offset:1632
	v_pk_fma_f32 v[38:39], v[240:241], v[38:39], 0 op_sel_hi:[0,1,0] neg_lo:[1,0,0] neg_hi:[1,0,0]
	v_pk_fma_f32 v[40:41], v[240:241], v[40:41], 0 op_sel_hi:[0,1,0] neg_lo:[1,0,0] neg_hi:[1,0,0]
	v_cvt_pk_bf16_f32 v38, v38, v39
	v_cvt_pk_bf16_f32 v39, v40, v41
	ds_write_b64 v186, v[38:39] offset:2176
	v_pk_fma_f32 v[18:19], v[242:243], v[18:19], 0 op_sel_hi:[0,1,0] neg_lo:[1,0,0] neg_hi:[1,0,0]
	v_pk_fma_f32 v[20:21], v[242:243], v[20:21], 0 op_sel_hi:[0,1,0] neg_lo:[1,0,0] neg_hi:[1,0,0]
	v_cvt_pk_bf16_f32 v18, v18, v19
	v_cvt_pk_bf16_f32 v19, v20, v21
	ds_write_b64 v186, v[18:19] offset:2720
	v_pk_fma_f32 v[10:11], v[244:245], v[10:11], 0 op_sel_hi:[0,1,0] neg_lo:[1,0,0] neg_hi:[1,0,0]
	v_pk_fma_f32 v[12:13], v[244:245], v[12:13], 0 op_sel_hi:[0,1,0] neg_lo:[1,0,0] neg_hi:[1,0,0]
	v_cvt_pk_bf16_f32 v10, v10, v11
	v_cvt_pk_bf16_f32 v11, v12, v13
	ds_write_b64 v186, v[10:11] offset:3264
	v_pk_fma_f32 v[2:3], v[246:247], v[2:3], 0 op_sel_hi:[0,1,0] neg_lo:[1,0,0] neg_hi:[1,0,0]
	v_pk_fma_f32 v[4:5], v[246:247], v[4:5], 0 op_sel_hi:[0,1,0] neg_lo:[1,0,0] neg_hi:[1,0,0]
	v_cvt_pk_bf16_f32 v2, v2, v3
	v_cvt_pk_bf16_f32 v3, v4, v5
	ds_write_b64 v186, v[2:3] offset:3808
	ds_read_b32 v232, v187 offset:0
	ds_read_b32 v234, v187 offset:8
	ds_read_b32 v236, v187 offset:16
	ds_read_b32 v238, v187 offset:24
	ds_read_b32 v240, v187 offset:32
	ds_read_b32 v242, v187 offset:40
	ds_read_b32 v244, v187 offset:48
	ds_read_b32 v246, v187 offset:56
	ds_read_b128 a[80:83], v1
	ds_read_b128 a[84:87], v1 offset:64
	ds_read_b128 a[88:91], v1 offset:128
	ds_read_b128 a[92:95], v1 offset:192
	v_lshl_add_u64 v[2:3], v[168:169], 0, s[26:27]
	v_lshl_add_u64 v[4:5], v[170:171], 0, s[26:27]
	v_lshl_add_u64 v[10:11], v[172:173], 0, s[26:27]
	v_lshl_add_u64 v[12:13], v[174:175], 0, s[26:27]
	v_lshl_add_u64 v[18:19], v[176:177], 0, s[26:27]
	v_lshl_add_u64 v[20:21], v[178:179], 0, s[26:27]
	v_lshl_add_u64 v[66:67], v[180:181], 0, s[26:27]
	v_lshl_add_u64 v[68:69], v[182:183], 0, s[26:27]
	global_load_dwordx4 v[106:109], v[2:3], off nt
	global_load_dwordx4 v[94:97], v[4:5], off nt
	global_load_dwordx4 v[74:77], v[10:11], off nt
	global_load_dwordx4 v[54:57], v[12:13], off nt
	global_load_dwordx4 v[38:41], v[18:19], off nt
	s_nop 0
	global_load_dwordx4 v[18:21], v[20:21], off nt
	s_nop 0
	global_load_dwordx4 v[10:13], v[66:67], off nt
	global_load_dwordx4 v[2:5], v[68:69], off nt
	v_mov_b32_e32 v66, v196
	s_waitcnt vmcnt(23)
	s_waitcnt vmcnt(22)
	s_waitcnt vmcnt(21)
	s_waitcnt vmcnt(20)
	s_waitcnt vmcnt(19)
	s_waitcnt vmcnt(18)
	s_waitcnt vmcnt(17)
	s_waitcnt vmcnt(16)
	s_waitcnt lgkmcnt(0)
	v_pk_fma_f32 v[68:69], v[232:233], v[86:87], 0 op_sel_hi:[0,1,0] neg_lo:[1,0,0] neg_hi:[1,0,0]
	v_pk_fma_f32 v[66:67], v[232:233], v[88:89], 0 op_sel_hi:[0,1,0] neg_lo:[1,0,0] neg_hi:[1,0,0]
	v_cvt_pk_bf16_f32 v68, v68, v69
	v_cvt_pk_bf16_f32 v69, v66, v67
	ds_write_b64 v186, v[68:69]
	v_pk_fma_f32 v[68:69], v[234:235], v[82:83], 0 op_sel_hi:[0,1,0] neg_lo:[1,0,0] neg_hi:[1,0,0]
	v_pk_fma_f32 v[66:67], v[234:235], v[84:85], 0 op_sel_hi:[0,1,0] neg_lo:[1,0,0] neg_hi:[1,0,0]
	v_cvt_pk_bf16_f32 v68, v68, v69
	v_cvt_pk_bf16_f32 v69, v66, v67
	ds_write_b64 v186, v[68:69] offset:544
	v_pk_fma_f32 v[68:69], v[236:237], v[78:79], 0 op_sel_hi:[0,1,0] neg_lo:[1,0,0] neg_hi:[1,0,0]
	v_pk_fma_f32 v[66:67], v[236:237], v[80:81], 0 op_sel_hi:[0,1,0] neg_lo:[1,0,0] neg_hi:[1,0,0]
	v_cvt_pk_bf16_f32 v68, v68, v69
	v_cvt_pk_bf16_f32 v69, v66, v67
	ds_write_b64 v186, v[68:69] offset:1088
	v_pk_fma_f32 v[58:59], v[238:239], v[58:59], 0 op_sel_hi:[0,1,0] neg_lo:[1,0,0] neg_hi:[1,0,0]
	v_pk_fma_f32 v[60:61], v[238:239], v[60:61], 0 op_sel_hi:[0,1,0] neg_lo:[1,0,0] neg_hi:[1,0,0]
	v_cvt_pk_bf16_f32 v58, v58, v59
	v_cvt_pk_bf16_f32 v59, v60, v61
	ds_write_b64 v186, v[58:59] offset:1632
	v_pk_fma_f32 v[46:47], v[240:241], v[46:47], 0 op_sel_hi:[0,1,0] neg_lo:[1,0,0] neg_hi:[1,0,0]
	v_pk_fma_f32 v[48:49], v[240:241], v[48:49], 0 op_sel_hi:[0,1,0] neg_lo:[1,0,0] neg_hi:[1,0,0]
	v_cvt_pk_bf16_f32 v46, v46, v47
	v_cvt_pk_bf16_f32 v47, v48, v49
	ds_write_b64 v186, v[46:47] offset:2176
	v_pk_fma_f32 v[42:43], v[242:243], v[42:43], 0 op_sel_hi:[0,1,0] neg_lo:[1,0,0] neg_hi:[1,0,0]
	v_pk_fma_f32 v[44:45], v[242:243], v[44:45], 0 op_sel_hi:[0,1,0] neg_lo:[1,0,0] neg_hi:[1,0,0]
	v_cvt_pk_bf16_f32 v42, v42, v43
	v_cvt_pk_bf16_f32 v43, v44, v45
	ds_write_b64 v186, v[42:43] offset:2720
	v_pk_fma_f32 v[30:31], v[244:245], v[30:31], 0 op_sel_hi:[0,1,0] neg_lo:[1,0,0] neg_hi:[1,0,0]
	v_pk_fma_f32 v[32:33], v[244:245], v[32:33], 0 op_sel_hi:[0,1,0] neg_lo:[1,0,0] neg_hi:[1,0,0]
	v_cvt_pk_bf16_f32 v30, v30, v31
	v_cvt_pk_bf16_f32 v31, v32, v33
	ds_write_b64 v186, v[30:31] offset:3264
	v_pk_fma_f32 v[26:27], v[246:247], v[26:27], 0 op_sel_hi:[0,1,0] neg_lo:[1,0,0] neg_hi:[1,0,0]
	v_pk_fma_f32 v[28:29], v[246:247], v[28:29], 0 op_sel_hi:[0,1,0] neg_lo:[1,0,0] neg_hi:[1,0,0]
	v_cvt_pk_bf16_f32 v26, v26, v27
	v_cvt_pk_bf16_f32 v27, v28, v29
	ds_write_b64 v186, v[26:27] offset:3808
	ds_read_b32 v232, v187 offset:64
	ds_read_b32 v234, v187 offset:72
	ds_read_b32 v236, v187 offset:80
	ds_read_b32 v238, v187 offset:88
	ds_read_b32 v240, v187 offset:96
	ds_read_b32 v242, v187 offset:104
	ds_read_b32 v244, v187 offset:112
	ds_read_b32 v246, v187 offset:120
	ds_read_b128 a[96:99], v1
	ds_read_b128 a[100:103], v1 offset:64
	ds_read_b128 a[104:107], v1 offset:128
	ds_read_b128 a[108:111], v1 offset:192
	v_lshl_add_u64 v[26:27], v[130:131], 0, s[24:25]
	v_add_co_u32_e32 v28, vcc, s7, v26
	s_nop 1
	v_addc_co_u32_e32 v29, vcc, 0, v27, vcc
	global_load_dwordx4 v[102:105], v[26:27], off nt
	global_load_dwordx4 v[90:93], v[28:29], off nt
	v_add_co_u32_e32 v28, vcc, s36, v26
	s_nop 1
	v_addc_co_u32_e32 v29, vcc, 0, v27, vcc
	v_add_co_u32_e32 v30, vcc, s37, v26
	s_nop 1
	v_addc_co_u32_e32 v31, vcc, 0, v27, vcc
	global_load_dwordx4 v[86:89], v[28:29], off nt
	global_load_dwordx4 v[70:73], v[30:31], off nt
	v_add_co_u32_e32 v28, vcc, s38, v26
	s_nop 1
	v_addc_co_u32_e32 v29, vcc, 0, v27, vcc
	v_add_co_u32_e32 v30, vcc, s39, v26
	s_nop 1
	v_addc_co_u32_e32 v31, vcc, 0, v27, vcc
	global_load_dwordx4 v[66:69], v[28:29], off nt
	global_load_dwordx4 v[46:49], v[30:31], off nt
	v_add_co_u32_e32 v28, vcc, s41, v26
	s_nop 1
	v_addc_co_u32_e32 v29, vcc, 0, v27, vcc
	v_add_co_u32_e32 v26, vcc, s42, v26
	s_nop 1
	v_addc_co_u32_e32 v27, vcc, 0, v27, vcc
	global_load_dwordx4 v[42:45], v[28:29], off nt
	global_load_dwordx4 v[30:33], v[26:27], off nt
	v_mov_b32_e32 v26, v196
	s_waitcnt vmcnt(23)
	s_waitcnt vmcnt(22)
	s_waitcnt vmcnt(21)
	s_waitcnt vmcnt(20)
	s_waitcnt vmcnt(19)
	s_waitcnt vmcnt(18)
	s_waitcnt vmcnt(17)
	s_waitcnt vmcnt(16)
	s_waitcnt lgkmcnt(0)
	v_pk_fma_f32 v[28:29], v[232:233], v[110:111], 0 op_sel_hi:[0,1,0] neg_lo:[1,0,0] neg_hi:[1,0,0]
	v_pk_fma_f32 v[26:27], v[232:233], v[112:113], 0 op_sel_hi:[0,1,0] neg_lo:[1,0,0] neg_hi:[1,0,0]
	v_cvt_pk_bf16_f32 v28, v28, v29
	v_cvt_pk_bf16_f32 v29, v26, v27
	ds_write_b64 v186, v[28:29]
	v_pk_fma_f32 v[28:29], v[234:235], v[98:99], 0 op_sel_hi:[0,1,0] neg_lo:[1,0,0] neg_hi:[1,0,0]
	v_pk_fma_f32 v[26:27], v[234:235], v[100:101], 0 op_sel_hi:[0,1,0] neg_lo:[1,0,0] neg_hi:[1,0,0]
	v_cvt_pk_bf16_f32 v28, v28, v29
	v_cvt_pk_bf16_f32 v29, v26, v27
	ds_write_b64 v186, v[28:29] offset:544
	v_pk_fma_f32 v[28:29], v[236:237], v[62:63], 0 op_sel_hi:[0,1,0] neg_lo:[1,0,0] neg_hi:[1,0,0]
	v_pk_fma_f32 v[26:27], v[236:237], v[64:65], 0 op_sel_hi:[0,1,0] neg_lo:[1,0,0] neg_hi:[1,0,0]
	v_cvt_pk_bf16_f32 v28, v28, v29
	v_cvt_pk_bf16_f32 v29, v26, v27
	ds_write_b64 v186, v[28:29] offset:1088
	v_pk_fma_f32 v[28:29], v[238:239], v[50:51], 0 op_sel_hi:[0,1,0] neg_lo:[1,0,0] neg_hi:[1,0,0]
	v_pk_fma_f32 v[26:27], v[238:239], v[52:53], 0 op_sel_hi:[0,1,0] neg_lo:[1,0,0] neg_hi:[1,0,0]
	v_cvt_pk_bf16_f32 v28, v28, v29
	v_cvt_pk_bf16_f32 v29, v26, v27
	ds_write_b64 v186, v[28:29] offset:1632
	v_pk_fma_f32 v[28:29], v[240:241], v[34:35], 0 op_sel_hi:[0,1,0] neg_lo:[1,0,0] neg_hi:[1,0,0]
	v_pk_fma_f32 v[26:27], v[240:241], v[36:37], 0 op_sel_hi:[0,1,0] neg_lo:[1,0,0] neg_hi:[1,0,0]
	v_cvt_pk_bf16_f32 v28, v28, v29
	v_cvt_pk_bf16_f32 v29, v26, v27
	ds_write_b64 v186, v[28:29] offset:2176
	v_pk_fma_f32 v[22:23], v[242:243], v[22:23], 0 op_sel_hi:[0,1,0] neg_lo:[1,0,0] neg_hi:[1,0,0]
	v_pk_fma_f32 v[24:25], v[242:243], v[24:25], 0 op_sel_hi:[0,1,0] neg_lo:[1,0,0] neg_hi:[1,0,0]
	v_cvt_pk_bf16_f32 v22, v22, v23
	v_cvt_pk_bf16_f32 v23, v24, v25
	ds_write_b64 v186, v[22:23] offset:2720
	v_pk_fma_f32 v[14:15], v[244:245], v[14:15], 0 op_sel_hi:[0,1,0] neg_lo:[1,0,0] neg_hi:[1,0,0]
	v_pk_fma_f32 v[16:17], v[244:245], v[16:17], 0 op_sel_hi:[0,1,0] neg_lo:[1,0,0] neg_hi:[1,0,0]
	v_cvt_pk_bf16_f32 v14, v14, v15
	v_cvt_pk_bf16_f32 v15, v16, v17
	ds_write_b64 v186, v[14:15] offset:3264
	v_pk_fma_f32 v[6:7], v[246:247], v[6:7], 0 op_sel_hi:[0,1,0] neg_lo:[1,0,0] neg_hi:[1,0,0]
	v_pk_fma_f32 v[8:9], v[246:247], v[8:9], 0 op_sel_hi:[0,1,0] neg_lo:[1,0,0] neg_hi:[1,0,0]
	v_cvt_pk_bf16_f32 v6, v6, v7
	v_cvt_pk_bf16_f32 v7, v8, v9
	ds_write_b64 v186, v[6:7] offset:3808
	ds_read_b32 v232, v187 offset:128
	ds_read_b32 v234, v187 offset:136
	ds_read_b32 v236, v187 offset:144
	ds_read_b32 v238, v187 offset:152
	ds_read_b32 v240, v187 offset:160
	ds_read_b32 v242, v187 offset:168
	ds_read_b32 v244, v187 offset:176
	ds_read_b32 v246, v187 offset:184
	ds_read_b128 a[112:115], v1
	ds_read_b128 a[116:119], v1 offset:64
	ds_read_b128 a[120:123], v1 offset:128
	ds_read_b128 a[124:127], v1 offset:192
	v_lshl_add_u64 v[6:7], v[150:151], 0, s[24:25]
	v_lshl_add_u64 v[8:9], v[152:153], 0, s[24:25]
	v_lshl_add_u64 v[14:15], v[156:157], 0, s[24:25]
	v_lshl_add_u64 v[16:17], v[158:159], 0, s[24:25]
	v_lshl_add_u64 v[22:23], v[160:161], 0, s[24:25]
	v_lshl_add_u64 v[24:25], v[162:163], 0, s[24:25]
	v_lshl_add_u64 v[26:27], v[164:165], 0, s[24:25]
	v_lshl_add_u64 v[28:29], v[166:167], 0, s[24:25]
	global_load_dwordx4 v[110:113], v[6:7], off nt
	global_load_dwordx4 v[98:101], v[8:9], off nt
	global_load_dwordx4 v[78:81], v[14:15], off nt
	global_load_dwordx4 v[58:61], v[16:17], off nt
	global_load_dwordx4 v[34:37], v[22:23], off nt
	s_nop 0
	global_load_dwordx4 v[22:25], v[24:25], off nt
	s_nop 0
	global_load_dwordx4 v[14:17], v[26:27], off nt
	global_load_dwordx4 v[6:9], v[28:29], off nt
	s_waitcnt vmcnt(23)
	s_waitcnt vmcnt(22)
	s_waitcnt vmcnt(21)
	s_waitcnt vmcnt(20)
	s_waitcnt vmcnt(19)
	s_waitcnt vmcnt(18)
	s_waitcnt vmcnt(17)
	s_waitcnt vmcnt(16)
	s_waitcnt lgkmcnt(0)
	v_pk_fma_f32 v[28:29], v[232:233], v[106:107], 0 op_sel_hi:[0,1,0] neg_lo:[1,0,0] neg_hi:[1,0,0]
	v_pk_fma_f32 v[26:27], v[232:233], v[108:109], 0 op_sel_hi:[0,1,0] neg_lo:[1,0,0] neg_hi:[1,0,0]
	v_cvt_pk_bf16_f32 v28, v28, v29
	v_cvt_pk_bf16_f32 v29, v26, v27
	ds_write_b64 v186, v[28:29]
	v_pk_fma_f32 v[28:29], v[234:235], v[94:95], 0 op_sel_hi:[0,1,0] neg_lo:[1,0,0] neg_hi:[1,0,0]
	v_pk_fma_f32 v[26:27], v[234:235], v[96:97], 0 op_sel_hi:[0,1,0] neg_lo:[1,0,0] neg_hi:[1,0,0]
	v_cvt_pk_bf16_f32 v28, v28, v29
	v_cvt_pk_bf16_f32 v29, v26, v27
	ds_write_b64 v186, v[28:29] offset:544
	v_pk_fma_f32 v[28:29], v[236:237], v[74:75], 0 op_sel_hi:[0,1,0] neg_lo:[1,0,0] neg_hi:[1,0,0]
	v_pk_fma_f32 v[26:27], v[236:237], v[76:77], 0 op_sel_hi:[0,1,0] neg_lo:[1,0,0] neg_hi:[1,0,0]
	v_cvt_pk_bf16_f32 v28, v28, v29
	v_cvt_pk_bf16_f32 v29, v26, v27
	ds_write_b64 v186, v[28:29] offset:1088
	v_pk_fma_f32 v[28:29], v[238:239], v[54:55], 0 op_sel_hi:[0,1,0] neg_lo:[1,0,0] neg_hi:[1,0,0]
	v_pk_fma_f32 v[26:27], v[238:239], v[56:57], 0 op_sel_hi:[0,1,0] neg_lo:[1,0,0] neg_hi:[1,0,0]
	v_cvt_pk_bf16_f32 v28, v28, v29
	v_cvt_pk_bf16_f32 v29, v26, v27
	ds_write_b64 v186, v[28:29] offset:1632
	v_pk_fma_f32 v[28:29], v[240:241], v[38:39], 0 op_sel_hi:[0,1,0] neg_lo:[1,0,0] neg_hi:[1,0,0]
	v_pk_fma_f32 v[26:27], v[240:241], v[40:41], 0 op_sel_hi:[0,1,0] neg_lo:[1,0,0] neg_hi:[1,0,0]
	v_cvt_pk_bf16_f32 v28, v28, v29
	v_cvt_pk_bf16_f32 v29, v26, v27
	ds_write_b64 v186, v[28:29] offset:2176
	v_pk_fma_f32 v[18:19], v[242:243], v[18:19], 0 op_sel_hi:[0,1,0] neg_lo:[1,0,0] neg_hi:[1,0,0]
	v_pk_fma_f32 v[20:21], v[242:243], v[20:21], 0 op_sel_hi:[0,1,0] neg_lo:[1,0,0] neg_hi:[1,0,0]
	v_cvt_pk_bf16_f32 v18, v18, v19
	v_cvt_pk_bf16_f32 v19, v20, v21
	ds_write_b64 v186, v[18:19] offset:2720
	v_pk_fma_f32 v[10:11], v[244:245], v[10:11], 0 op_sel_hi:[0,1,0] neg_lo:[1,0,0] neg_hi:[1,0,0]
	v_pk_fma_f32 v[12:13], v[244:245], v[12:13], 0 op_sel_hi:[0,1,0] neg_lo:[1,0,0] neg_hi:[1,0,0]
	v_cvt_pk_bf16_f32 v10, v10, v11
	v_cvt_pk_bf16_f32 v11, v12, v13
	ds_write_b64 v186, v[10:11] offset:3264
	v_pk_fma_f32 v[2:3], v[246:247], v[2:3], 0 op_sel_hi:[0,1,0] neg_lo:[1,0,0] neg_hi:[1,0,0]
	v_pk_fma_f32 v[4:5], v[246:247], v[4:5], 0 op_sel_hi:[0,1,0] neg_lo:[1,0,0] neg_hi:[1,0,0]
	v_cvt_pk_bf16_f32 v2, v2, v3
	v_cvt_pk_bf16_f32 v3, v4, v5
	ds_write_b64 v186, v[2:3] offset:3808
	ds_read_b32 v232, v187 offset:0
	ds_read_b32 v234, v187 offset:8
	ds_read_b32 v236, v187 offset:16
	ds_read_b32 v238, v187 offset:24
	ds_read_b32 v240, v187 offset:32
	ds_read_b32 v242, v187 offset:40
	ds_read_b32 v244, v187 offset:48
	ds_read_b32 v246, v187 offset:56
	ds_read_b128 a[128:131], v1
	ds_read_b128 a[132:135], v1 offset:64
	ds_read_b128 a[136:139], v1 offset:128
	ds_read_b128 a[140:143], v1 offset:192
	v_lshl_add_u64 v[2:3], v[168:169], 0, s[24:25]
	v_lshl_add_u64 v[4:5], v[170:171], 0, s[24:25]
	v_lshl_add_u64 v[10:11], v[172:173], 0, s[24:25]
	v_lshl_add_u64 v[12:13], v[174:175], 0, s[24:25]
	v_lshl_add_u64 v[18:19], v[176:177], 0, s[24:25]
	v_lshl_add_u64 v[20:21], v[178:179], 0, s[24:25]
	v_lshl_add_u64 v[50:51], v[180:181], 0, s[24:25]
	v_lshl_add_u64 v[52:53], v[182:183], 0, s[24:25]
	global_load_dwordx4 v[114:117], v[2:3], off nt
	global_load_dwordx4 v[94:97], v[4:5], off nt
	global_load_dwordx4 v[82:85], v[10:11], off nt
	global_load_dwordx4 v[62:65], v[12:13], off nt
	global_load_dwordx4 v[38:41], v[18:19], off nt
	global_load_dwordx4 v[26:29], v[20:21], off nt
	s_nop 0
	global_load_dwordx4 v[10:13], v[50:51], off nt
	global_load_dwordx4 v[2:5], v[52:53], off nt
	v_mov_b32_e32 v18, v195
	s_waitcnt vmcnt(23)
	s_waitcnt vmcnt(22)
	s_waitcnt vmcnt(21)
	s_waitcnt vmcnt(20)
	s_waitcnt vmcnt(19)
	s_waitcnt vmcnt(18)
	s_waitcnt vmcnt(17)
	s_waitcnt vmcnt(16)
	s_waitcnt lgkmcnt(0)
	v_pk_fma_f32 v[20:21], v[232:233], v[102:103], 0 op_sel_hi:[0,1,0] neg_lo:[1,0,0] neg_hi:[1,0,0]
	v_pk_fma_f32 v[18:19], v[232:233], v[104:105], 0 op_sel_hi:[0,1,0] neg_lo:[1,0,0] neg_hi:[1,0,0]
	v_cvt_pk_bf16_f32 v20, v20, v21
	v_cvt_pk_bf16_f32 v21, v18, v19
	ds_write_b64 v186, v[20:21]
	v_pk_fma_f32 v[20:21], v[234:235], v[90:91], 0 op_sel_hi:[0,1,0] neg_lo:[1,0,0] neg_hi:[1,0,0]
	v_pk_fma_f32 v[18:19], v[234:235], v[92:93], 0 op_sel_hi:[0,1,0] neg_lo:[1,0,0] neg_hi:[1,0,0]
	v_cvt_pk_bf16_f32 v20, v20, v21
	v_cvt_pk_bf16_f32 v21, v18, v19
	ds_write_b64 v186, v[20:21] offset:544
	v_pk_fma_f32 v[20:21], v[236:237], v[86:87], 0 op_sel_hi:[0,1,0] neg_lo:[1,0,0] neg_hi:[1,0,0]
	v_pk_fma_f32 v[18:19], v[236:237], v[88:89], 0 op_sel_hi:[0,1,0] neg_lo:[1,0,0] neg_hi:[1,0,0]
	v_cvt_pk_bf16_f32 v20, v20, v21
	v_cvt_pk_bf16_f32 v21, v18, v19
	ds_write_b64 v186, v[20:21] offset:1088
	v_pk_fma_f32 v[20:21], v[238:239], v[70:71], 0 op_sel_hi:[0,1,0] neg_lo:[1,0,0] neg_hi:[1,0,0]
	v_pk_fma_f32 v[18:19], v[238:239], v[72:73], 0 op_sel_hi:[0,1,0] neg_lo:[1,0,0] neg_hi:[1,0,0]
	v_cvt_pk_bf16_f32 v20, v20, v21
	v_cvt_pk_bf16_f32 v21, v18, v19
	ds_write_b64 v186, v[20:21] offset:1632
	v_pk_fma_f32 v[20:21], v[240:241], v[66:67], 0 op_sel_hi:[0,1,0] neg_lo:[1,0,0] neg_hi:[1,0,0]
	v_pk_fma_f32 v[18:19], v[240:241], v[68:69], 0 op_sel_hi:[0,1,0] neg_lo:[1,0,0] neg_hi:[1,0,0]
	v_cvt_pk_bf16_f32 v20, v20, v21
	v_cvt_pk_bf16_f32 v21, v18, v19
	ds_write_b64 v186, v[20:21] offset:2176
	v_pk_fma_f32 v[20:21], v[242:243], v[46:47], 0 op_sel_hi:[0,1,0] neg_lo:[1,0,0] neg_hi:[1,0,0]
	v_pk_fma_f32 v[18:19], v[242:243], v[48:49], 0 op_sel_hi:[0,1,0] neg_lo:[1,0,0] neg_hi:[1,0,0]
	v_cvt_pk_bf16_f32 v20, v20, v21
	v_cvt_pk_bf16_f32 v21, v18, v19
	ds_write_b64 v186, v[20:21] offset:2720
	v_pk_fma_f32 v[20:21], v[244:245], v[42:43], 0 op_sel_hi:[0,1,0] neg_lo:[1,0,0] neg_hi:[1,0,0]
	v_pk_fma_f32 v[18:19], v[244:245], v[44:45], 0 op_sel_hi:[0,1,0] neg_lo:[1,0,0] neg_hi:[1,0,0]
	v_cvt_pk_bf16_f32 v20, v20, v21
	v_cvt_pk_bf16_f32 v21, v18, v19
	ds_write_b64 v186, v[20:21] offset:3264
	v_pk_fma_f32 v[20:21], v[246:247], v[30:31], 0 op_sel_hi:[0,1,0] neg_lo:[1,0,0] neg_hi:[1,0,0]
	v_pk_fma_f32 v[18:19], v[246:247], v[32:33], 0 op_sel_hi:[0,1,0] neg_lo:[1,0,0] neg_hi:[1,0,0]
	v_cvt_pk_bf16_f32 v20, v20, v21
	v_cvt_pk_bf16_f32 v21, v18, v19
	ds_write_b64 v186, v[20:21] offset:3808
	ds_read_b32 v232, v187 offset:64
	ds_read_b32 v234, v187 offset:72
	ds_read_b32 v236, v187 offset:80
	ds_read_b32 v238, v187 offset:88
	ds_read_b32 v240, v187 offset:96
	ds_read_b32 v242, v187 offset:104
	ds_read_b32 v244, v187 offset:112
	ds_read_b32 v246, v187 offset:120
	ds_read_b128 a[144:147], v1
	ds_read_b128 a[148:151], v1 offset:64
	ds_read_b128 a[152:155], v1 offset:128
	ds_read_b128 a[156:159], v1 offset:192
	v_lshl_add_u64 v[18:19], v[130:131], 0, s[22:23]
	v_add_co_u32_e32 v20, vcc, s7, v18
	s_nop 1
	v_addc_co_u32_e32 v21, vcc, 0, v19, vcc
	global_load_dwordx4 v[106:109], v[18:19], off nt
	global_load_dwordx4 v[90:93], v[20:21], off nt
	v_add_co_u32_e32 v20, vcc, s36, v18
	s_nop 1
	v_addc_co_u32_e32 v21, vcc, 0, v19, vcc
	v_add_co_u32_e32 v30, vcc, s37, v18
	s_nop 1
	v_addc_co_u32_e32 v31, vcc, 0, v19, vcc
	global_load_dwordx4 v[86:89], v[20:21], off nt
	global_load_dwordx4 v[74:77], v[30:31], off nt
	v_add_co_u32_e32 v20, vcc, s38, v18
	s_nop 1
	v_addc_co_u32_e32 v21, vcc, 0, v19, vcc
	v_add_co_u32_e32 v30, vcc, s39, v18
	s_nop 1
	v_addc_co_u32_e32 v31, vcc, 0, v19, vcc
	global_load_dwordx4 v[70:73], v[20:21], off nt
	global_load_dwordx4 v[54:57], v[30:31], off nt
	v_add_co_u32_e32 v20, vcc, s41, v18
	s_nop 1
	v_addc_co_u32_e32 v21, vcc, 0, v19, vcc
	v_add_co_u32_e32 v18, vcc, s42, v18
	s_nop 1
	v_addc_co_u32_e32 v19, vcc, 0, v19, vcc
	global_load_dwordx4 v[50:53], v[20:21], off nt
	global_load_dwordx4 v[46:49], v[18:19], off nt
	v_mov_b32_e32 v18, v195
	s_waitcnt vmcnt(23)
	s_waitcnt vmcnt(22)
	s_waitcnt vmcnt(21)
	s_waitcnt vmcnt(20)
	s_waitcnt vmcnt(19)
	s_waitcnt vmcnt(18)
	s_waitcnt vmcnt(17)
	s_waitcnt vmcnt(16)
	s_waitcnt lgkmcnt(0)
	v_pk_fma_f32 v[20:21], v[232:233], v[110:111], 0 op_sel_hi:[0,1,0] neg_lo:[1,0,0] neg_hi:[1,0,0]
	v_pk_fma_f32 v[18:19], v[232:233], v[112:113], 0 op_sel_hi:[0,1,0] neg_lo:[1,0,0] neg_hi:[1,0,0]
	v_cvt_pk_bf16_f32 v20, v20, v21
	v_cvt_pk_bf16_f32 v21, v18, v19
	ds_write_b64 v186, v[20:21]
	v_pk_fma_f32 v[20:21], v[234:235], v[98:99], 0 op_sel_hi:[0,1,0] neg_lo:[1,0,0] neg_hi:[1,0,0]
	v_pk_fma_f32 v[18:19], v[234:235], v[100:101], 0 op_sel_hi:[0,1,0] neg_lo:[1,0,0] neg_hi:[1,0,0]
	v_cvt_pk_bf16_f32 v20, v20, v21
	v_cvt_pk_bf16_f32 v21, v18, v19
	ds_write_b64 v186, v[20:21] offset:544
	v_pk_fma_f32 v[20:21], v[236:237], v[78:79], 0 op_sel_hi:[0,1,0] neg_lo:[1,0,0] neg_hi:[1,0,0]
	v_pk_fma_f32 v[18:19], v[236:237], v[80:81], 0 op_sel_hi:[0,1,0] neg_lo:[1,0,0] neg_hi:[1,0,0]
	v_cvt_pk_bf16_f32 v20, v20, v21
	v_cvt_pk_bf16_f32 v21, v18, v19
	ds_write_b64 v186, v[20:21] offset:1088
	v_pk_fma_f32 v[20:21], v[238:239], v[58:59], 0 op_sel_hi:[0,1,0] neg_lo:[1,0,0] neg_hi:[1,0,0]
	v_pk_fma_f32 v[18:19], v[238:239], v[60:61], 0 op_sel_hi:[0,1,0] neg_lo:[1,0,0] neg_hi:[1,0,0]
	v_cvt_pk_bf16_f32 v20, v20, v21
	v_cvt_pk_bf16_f32 v21, v18, v19
	ds_write_b64 v186, v[20:21] offset:1632
	v_pk_fma_f32 v[20:21], v[240:241], v[34:35], 0 op_sel_hi:[0,1,0] neg_lo:[1,0,0] neg_hi:[1,0,0]
	v_pk_fma_f32 v[18:19], v[240:241], v[36:37], 0 op_sel_hi:[0,1,0] neg_lo:[1,0,0] neg_hi:[1,0,0]
	v_cvt_pk_bf16_f32 v20, v20, v21
	v_cvt_pk_bf16_f32 v21, v18, v19
	ds_write_b64 v186, v[20:21] offset:2176
	v_pk_fma_f32 v[20:21], v[242:243], v[22:23], 0 op_sel_hi:[0,1,0] neg_lo:[1,0,0] neg_hi:[1,0,0]
	v_pk_fma_f32 v[18:19], v[242:243], v[24:25], 0 op_sel_hi:[0,1,0] neg_lo:[1,0,0] neg_hi:[1,0,0]
	v_cvt_pk_bf16_f32 v20, v20, v21
	v_cvt_pk_bf16_f32 v21, v18, v19
	ds_write_b64 v186, v[20:21] offset:2720
	v_pk_fma_f32 v[14:15], v[244:245], v[14:15], 0 op_sel_hi:[0,1,0] neg_lo:[1,0,0] neg_hi:[1,0,0]
	v_pk_fma_f32 v[16:17], v[244:245], v[16:17], 0 op_sel_hi:[0,1,0] neg_lo:[1,0,0] neg_hi:[1,0,0]
	v_cvt_pk_bf16_f32 v14, v14, v15
	v_cvt_pk_bf16_f32 v15, v16, v17
	ds_write_b64 v186, v[14:15] offset:3264
	v_pk_fma_f32 v[6:7], v[246:247], v[6:7], 0 op_sel_hi:[0,1,0] neg_lo:[1,0,0] neg_hi:[1,0,0]
	v_pk_fma_f32 v[8:9], v[246:247], v[8:9], 0 op_sel_hi:[0,1,0] neg_lo:[1,0,0] neg_hi:[1,0,0]
	v_cvt_pk_bf16_f32 v6, v6, v7
	v_cvt_pk_bf16_f32 v7, v8, v9
	ds_write_b64 v186, v[6:7] offset:3808
	ds_read_b32 v232, v187 offset:128
	ds_read_b32 v234, v187 offset:136
	ds_read_b32 v236, v187 offset:144
	ds_read_b32 v238, v187 offset:152
	ds_read_b32 v240, v187 offset:160
	ds_read_b32 v242, v187 offset:168
	ds_read_b32 v244, v187 offset:176
	ds_read_b32 v246, v187 offset:184
	ds_read_b128 a[160:163], v1
	ds_read_b128 a[164:167], v1 offset:64
	ds_read_b128 a[168:171], v1 offset:128
	ds_read_b128 a[172:175], v1 offset:192
	v_lshl_add_u64 v[6:7], v[150:151], 0, s[22:23]
	v_lshl_add_u64 v[18:19], v[160:161], 0, s[22:23]
	v_lshl_add_u64 v[20:21], v[162:163], 0, s[22:23]
	v_lshl_add_u64 v[22:23], v[164:165], 0, s[22:23]
	v_lshl_add_u64 v[8:9], v[152:153], 0, s[22:23]
	v_lshl_add_u64 v[14:15], v[156:157], 0, s[22:23]
	v_lshl_add_u64 v[16:17], v[158:159], 0, s[22:23]
	v_lshl_add_u64 v[34:35], v[166:167], 0, s[22:23]
	global_load_dwordx4 v[110:113], v[6:7], off nt
	global_load_dwordx4 v[98:101], v[8:9], off nt
	global_load_dwordx4 v[78:81], v[14:15], off nt
	global_load_dwordx4 v[66:69], v[16:17], off nt
	global_load_dwordx4 v[58:61], v[18:19], off nt
	global_load_dwordx4 v[30:33], v[20:21], off nt
	s_nop 0
	global_load_dwordx4 v[22:25], v[22:23], off nt
	s_nop 0
	global_load_dwordx4 v[18:21], v[34:35], off nt
	s_waitcnt vmcnt(23)
	s_waitcnt vmcnt(22)
	s_waitcnt vmcnt(21)
	s_waitcnt vmcnt(20)
	s_waitcnt vmcnt(19)
	s_waitcnt vmcnt(18)
	s_waitcnt vmcnt(17)
	s_waitcnt vmcnt(16)
	s_waitcnt lgkmcnt(0)
	v_pk_fma_f32 v[8:9], v[232:233], v[114:115], 0 op_sel_hi:[0,1,0] neg_lo:[1,0,0] neg_hi:[1,0,0]
	v_pk_fma_f32 v[6:7], v[232:233], v[116:117], 0 op_sel_hi:[0,1,0] neg_lo:[1,0,0] neg_hi:[1,0,0]
	v_cvt_pk_bf16_f32 v8, v8, v9
	v_cvt_pk_bf16_f32 v9, v6, v7
	ds_write_b64 v186, v[8:9]
	v_pk_fma_f32 v[8:9], v[234:235], v[94:95], 0 op_sel_hi:[0,1,0] neg_lo:[1,0,0] neg_hi:[1,0,0]
	v_pk_fma_f32 v[6:7], v[234:235], v[96:97], 0 op_sel_hi:[0,1,0] neg_lo:[1,0,0] neg_hi:[1,0,0]
	v_cvt_pk_bf16_f32 v8, v8, v9
	v_cvt_pk_bf16_f32 v9, v6, v7
	ds_write_b64 v186, v[8:9] offset:544
	v_pk_fma_f32 v[8:9], v[236:237], v[82:83], 0 op_sel_hi:[0,1,0] neg_lo:[1,0,0] neg_hi:[1,0,0]
	v_pk_fma_f32 v[6:7], v[236:237], v[84:85], 0 op_sel_hi:[0,1,0] neg_lo:[1,0,0] neg_hi:[1,0,0]
	v_cvt_pk_bf16_f32 v8, v8, v9
	v_cvt_pk_bf16_f32 v9, v6, v7
	ds_write_b64 v186, v[8:9] offset:1088
	v_pk_fma_f32 v[8:9], v[238:239], v[62:63], 0 op_sel_hi:[0,1,0] neg_lo:[1,0,0] neg_hi:[1,0,0]
	v_pk_fma_f32 v[6:7], v[238:239], v[64:65], 0 op_sel_hi:[0,1,0] neg_lo:[1,0,0] neg_hi:[1,0,0]
	v_cvt_pk_bf16_f32 v8, v8, v9
	v_cvt_pk_bf16_f32 v9, v6, v7
	ds_write_b64 v186, v[8:9] offset:1632
	v_pk_fma_f32 v[8:9], v[240:241], v[38:39], 0 op_sel_hi:[0,1,0] neg_lo:[1,0,0] neg_hi:[1,0,0]
	v_pk_fma_f32 v[6:7], v[240:241], v[40:41], 0 op_sel_hi:[0,1,0] neg_lo:[1,0,0] neg_hi:[1,0,0]
	v_cvt_pk_bf16_f32 v8, v8, v9
	v_cvt_pk_bf16_f32 v9, v6, v7
	ds_write_b64 v186, v[8:9] offset:2176
	v_pk_fma_f32 v[8:9], v[242:243], v[26:27], 0 op_sel_hi:[0,1,0] neg_lo:[1,0,0] neg_hi:[1,0,0]
	v_pk_fma_f32 v[6:7], v[242:243], v[28:29], 0 op_sel_hi:[0,1,0] neg_lo:[1,0,0] neg_hi:[1,0,0]
	v_cvt_pk_bf16_f32 v8, v8, v9
	v_cvt_pk_bf16_f32 v9, v6, v7
	ds_write_b64 v186, v[8:9] offset:2720
	v_pk_fma_f32 v[8:9], v[244:245], v[10:11], 0 op_sel_hi:[0,1,0] neg_lo:[1,0,0] neg_hi:[1,0,0]
	v_pk_fma_f32 v[6:7], v[244:245], v[12:13], 0 op_sel_hi:[0,1,0] neg_lo:[1,0,0] neg_hi:[1,0,0]
	v_cvt_pk_bf16_f32 v8, v8, v9
	v_cvt_pk_bf16_f32 v9, v6, v7
	ds_write_b64 v186, v[8:9] offset:3264
	v_pk_fma_f32 v[2:3], v[246:247], v[2:3], 0 op_sel_hi:[0,1,0] neg_lo:[1,0,0] neg_hi:[1,0,0]
	v_pk_fma_f32 v[4:5], v[246:247], v[4:5], 0 op_sel_hi:[0,1,0] neg_lo:[1,0,0] neg_hi:[1,0,0]
	v_cvt_pk_bf16_f32 v2, v2, v3
	v_cvt_pk_bf16_f32 v3, v4, v5
	ds_write_b64 v186, v[2:3] offset:3808
	ds_read_b32 v232, v187 offset:0
	ds_read_b32 v234, v187 offset:8
	ds_read_b32 v236, v187 offset:16
	ds_read_b32 v238, v187 offset:24
	ds_read_b32 v240, v187 offset:32
	ds_read_b32 v242, v187 offset:40
	ds_read_b32 v244, v187 offset:48
	ds_read_b32 v246, v187 offset:56
	ds_read_b128 a[176:179], v1
	ds_read_b128 a[180:183], v1 offset:64
	ds_read_b128 a[184:187], v1 offset:128
	ds_read_b128 a[188:191], v1 offset:192
	v_lshl_add_u64 v[2:3], v[168:169], 0, s[22:23]
	v_lshl_add_u64 v[4:5], v[170:171], 0, s[22:23]
	v_lshl_add_u64 v[6:7], v[172:173], 0, s[22:23]
	v_lshl_add_u64 v[8:9], v[174:175], 0, s[22:23]
	v_lshl_add_u64 v[10:11], v[176:177], 0, s[22:23]
	v_lshl_add_u64 v[12:13], v[178:179], 0, s[22:23]
	v_lshl_add_u64 v[14:15], v[180:181], 0, s[22:23]
	v_lshl_add_u64 v[16:17], v[182:183], 0, s[22:23]
	global_load_dwordx4 v[114:117], v[2:3], off nt
	global_load_dwordx4 v[102:105], v[4:5], off nt
	global_load_dwordx4 v[94:97], v[6:7], off nt
	global_load_dwordx4 v[82:85], v[8:9], off nt
	global_load_dwordx4 v[62:65], v[10:11], off nt
	global_load_dwordx4 v[42:45], v[12:13], off nt
	global_load_dwordx4 v[38:41], v[14:15], off nt
	global_load_dwordx4 v[34:37], v[16:17], off nt
	v_mov_b32_e32 v2, v194
	s_waitcnt vmcnt(23)
	s_waitcnt vmcnt(22)
	s_waitcnt vmcnt(21)
	s_waitcnt vmcnt(20)
	s_waitcnt vmcnt(19)
	s_waitcnt vmcnt(18)
	s_waitcnt vmcnt(17)
	s_waitcnt vmcnt(16)
	s_waitcnt lgkmcnt(0)
	v_pk_fma_f32 v[4:5], v[232:233], v[106:107], 0 op_sel_hi:[0,1,0] neg_lo:[1,0,0] neg_hi:[1,0,0]
	v_pk_fma_f32 v[2:3], v[232:233], v[108:109], 0 op_sel_hi:[0,1,0] neg_lo:[1,0,0] neg_hi:[1,0,0]
	v_cvt_pk_bf16_f32 v4, v4, v5
	v_cvt_pk_bf16_f32 v5, v2, v3
	ds_write_b64 v186, v[4:5]
	v_pk_fma_f32 v[4:5], v[234:235], v[90:91], 0 op_sel_hi:[0,1,0] neg_lo:[1,0,0] neg_hi:[1,0,0]
	v_pk_fma_f32 v[2:3], v[234:235], v[92:93], 0 op_sel_hi:[0,1,0] neg_lo:[1,0,0] neg_hi:[1,0,0]
	v_cvt_pk_bf16_f32 v4, v4, v5
	v_cvt_pk_bf16_f32 v5, v2, v3
	ds_write_b64 v186, v[4:5] offset:544
	v_pk_fma_f32 v[4:5], v[236:237], v[86:87], 0 op_sel_hi:[0,1,0] neg_lo:[1,0,0] neg_hi:[1,0,0]
	v_pk_fma_f32 v[2:3], v[236:237], v[88:89], 0 op_sel_hi:[0,1,0] neg_lo:[1,0,0] neg_hi:[1,0,0]
	v_cvt_pk_bf16_f32 v4, v4, v5
	v_cvt_pk_bf16_f32 v5, v2, v3
	ds_write_b64 v186, v[4:5] offset:1088
	v_pk_fma_f32 v[4:5], v[238:239], v[74:75], 0 op_sel_hi:[0,1,0] neg_lo:[1,0,0] neg_hi:[1,0,0]
	v_pk_fma_f32 v[2:3], v[238:239], v[76:77], 0 op_sel_hi:[0,1,0] neg_lo:[1,0,0] neg_hi:[1,0,0]
	v_cvt_pk_bf16_f32 v4, v4, v5
	v_cvt_pk_bf16_f32 v5, v2, v3
	ds_write_b64 v186, v[4:5] offset:1632
	v_pk_fma_f32 v[4:5], v[240:241], v[70:71], 0 op_sel_hi:[0,1,0] neg_lo:[1,0,0] neg_hi:[1,0,0]
	v_pk_fma_f32 v[2:3], v[240:241], v[72:73], 0 op_sel_hi:[0,1,0] neg_lo:[1,0,0] neg_hi:[1,0,0]
	v_cvt_pk_bf16_f32 v4, v4, v5
	v_cvt_pk_bf16_f32 v5, v2, v3
	ds_write_b64 v186, v[4:5] offset:2176
	v_pk_fma_f32 v[4:5], v[242:243], v[54:55], 0 op_sel_hi:[0,1,0] neg_lo:[1,0,0] neg_hi:[1,0,0]
	v_pk_fma_f32 v[2:3], v[242:243], v[56:57], 0 op_sel_hi:[0,1,0] neg_lo:[1,0,0] neg_hi:[1,0,0]
	v_cvt_pk_bf16_f32 v4, v4, v5
	v_cvt_pk_bf16_f32 v5, v2, v3
	ds_write_b64 v186, v[4:5] offset:2720
	v_pk_fma_f32 v[4:5], v[244:245], v[50:51], 0 op_sel_hi:[0,1,0] neg_lo:[1,0,0] neg_hi:[1,0,0]
	v_pk_fma_f32 v[2:3], v[244:245], v[52:53], 0 op_sel_hi:[0,1,0] neg_lo:[1,0,0] neg_hi:[1,0,0]
	v_cvt_pk_bf16_f32 v4, v4, v5
	v_cvt_pk_bf16_f32 v5, v2, v3
	ds_write_b64 v186, v[4:5] offset:3264
	v_pk_fma_f32 v[4:5], v[246:247], v[46:47], 0 op_sel_hi:[0,1,0] neg_lo:[1,0,0] neg_hi:[1,0,0]
	v_pk_fma_f32 v[2:3], v[246:247], v[48:49], 0 op_sel_hi:[0,1,0] neg_lo:[1,0,0] neg_hi:[1,0,0]
	v_cvt_pk_bf16_f32 v4, v4, v5
	v_cvt_pk_bf16_f32 v5, v2, v3
	ds_write_b64 v186, v[4:5] offset:3808
	ds_read_b32 v232, v187 offset:64
	ds_read_b32 v234, v187 offset:72
	ds_read_b32 v236, v187 offset:80
	ds_read_b32 v238, v187 offset:88
	ds_read_b32 v240, v187 offset:96
	ds_read_b32 v242, v187 offset:104
	ds_read_b32 v244, v187 offset:112
	ds_read_b32 v246, v187 offset:120
	ds_read_b128 a[192:195], v1
	ds_read_b128 a[196:199], v1 offset:64
	ds_read_b128 a[200:203], v1 offset:128
	ds_read_b128 a[204:207], v1 offset:192
	v_lshl_add_u64 v[118:119], v[130:131], 0, s[20:21]
	v_add_co_u32_e32 v126, vcc, s7, v118
	s_nop 1
	v_addc_co_u32_e32 v127, vcc, 0, v119, vcc
	v_add_co_u32_e32 v128, vcc, s36, v118
	global_load_dwordx4 v[90:93], v[118:119], off nt
	global_load_dwordx4 v[86:89], v[126:127], off nt
	v_addc_co_u32_e32 v129, vcc, 0, v119, vcc
	v_add_co_u32_e32 v134, vcc, s37, v118
	s_nop 1
	v_addc_co_u32_e32 v135, vcc, 0, v119, vcc
	v_add_co_u32_e32 v136, vcc, s38, v118
	global_load_dwordx4 v[54:57], v[128:129], off nt
	global_load_dwordx4 v[50:53], v[134:135], off nt
	v_addc_co_u32_e32 v137, vcc, 0, v119, vcc
	v_add_co_u32_e32 v138, vcc, s39, v118
	s_nop 1
	v_addc_co_u32_e32 v139, vcc, 0, v119, vcc
	v_add_co_u32_e32 v140, vcc, s41, v118
	global_load_dwordx4 v[14:17], v[136:137], off nt
	global_load_dwordx4 v[10:13], v[138:139], off nt
	v_addc_co_u32_e32 v141, vcc, 0, v119, vcc
	v_add_co_u32_e32 v142, vcc, s42, v118
	s_nop 1
	v_addc_co_u32_e32 v143, vcc, 0, v119, vcc
	global_load_dwordx4 v[6:9], v[140:141], off nt
	global_load_dwordx4 v[2:5], v[142:143], off nt
	v_mov_b32_e32 v26, v194
	s_waitcnt vmcnt(23)
	s_waitcnt vmcnt(22)
	s_waitcnt vmcnt(21)
	s_waitcnt vmcnt(20)
	s_waitcnt vmcnt(19)
	s_waitcnt vmcnt(18)
	s_waitcnt vmcnt(17)
	s_waitcnt vmcnt(16)
	s_waitcnt lgkmcnt(0)
	v_pk_fma_f32 v[28:29], v[232:233], v[110:111], 0 op_sel_hi:[0,1,0] neg_lo:[1,0,0] neg_hi:[1,0,0]
	v_pk_fma_f32 v[26:27], v[232:233], v[112:113], 0 op_sel_hi:[0,1,0] neg_lo:[1,0,0] neg_hi:[1,0,0]
	v_cvt_pk_bf16_f32 v28, v28, v29
	v_cvt_pk_bf16_f32 v29, v26, v27
	ds_write_b64 v186, v[28:29]
	v_pk_fma_f32 v[28:29], v[234:235], v[98:99], 0 op_sel_hi:[0,1,0] neg_lo:[1,0,0] neg_hi:[1,0,0]
	v_pk_fma_f32 v[26:27], v[234:235], v[100:101], 0 op_sel_hi:[0,1,0] neg_lo:[1,0,0] neg_hi:[1,0,0]
	v_cvt_pk_bf16_f32 v28, v28, v29
	v_cvt_pk_bf16_f32 v29, v26, v27
	ds_write_b64 v186, v[28:29] offset:544
	v_pk_fma_f32 v[28:29], v[236:237], v[78:79], 0 op_sel_hi:[0,1,0] neg_lo:[1,0,0] neg_hi:[1,0,0]
	v_pk_fma_f32 v[26:27], v[236:237], v[80:81], 0 op_sel_hi:[0,1,0] neg_lo:[1,0,0] neg_hi:[1,0,0]
	v_cvt_pk_bf16_f32 v28, v28, v29
	v_cvt_pk_bf16_f32 v29, v26, v27
	ds_write_b64 v186, v[28:29] offset:1088
	v_pk_fma_f32 v[28:29], v[238:239], v[66:67], 0 op_sel_hi:[0,1,0] neg_lo:[1,0,0] neg_hi:[1,0,0]
	v_pk_fma_f32 v[26:27], v[238:239], v[68:69], 0 op_sel_hi:[0,1,0] neg_lo:[1,0,0] neg_hi:[1,0,0]
	v_cvt_pk_bf16_f32 v28, v28, v29
	v_cvt_pk_bf16_f32 v29, v26, v27
	ds_write_b64 v186, v[28:29] offset:1632
	v_pk_fma_f32 v[28:29], v[240:241], v[58:59], 0 op_sel_hi:[0,1,0] neg_lo:[1,0,0] neg_hi:[1,0,0]
	v_pk_fma_f32 v[26:27], v[240:241], v[60:61], 0 op_sel_hi:[0,1,0] neg_lo:[1,0,0] neg_hi:[1,0,0]
	v_cvt_pk_bf16_f32 v28, v28, v29
	v_cvt_pk_bf16_f32 v29, v26, v27
	ds_write_b64 v186, v[28:29] offset:2176
	v_pk_fma_f32 v[28:29], v[242:243], v[30:31], 0 op_sel_hi:[0,1,0] neg_lo:[1,0,0] neg_hi:[1,0,0]
	v_pk_fma_f32 v[26:27], v[242:243], v[32:33], 0 op_sel_hi:[0,1,0] neg_lo:[1,0,0] neg_hi:[1,0,0]
	v_cvt_pk_bf16_f32 v28, v28, v29
	v_cvt_pk_bf16_f32 v29, v26, v27
	ds_write_b64 v186, v[28:29] offset:2720
	v_pk_fma_f32 v[22:23], v[244:245], v[22:23], 0 op_sel_hi:[0,1,0] neg_lo:[1,0,0] neg_hi:[1,0,0]
	v_pk_fma_f32 v[24:25], v[244:245], v[24:25], 0 op_sel_hi:[0,1,0] neg_lo:[1,0,0] neg_hi:[1,0,0]
	v_cvt_pk_bf16_f32 v22, v22, v23
	v_cvt_pk_bf16_f32 v23, v24, v25
	ds_write_b64 v186, v[22:23] offset:3264
	v_pk_fma_f32 v[18:19], v[246:247], v[18:19], 0 op_sel_hi:[0,1,0] neg_lo:[1,0,0] neg_hi:[1,0,0]
	v_pk_fma_f32 v[20:21], v[246:247], v[20:21], 0 op_sel_hi:[0,1,0] neg_lo:[1,0,0] neg_hi:[1,0,0]
	v_cvt_pk_bf16_f32 v18, v18, v19
	v_cvt_pk_bf16_f32 v19, v20, v21
	ds_write_b64 v186, v[18:19] offset:3808
	ds_read_b32 v232, v187 offset:128
	ds_read_b32 v234, v187 offset:136
	ds_read_b32 v236, v187 offset:144
	ds_read_b32 v238, v187 offset:152
	ds_read_b32 v240, v187 offset:160
	ds_read_b32 v242, v187 offset:168
	ds_read_b32 v244, v187 offset:176
	ds_read_b32 v246, v187 offset:184
	ds_read_b128 a[208:211], v1
	ds_read_b128 a[212:215], v1 offset:64
	ds_read_b128 a[216:219], v1 offset:128
	ds_read_b128 a[220:223], v1 offset:192
	v_lshl_add_u64 v[18:19], v[150:151], 0, s[20:21]
	v_lshl_add_u64 v[20:21], v[152:153], 0, s[20:21]
	v_lshl_add_u64 v[22:23], v[156:157], 0, s[20:21]
	v_lshl_add_u64 v[24:25], v[158:159], 0, s[20:21]
	v_lshl_add_u64 v[26:27], v[160:161], 0, s[20:21]
	v_lshl_add_u64 v[28:29], v[162:163], 0, s[20:21]
	v_lshl_add_u64 v[46:47], v[164:165], 0, s[20:21]
	v_lshl_add_u64 v[48:49], v[166:167], 0, s[20:21]
	global_load_dwordx4 v[78:81], v[18:19], off nt
	global_load_dwordx4 v[74:77], v[20:21], off nt
	global_load_dwordx4 v[70:73], v[22:23], off nt
	global_load_dwordx4 v[66:69], v[24:25], off nt
	global_load_dwordx4 v[30:33], v[26:27], off nt
	s_nop 0
	global_load_dwordx4 v[26:29], v[28:29], off nt
	s_nop 0
	global_load_dwordx4 v[22:25], v[46:47], off nt
	global_load_dwordx4 v[18:21], v[48:49], off nt
	s_waitcnt vmcnt(23)
	s_waitcnt vmcnt(22)
	s_waitcnt vmcnt(21)
	s_waitcnt vmcnt(20)
	s_waitcnt vmcnt(19)
	s_waitcnt vmcnt(18)
	s_waitcnt vmcnt(17)
	s_waitcnt vmcnt(16)
	s_waitcnt lgkmcnt(0)
	v_pk_fma_f32 v[48:49], v[232:233], v[114:115], 0 op_sel_hi:[0,1,0] neg_lo:[1,0,0] neg_hi:[1,0,0]
	v_pk_fma_f32 v[46:47], v[232:233], v[116:117], 0 op_sel_hi:[0,1,0] neg_lo:[1,0,0] neg_hi:[1,0,0]
	v_cvt_pk_bf16_f32 v48, v48, v49
	v_cvt_pk_bf16_f32 v49, v46, v47
	ds_write_b64 v186, v[48:49]
	v_pk_fma_f32 v[48:49], v[234:235], v[102:103], 0 op_sel_hi:[0,1,0] neg_lo:[1,0,0] neg_hi:[1,0,0]
	v_pk_fma_f32 v[46:47], v[234:235], v[104:105], 0 op_sel_hi:[0,1,0] neg_lo:[1,0,0] neg_hi:[1,0,0]
	v_cvt_pk_bf16_f32 v48, v48, v49
	v_cvt_pk_bf16_f32 v49, v46, v47
	ds_write_b64 v186, v[48:49] offset:544
	v_pk_fma_f32 v[48:49], v[236:237], v[94:95], 0 op_sel_hi:[0,1,0] neg_lo:[1,0,0] neg_hi:[1,0,0]
	v_pk_fma_f32 v[46:47], v[236:237], v[96:97], 0 op_sel_hi:[0,1,0] neg_lo:[1,0,0] neg_hi:[1,0,0]
	v_cvt_pk_bf16_f32 v48, v48, v49
	v_cvt_pk_bf16_f32 v49, v46, v47
	ds_write_b64 v186, v[48:49] offset:1088
	v_pk_fma_f32 v[48:49], v[238:239], v[82:83], 0 op_sel_hi:[0,1,0] neg_lo:[1,0,0] neg_hi:[1,0,0]
	v_pk_fma_f32 v[46:47], v[238:239], v[84:85], 0 op_sel_hi:[0,1,0] neg_lo:[1,0,0] neg_hi:[1,0,0]
	v_cvt_pk_bf16_f32 v48, v48, v49
	v_cvt_pk_bf16_f32 v49, v46, v47
	ds_write_b64 v186, v[48:49] offset:1632
	v_pk_fma_f32 v[48:49], v[240:241], v[62:63], 0 op_sel_hi:[0,1,0] neg_lo:[1,0,0] neg_hi:[1,0,0]
	v_pk_fma_f32 v[46:47], v[240:241], v[64:65], 0 op_sel_hi:[0,1,0] neg_lo:[1,0,0] neg_hi:[1,0,0]
	v_cvt_pk_bf16_f32 v48, v48, v49
	v_cvt_pk_bf16_f32 v49, v46, v47
	ds_write_b64 v186, v[48:49] offset:2176
	v_pk_fma_f32 v[42:43], v[242:243], v[42:43], 0 op_sel_hi:[0,1,0] neg_lo:[1,0,0] neg_hi:[1,0,0]
	v_pk_fma_f32 v[44:45], v[242:243], v[44:45], 0 op_sel_hi:[0,1,0] neg_lo:[1,0,0] neg_hi:[1,0,0]
	v_cvt_pk_bf16_f32 v42, v42, v43
	v_cvt_pk_bf16_f32 v43, v44, v45
	ds_write_b64 v186, v[42:43] offset:2720
	v_pk_fma_f32 v[38:39], v[244:245], v[38:39], 0 op_sel_hi:[0,1,0] neg_lo:[1,0,0] neg_hi:[1,0,0]
	v_pk_fma_f32 v[40:41], v[244:245], v[40:41], 0 op_sel_hi:[0,1,0] neg_lo:[1,0,0] neg_hi:[1,0,0]
	v_cvt_pk_bf16_f32 v38, v38, v39
	v_cvt_pk_bf16_f32 v39, v40, v41
	ds_write_b64 v186, v[38:39] offset:3264
	v_pk_fma_f32 v[34:35], v[246:247], v[34:35], 0 op_sel_hi:[0,1,0] neg_lo:[1,0,0] neg_hi:[1,0,0]
	v_pk_fma_f32 v[36:37], v[246:247], v[36:37], 0 op_sel_hi:[0,1,0] neg_lo:[1,0,0] neg_hi:[1,0,0]
	v_cvt_pk_bf16_f32 v34, v34, v35
	v_cvt_pk_bf16_f32 v35, v36, v37
	ds_write_b64 v186, v[34:35] offset:3808
	ds_read_b32 v232, v187 offset:0
	ds_read_b32 v234, v187 offset:8
	ds_read_b32 v236, v187 offset:16
	ds_read_b32 v238, v187 offset:24
	ds_read_b32 v240, v187 offset:32
	ds_read_b32 v242, v187 offset:40
	ds_read_b32 v244, v187 offset:48
	ds_read_b32 v246, v187 offset:56
	ds_read_b128 a[224:227], v1
	ds_read_b128 a[228:231], v1 offset:64
	ds_read_b128 a[232:235], v1 offset:128
	ds_read_b128 a[236:239], v1 offset:192
	v_lshl_add_u64 v[34:35], v[168:169], 0, s[20:21]
	v_lshl_add_u64 v[36:37], v[170:171], 0, s[20:21]
	v_lshl_add_u64 v[38:39], v[172:173], 0, s[20:21]
	v_lshl_add_u64 v[40:41], v[174:175], 0, s[20:21]
	v_lshl_add_u64 v[42:43], v[176:177], 0, s[20:21]
	v_lshl_add_u64 v[44:45], v[178:179], 0, s[20:21]
	v_lshl_add_u64 v[58:59], v[180:181], 0, s[20:21]
	v_lshl_add_u64 v[60:61], v[182:183], 0, s[20:21]
	global_load_dwordx4 v[122:125], v[34:35], off nt
	global_load_dwordx4 v[106:109], v[36:37], off nt
	global_load_dwordx4 v[94:97], v[38:39], off nt
	global_load_dwordx4 v[82:85], v[40:41], off nt
	global_load_dwordx4 v[46:49], v[42:43], off nt
	s_nop 0
	global_load_dwordx4 v[42:45], v[44:45], off nt
	s_nop 0
	global_load_dwordx4 v[38:41], v[58:59], off nt
	global_load_dwordx4 v[34:37], v[60:61], off nt
	v_mov_b32_e32 v98, v133
	s_waitcnt vmcnt(23)
	s_waitcnt vmcnt(22)
	s_waitcnt vmcnt(21)
	s_waitcnt vmcnt(20)
	s_waitcnt vmcnt(19)
	s_waitcnt vmcnt(18)
	s_waitcnt vmcnt(17)
	s_waitcnt vmcnt(16)
	v_add_u32_e32 v99, 1, v98
	v_cmp_eq_u32_e32 vcc, v98, v132
	s_nop 1
	v_cndmask_b32_e64 v60, 0, 1.0, vcc
	v_cmp_eq_u32_e32 vcc, v99, v132
	s_nop 1
	v_cndmask_b32_e64 v61, 0, 1.0, vcc
	s_waitcnt lgkmcnt(0)
	v_pk_fma_f32 v[62:63], v[232:233], v[90:91], v[60:61] op_sel_hi:[0,1,1] neg_lo:[1,0,0] neg_hi:[1,0,0]
	v_add_u32_e32 v90, 3, v98
	v_add_u32_e32 v91, 2, v98
	v_cmp_eq_u32_e32 vcc, v90, v132
	v_cvt_pk_bf16_f32 v62, v62, v63
	s_nop 0
	v_cndmask_b32_e64 v65, 0, 1.0, vcc
	v_cmp_eq_u32_e32 vcc, v91, v132
	s_nop 1
	v_cndmask_b32_e64 v64, 0, 1.0, vcc
	v_pk_fma_f32 v[58:59], v[232:233], v[92:93], v[64:65] op_sel_hi:[0,1,1] neg_lo:[1,0,0] neg_hi:[1,0,0]
	v_cvt_pk_bf16_f32 v63, v58, v59
	ds_write_b64 v186, v[62:63]
	v_cmp_eq_u32_e32 vcc, v98, v193
	s_nop 1
	v_cndmask_b32_e64 v62, 0, 1.0, vcc
	v_cmp_eq_u32_e32 vcc, v99, v193
	s_nop 1
	v_cndmask_b32_e64 v63, 0, 1.0, vcc
	v_cmp_eq_u32_e32 vcc, v90, v193
	v_pk_fma_f32 v[62:63], v[234:235], v[86:87], v[62:63] op_sel_hi:[0,1,1] neg_lo:[1,0,0] neg_hi:[1,0,0]
	v_cvt_pk_bf16_f32 v62, v62, v63
	v_cndmask_b32_e64 v61, 0, 1.0, vcc
	v_pk_fma_f32 v[58:59], v[234:235], v[88:89], v[60:61] op_sel_hi:[0,1,1] neg_lo:[1,0,0] neg_hi:[1,0,0]
	v_cvt_pk_bf16_f32 v63, v58, v59
	ds_write_b64 v186, v[62:63] offset:544
	v_cmp_eq_u32_e32 vcc, v98, v192
	s_nop 1
	v_cndmask_b32_e64 v60, 0, 1.0, vcc
	v_cmp_eq_u32_e32 vcc, v99, v192
	s_nop 1
	v_cndmask_b32_e64 v61, 0, 1.0, vcc
	v_cmp_eq_u32_e32 vcc, v90, v192
	v_pk_fma_f32 v[54:55], v[236:237], v[54:55], v[60:61] op_sel_hi:[0,1,1] neg_lo:[1,0,0] neg_hi:[1,0,0]
	v_cvt_pk_bf16_f32 v54, v54, v55
	v_cndmask_b32_e64 v61, 0, 1.0, vcc
	v_cmp_eq_u32_e32 vcc, v91, v192
	s_nop 1
	v_cndmask_b32_e64 v60, 0, 1.0, vcc
	v_pk_fma_f32 v[56:57], v[236:237], v[56:57], v[60:61] op_sel_hi:[0,1,1] neg_lo:[1,0,0] neg_hi:[1,0,0]
	v_cvt_pk_bf16_f32 v55, v56, v57
	ds_write_b64 v186, v[54:55] offset:1088
	v_cmp_eq_u32_e32 vcc, v98, v190
	s_nop 1
	v_cndmask_b32_e64 v56, 0, 1.0, vcc
	v_cmp_eq_u32_e32 vcc, v99, v190
	s_nop 1
	v_cndmask_b32_e64 v57, 0, 1.0, vcc
	v_cmp_eq_u32_e32 vcc, v90, v190
	v_pk_fma_f32 v[50:51], v[238:239], v[50:51], v[56:57] op_sel_hi:[0,1,1] neg_lo:[1,0,0] neg_hi:[1,0,0]
	v_cvt_pk_bf16_f32 v50, v50, v51
	v_cndmask_b32_e64 v57, 0, 1.0, vcc
	v_cmp_eq_u32_e32 vcc, v91, v190
	s_nop 1
	v_cndmask_b32_e64 v56, 0, 1.0, vcc
	v_pk_fma_f32 v[52:53], v[238:239], v[52:53], v[56:57] op_sel_hi:[0,1,1] neg_lo:[1,0,0] neg_hi:[1,0,0]
	v_cvt_pk_bf16_f32 v51, v52, v53
	ds_write_b64 v186, v[50:51] offset:1632
	v_cmp_eq_u32_e32 vcc, v98, v149
	s_nop 1
	v_cndmask_b32_e64 v52, 0, 1.0, vcc
	v_cmp_eq_u32_e32 vcc, v99, v149
	s_nop 1
	v_cndmask_b32_e64 v53, 0, 1.0, vcc
	v_cmp_eq_u32_e32 vcc, v90, v149
	v_pk_fma_f32 v[14:15], v[240:241], v[14:15], v[52:53] op_sel_hi:[0,1,1] neg_lo:[1,0,0] neg_hi:[1,0,0]
	v_cvt_pk_bf16_f32 v14, v14, v15
	v_cndmask_b32_e64 v53, 0, 1.0, vcc
	v_cmp_eq_u32_e32 vcc, v91, v149
	s_nop 1
	v_cndmask_b32_e64 v52, 0, 1.0, vcc
	v_pk_fma_f32 v[16:17], v[240:241], v[16:17], v[52:53] op_sel_hi:[0,1,1] neg_lo:[1,0,0] neg_hi:[1,0,0]
	v_cvt_pk_bf16_f32 v15, v16, v17
	ds_write_b64 v186, v[14:15] offset:2176
	v_cmp_eq_u32_e32 vcc, v98, v148
	s_nop 1
	v_cndmask_b32_e64 v16, 0, 1.0, vcc
	v_cmp_eq_u32_e32 vcc, v99, v148
	s_nop 1
	v_cndmask_b32_e64 v17, 0, 1.0, vcc
	v_cmp_eq_u32_e32 vcc, v90, v148
	v_pk_fma_f32 v[10:11], v[242:243], v[10:11], v[16:17] op_sel_hi:[0,1,1] neg_lo:[1,0,0] neg_hi:[1,0,0]
	v_cvt_pk_bf16_f32 v10, v10, v11
	v_cndmask_b32_e64 v17, 0, 1.0, vcc
	v_cmp_eq_u32_e32 vcc, v91, v148
	s_nop 1
	v_cndmask_b32_e64 v16, 0, 1.0, vcc
	v_pk_fma_f32 v[12:13], v[242:243], v[12:13], v[16:17] op_sel_hi:[0,1,1] neg_lo:[1,0,0] neg_hi:[1,0,0]
	v_cvt_pk_bf16_f32 v11, v12, v13
	ds_write_b64 v186, v[10:11] offset:2720
	v_cmp_eq_u32_e32 vcc, v98, v147
	s_nop 1
	v_cndmask_b32_e64 v12, 0, 1.0, vcc
	v_cmp_eq_u32_e32 vcc, v99, v147
	s_nop 1
	v_cndmask_b32_e64 v13, 0, 1.0, vcc
	v_cmp_eq_u32_e32 vcc, v90, v147
	v_pk_fma_f32 v[6:7], v[244:245], v[6:7], v[12:13] op_sel_hi:[0,1,1] neg_lo:[1,0,0] neg_hi:[1,0,0]
	v_cvt_pk_bf16_f32 v6, v6, v7
	v_cndmask_b32_e64 v13, 0, 1.0, vcc
	v_cmp_eq_u32_e32 vcc, v91, v147
	s_nop 1
	v_cndmask_b32_e64 v12, 0, 1.0, vcc
	v_pk_fma_f32 v[8:9], v[244:245], v[8:9], v[12:13] op_sel_hi:[0,1,1] neg_lo:[1,0,0] neg_hi:[1,0,0]
	v_cvt_pk_bf16_f32 v7, v8, v9
	ds_write_b64 v186, v[6:7] offset:3264
	v_cmp_eq_u32_e32 vcc, v98, v146
	s_nop 1
	v_cndmask_b32_e64 v8, 0, 1.0, vcc
	v_cmp_eq_u32_e32 vcc, v99, v146
	s_nop 1
	v_cndmask_b32_e64 v9, 0, 1.0, vcc
	v_cmp_eq_u32_e32 vcc, v90, v146
	v_pk_fma_f32 v[2:3], v[246:247], v[2:3], v[8:9] op_sel_hi:[0,1,1] neg_lo:[1,0,0] neg_hi:[1,0,0]
	v_cvt_pk_bf16_f32 v2, v2, v3
	v_cndmask_b32_e64 v9, 0, 1.0, vcc
	v_cmp_eq_u32_e32 vcc, v91, v146
	s_nop 1
	v_cndmask_b32_e64 v8, 0, 1.0, vcc
	v_pk_fma_f32 v[4:5], v[246:247], v[4:5], v[8:9] op_sel_hi:[0,1,1] neg_lo:[1,0,0] neg_hi:[1,0,0]
	v_cvt_pk_bf16_f32 v3, v4, v5
	ds_write_b64 v186, v[2:3] offset:3808
	ds_read_b32 v232, v187 offset:64
	ds_read_b32 v234, v187 offset:72
	ds_read_b32 v236, v187 offset:80
	ds_read_b32 v238, v187 offset:88
	ds_read_b32 v240, v187 offset:96
	ds_read_b32 v242, v187 offset:104
	ds_read_b32 v244, v187 offset:112
	ds_read_b32 v246, v187 offset:120
	ds_read_b128 v[2:5], v1
	ds_read_b128 v[6:9], v1 offset:64
	ds_read_b128 v[10:13], v1 offset:128
	ds_read_b128 v[14:17], v1 offset:192
	global_load_dwordx4 v[118:121], v[118:119], off offset:512 nt
	s_nop 0
	global_load_dwordx4 v[110:113], v[126:127], off offset:512 nt
	global_load_dwordx4 v[98:101], v[128:129], off offset:512 nt
	global_load_dwordx4 v[86:89], v[134:135], off offset:512 nt
	global_load_dwordx4 v[62:65], v[136:137], off offset:512 nt
	global_load_dwordx4 v[58:61], v[138:139], off offset:512 nt
	global_load_dwordx4 v[54:57], v[140:141], off offset:512 nt
	global_load_dwordx4 v[50:53], v[142:143], off offset:512 nt
	v_mov_b32_e32 v91, v133
	s_waitcnt vmcnt(23)
	s_waitcnt vmcnt(22)
	s_waitcnt vmcnt(21)
	s_waitcnt vmcnt(20)
	s_waitcnt vmcnt(19)
	s_waitcnt vmcnt(18)
	s_waitcnt vmcnt(17)
	s_waitcnt vmcnt(16)
	v_or_b32_e32 v138, 16, v132
	v_add_u32_e32 v102, 1, v91
	v_cmp_eq_u32_e32 vcc, v91, v138
	v_add_u32_e32 v103, 3, v91
	v_add_u32_e32 v104, 2, v91
	v_cndmask_b32_e64 v92, 0, 1.0, vcc
	v_cmp_eq_u32_e32 vcc, v102, v138
	v_or_b32_e32 v139, 18, v132
	v_or_b32_e32 v140, 20, v132
	v_cndmask_b32_e64 v93, 0, 1.0, vcc
	v_cmp_eq_u32_e32 vcc, v103, v138
	s_waitcnt lgkmcnt(0)
	v_pk_fma_f32 v[78:79], v[232:233], v[78:79], v[92:93] op_sel_hi:[0,1,1] neg_lo:[1,0,0] neg_hi:[1,0,0]
	v_cvt_pk_bf16_f32 v78, v78, v79
	v_cndmask_b32_e64 v93, 0, 1.0, vcc
	v_cmp_eq_u32_e32 vcc, v104, v138
	v_or_b32_e32 v141, 22, v132
	v_or_b32_e32 v142, 24, v132
	v_cndmask_b32_e64 v92, 0, 1.0, vcc
	v_pk_fma_f32 v[80:81], v[232:233], v[80:81], v[92:93] op_sel_hi:[0,1,1] neg_lo:[1,0,0] neg_hi:[1,0,0]
	v_cvt_pk_bf16_f32 v79, v80, v81
	ds_write_b64 v186, v[78:79]
	v_cmp_eq_u32_e32 vcc, v91, v139
	v_or_b32_e32 v143, 26, v132
	v_or_b32_e32 v144, 28, v132
	v_cndmask_b32_e64 v80, 0, 1.0, vcc
	v_cmp_eq_u32_e32 vcc, v102, v139
	v_or_b32_e32 v145, 30, v132
	s_nop 0
	v_cndmask_b32_e64 v81, 0, 1.0, vcc
	v_cmp_eq_u32_e32 vcc, v103, v139
	v_pk_fma_f32 v[74:75], v[234:235], v[74:75], v[80:81] op_sel_hi:[0,1,1] neg_lo:[1,0,0] neg_hi:[1,0,0]
	v_cvt_pk_bf16_f32 v74, v74, v75
	v_cndmask_b32_e64 v81, 0, 1.0, vcc
	v_cmp_eq_u32_e32 vcc, v104, v139
	s_nop 1
	v_cndmask_b32_e64 v80, 0, 1.0, vcc
	v_pk_fma_f32 v[76:77], v[234:235], v[76:77], v[80:81] op_sel_hi:[0,1,1] neg_lo:[1,0,0] neg_hi:[1,0,0]
	v_cvt_pk_bf16_f32 v75, v76, v77
	ds_write_b64 v186, v[74:75] offset:544
	v_cmp_eq_u32_e32 vcc, v91, v140
	s_nop 1
	v_cndmask_b32_e64 v76, 0, 1.0, vcc
	v_cmp_eq_u32_e32 vcc, v102, v140
	s_nop 1
	v_cndmask_b32_e64 v77, 0, 1.0, vcc
	v_cmp_eq_u32_e32 vcc, v103, v140
	v_pk_fma_f32 v[70:71], v[236:237], v[70:71], v[76:77] op_sel_hi:[0,1,1] neg_lo:[1,0,0] neg_hi:[1,0,0]
	v_cvt_pk_bf16_f32 v70, v70, v71
	v_cndmask_b32_e64 v77, 0, 1.0, vcc
	v_cmp_eq_u32_e32 vcc, v104, v140
	s_nop 1
	v_cndmask_b32_e64 v76, 0, 1.0, vcc
	v_pk_fma_f32 v[72:73], v[236:237], v[72:73], v[76:77] op_sel_hi:[0,1,1] neg_lo:[1,0,0] neg_hi:[1,0,0]
	v_cvt_pk_bf16_f32 v71, v72, v73
	ds_write_b64 v186, v[70:71] offset:1088
	v_cmp_eq_u32_e32 vcc, v91, v141
	s_nop 1
	v_cndmask_b32_e64 v72, 0, 1.0, vcc
	v_cmp_eq_u32_e32 vcc, v102, v141
	s_nop 1
	v_cndmask_b32_e64 v73, 0, 1.0, vcc
	v_cmp_eq_u32_e32 vcc, v103, v141
	v_pk_fma_f32 v[66:67], v[238:239], v[66:67], v[72:73] op_sel_hi:[0,1,1] neg_lo:[1,0,0] neg_hi:[1,0,0]
	v_cvt_pk_bf16_f32 v66, v66, v67
	v_cndmask_b32_e64 v73, 0, 1.0, vcc
	v_cmp_eq_u32_e32 vcc, v104, v141
	s_nop 1
	v_cndmask_b32_e64 v72, 0, 1.0, vcc
	v_pk_fma_f32 v[68:69], v[238:239], v[68:69], v[72:73] op_sel_hi:[0,1,1] neg_lo:[1,0,0] neg_hi:[1,0,0]
	v_cvt_pk_bf16_f32 v67, v68, v69
	ds_write_b64 v186, v[66:67] offset:1632
	v_cmp_eq_u32_e32 vcc, v91, v142
	s_nop 1
	v_cndmask_b32_e64 v68, 0, 1.0, vcc
	v_cmp_eq_u32_e32 vcc, v102, v142
	s_nop 1
	v_cndmask_b32_e64 v69, 0, 1.0, vcc
	v_cmp_eq_u32_e32 vcc, v103, v142
	v_pk_fma_f32 v[30:31], v[240:241], v[30:31], v[68:69] op_sel_hi:[0,1,1] neg_lo:[1,0,0] neg_hi:[1,0,0]
	v_cvt_pk_bf16_f32 v30, v30, v31
	v_cndmask_b32_e64 v69, 0, 1.0, vcc
	v_cmp_eq_u32_e32 vcc, v104, v142
	s_nop 1
	v_cndmask_b32_e64 v68, 0, 1.0, vcc
	v_pk_fma_f32 v[32:33], v[240:241], v[32:33], v[68:69] op_sel_hi:[0,1,1] neg_lo:[1,0,0] neg_hi:[1,0,0]
	v_cvt_pk_bf16_f32 v31, v32, v33
	ds_write_b64 v186, v[30:31] offset:2176
	v_cmp_eq_u32_e32 vcc, v91, v143
	s_nop 1
	v_cndmask_b32_e64 v32, 0, 1.0, vcc
	v_cmp_eq_u32_e32 vcc, v102, v143
	s_nop 1
	v_cndmask_b32_e64 v33, 0, 1.0, vcc
	v_cmp_eq_u32_e32 vcc, v103, v143
	v_pk_fma_f32 v[26:27], v[242:243], v[26:27], v[32:33] op_sel_hi:[0,1,1] neg_lo:[1,0,0] neg_hi:[1,0,0]
	v_cvt_pk_bf16_f32 v26, v26, v27
	v_cndmask_b32_e64 v33, 0, 1.0, vcc
	v_cmp_eq_u32_e32 vcc, v104, v143
	s_nop 1
	v_cndmask_b32_e64 v32, 0, 1.0, vcc
	v_pk_fma_f32 v[28:29], v[242:243], v[28:29], v[32:33] op_sel_hi:[0,1,1] neg_lo:[1,0,0] neg_hi:[1,0,0]
	v_cvt_pk_bf16_f32 v27, v28, v29
	ds_write_b64 v186, v[26:27] offset:2720
	v_cmp_eq_u32_e32 vcc, v91, v144
	s_nop 1
	v_cndmask_b32_e64 v28, 0, 1.0, vcc
	v_cmp_eq_u32_e32 vcc, v102, v144
	s_nop 1
	v_cndmask_b32_e64 v29, 0, 1.0, vcc
	v_cmp_eq_u32_e32 vcc, v103, v144
	v_pk_fma_f32 v[22:23], v[244:245], v[22:23], v[28:29] op_sel_hi:[0,1,1] neg_lo:[1,0,0] neg_hi:[1,0,0]
	v_cvt_pk_bf16_f32 v22, v22, v23
	v_cndmask_b32_e64 v29, 0, 1.0, vcc
	v_cmp_eq_u32_e32 vcc, v104, v144
	s_nop 1
	v_cndmask_b32_e64 v28, 0, 1.0, vcc
	v_pk_fma_f32 v[24:25], v[244:245], v[24:25], v[28:29] op_sel_hi:[0,1,1] neg_lo:[1,0,0] neg_hi:[1,0,0]
	v_cvt_pk_bf16_f32 v23, v24, v25
	ds_write_b64 v186, v[22:23] offset:3264
	v_cmp_eq_u32_e32 vcc, v91, v145
	s_nop 1
	v_cndmask_b32_e64 v24, 0, 1.0, vcc
	v_cmp_eq_u32_e32 vcc, v102, v145
	s_nop 1
	v_cndmask_b32_e64 v25, 0, 1.0, vcc
	v_cmp_eq_u32_e32 vcc, v103, v145
	v_pk_fma_f32 v[18:19], v[246:247], v[18:19], v[24:25] op_sel_hi:[0,1,1] neg_lo:[1,0,0] neg_hi:[1,0,0]
	v_cvt_pk_bf16_f32 v18, v18, v19
	v_cndmask_b32_e64 v25, 0, 1.0, vcc
	v_cmp_eq_u32_e32 vcc, v104, v145
	s_nop 1
	v_cndmask_b32_e64 v24, 0, 1.0, vcc
	v_pk_fma_f32 v[20:21], v[246:247], v[20:21], v[24:25] op_sel_hi:[0,1,1] neg_lo:[1,0,0] neg_hi:[1,0,0]
	v_cvt_pk_bf16_f32 v19, v20, v21
	ds_write_b64 v186, v[18:19] offset:3808
	ds_read_b32 v232, v187 offset:128
	ds_read_b32 v234, v187 offset:136
	ds_read_b32 v236, v187 offset:144
	ds_read_b32 v238, v187 offset:152
	ds_read_b32 v240, v187 offset:160
	ds_read_b32 v242, v187 offset:168
	ds_read_b32 v244, v187 offset:176
	ds_read_b32 v246, v187 offset:184
	ds_read_b128 v[18:21], v1
	ds_read_b128 v[22:25], v1 offset:64
	ds_read_b128 v[26:29], v1 offset:128
	ds_read_b128 v[30:33], v1 offset:192
	v_lshl_add_u64 v[66:67], v[150:151], 0, s[8:9]
	v_lshl_add_u64 v[68:69], v[152:153], 0, s[8:9]
	v_lshl_add_u64 v[70:71], v[156:157], 0, s[8:9]
	v_lshl_add_u64 v[72:73], v[158:159], 0, s[8:9]
	v_lshl_add_u64 v[74:75], v[160:161], 0, s[8:9]
	v_lshl_add_u64 v[76:77], v[162:163], 0, s[8:9]
	v_lshl_add_u64 v[134:135], v[164:165], 0, s[8:9]
	v_lshl_add_u64 v[136:137], v[166:167], 0, s[8:9]
	global_load_dwordx4 v[126:129], v[66:67], off nt
	global_load_dwordx4 v[114:117], v[68:69], off nt
	global_load_dwordx4 v[102:105], v[70:71], off nt
	global_load_dwordx4 v[90:93], v[72:73], off nt
	global_load_dwordx4 v[78:81], v[74:75], off nt
	s_nop 0
	global_load_dwordx4 v[74:77], v[76:77], off nt
	s_nop 0
	global_load_dwordx4 v[70:73], v[134:135], off nt
	global_load_dwordx4 v[66:69], v[136:137], off nt
	s_waitcnt vmcnt(23)
	s_waitcnt vmcnt(22)
	s_waitcnt vmcnt(21)
	s_waitcnt vmcnt(20)
	s_waitcnt vmcnt(19)
	s_waitcnt vmcnt(18)
	s_waitcnt vmcnt(17)
	s_waitcnt vmcnt(16)
	v_or_b32_e32 v194, 32, v132
	v_add_u32_e32 v135, 1, v133
	v_cmp_eq_u32_e32 vcc, v133, v194
	v_add_u32_e32 v202, 3, v133
	v_add_u32_e32 v203, 2, v133
	v_cndmask_b32_e64 v136, 0, 1.0, vcc
	v_cmp_eq_u32_e32 vcc, v135, v194
	v_or_b32_e32 v195, 34, v132
	v_or_b32_e32 v196, 36, v132
	v_cndmask_b32_e64 v137, 0, 1.0, vcc
	v_cmp_eq_u32_e32 vcc, v202, v194
	s_waitcnt lgkmcnt(0)
	v_pk_fma_f32 v[122:123], v[232:233], v[122:123], v[136:137] op_sel_hi:[0,1,1] neg_lo:[1,0,0] neg_hi:[1,0,0]
	v_cvt_pk_bf16_f32 v122, v122, v123
	v_cndmask_b32_e64 v137, 0, 1.0, vcc
	v_cmp_eq_u32_e32 vcc, v203, v194
	v_or_b32_e32 v197, 38, v132
	v_or_b32_e32 v198, 40, v132
	v_cndmask_b32_e64 v136, 0, 1.0, vcc
	v_pk_fma_f32 v[124:125], v[232:233], v[124:125], v[136:137] op_sel_hi:[0,1,1] neg_lo:[1,0,0] neg_hi:[1,0,0]
	v_cvt_pk_bf16_f32 v123, v124, v125
	ds_write_b64 v186, v[122:123]
	v_cmp_eq_u32_e32 vcc, v133, v195
	v_or_b32_e32 v199, 42, v132
	v_or_b32_e32 v200, 44, v132
	v_cndmask_b32_e64 v124, 0, 1.0, vcc
	v_cmp_eq_u32_e32 vcc, v135, v195
	v_or_b32_e32 v201, 46, v132
	s_nop 0
	v_cndmask_b32_e64 v125, 0, 1.0, vcc
	v_cmp_eq_u32_e32 vcc, v202, v195
	v_pk_fma_f32 v[106:107], v[234:235], v[106:107], v[124:125] op_sel_hi:[0,1,1] neg_lo:[1,0,0] neg_hi:[1,0,0]
	v_cvt_pk_bf16_f32 v106, v106, v107
	v_cndmask_b32_e64 v125, 0, 1.0, vcc
	v_cmp_eq_u32_e32 vcc, v203, v195
	s_nop 1
	v_cndmask_b32_e64 v124, 0, 1.0, vcc
	v_pk_fma_f32 v[108:109], v[234:235], v[108:109], v[124:125] op_sel_hi:[0,1,1] neg_lo:[1,0,0] neg_hi:[1,0,0]
	v_cvt_pk_bf16_f32 v107, v108, v109
	ds_write_b64 v186, v[106:107] offset:544
	v_cmp_eq_u32_e32 vcc, v133, v196
	s_nop 1
	v_cndmask_b32_e64 v108, 0, 1.0, vcc
	v_cmp_eq_u32_e32 vcc, v135, v196
	s_nop 1
	v_cndmask_b32_e64 v109, 0, 1.0, vcc
	v_cmp_eq_u32_e32 vcc, v202, v196
	v_pk_fma_f32 v[94:95], v[236:237], v[94:95], v[108:109] op_sel_hi:[0,1,1] neg_lo:[1,0,0] neg_hi:[1,0,0]
	v_cvt_pk_bf16_f32 v94, v94, v95
	v_cndmask_b32_e64 v109, 0, 1.0, vcc
	v_cmp_eq_u32_e32 vcc, v203, v196
	s_nop 1
	v_cndmask_b32_e64 v108, 0, 1.0, vcc
	v_pk_fma_f32 v[96:97], v[236:237], v[96:97], v[108:109] op_sel_hi:[0,1,1] neg_lo:[1,0,0] neg_hi:[1,0,0]
	v_cvt_pk_bf16_f32 v95, v96, v97
	ds_write_b64 v186, v[94:95] offset:1088
	v_cmp_eq_u32_e32 vcc, v133, v197
	s_nop 1
	v_cndmask_b32_e64 v96, 0, 1.0, vcc
	v_cmp_eq_u32_e32 vcc, v135, v197
	s_nop 1
	v_cndmask_b32_e64 v97, 0, 1.0, vcc
	v_cmp_eq_u32_e32 vcc, v202, v197
	v_pk_fma_f32 v[82:83], v[238:239], v[82:83], v[96:97] op_sel_hi:[0,1,1] neg_lo:[1,0,0] neg_hi:[1,0,0]
	v_cvt_pk_bf16_f32 v82, v82, v83
	v_cndmask_b32_e64 v97, 0, 1.0, vcc
	v_cmp_eq_u32_e32 vcc, v203, v197
	s_nop 1
	v_cndmask_b32_e64 v96, 0, 1.0, vcc
	v_pk_fma_f32 v[84:85], v[238:239], v[84:85], v[96:97] op_sel_hi:[0,1,1] neg_lo:[1,0,0] neg_hi:[1,0,0]
	v_cvt_pk_bf16_f32 v83, v84, v85
	ds_write_b64 v186, v[82:83] offset:1632
	v_cmp_eq_u32_e32 vcc, v133, v198
	s_nop 1
	v_cndmask_b32_e64 v84, 0, 1.0, vcc
	v_cmp_eq_u32_e32 vcc, v135, v198
	s_nop 1
	v_cndmask_b32_e64 v85, 0, 1.0, vcc
	v_cmp_eq_u32_e32 vcc, v202, v198
	v_pk_fma_f32 v[46:47], v[240:241], v[46:47], v[84:85] op_sel_hi:[0,1,1] neg_lo:[1,0,0] neg_hi:[1,0,0]
	v_cvt_pk_bf16_f32 v46, v46, v47
	v_cndmask_b32_e64 v85, 0, 1.0, vcc
	v_cmp_eq_u32_e32 vcc, v203, v198
	s_nop 1
	v_cndmask_b32_e64 v84, 0, 1.0, vcc
	v_pk_fma_f32 v[48:49], v[240:241], v[48:49], v[84:85] op_sel_hi:[0,1,1] neg_lo:[1,0,0] neg_hi:[1,0,0]
	v_cvt_pk_bf16_f32 v47, v48, v49
	ds_write_b64 v186, v[46:47] offset:2176
	v_cmp_eq_u32_e32 vcc, v133, v199
	s_nop 1
	v_cndmask_b32_e64 v48, 0, 1.0, vcc
	v_cmp_eq_u32_e32 vcc, v135, v199
	s_nop 1
	v_cndmask_b32_e64 v49, 0, 1.0, vcc
	v_cmp_eq_u32_e32 vcc, v202, v199
	v_pk_fma_f32 v[42:43], v[242:243], v[42:43], v[48:49] op_sel_hi:[0,1,1] neg_lo:[1,0,0] neg_hi:[1,0,0]
	v_cvt_pk_bf16_f32 v42, v42, v43
	v_cndmask_b32_e64 v49, 0, 1.0, vcc
	v_cmp_eq_u32_e32 vcc, v203, v199
	s_nop 1
	v_cndmask_b32_e64 v48, 0, 1.0, vcc
	v_pk_fma_f32 v[44:45], v[242:243], v[44:45], v[48:49] op_sel_hi:[0,1,1] neg_lo:[1,0,0] neg_hi:[1,0,0]
	v_cvt_pk_bf16_f32 v43, v44, v45
	ds_write_b64 v186, v[42:43] offset:2720
	v_cmp_eq_u32_e32 vcc, v133, v200
	s_nop 1
	v_cndmask_b32_e64 v44, 0, 1.0, vcc
	v_cmp_eq_u32_e32 vcc, v135, v200
	s_nop 1
	v_cndmask_b32_e64 v45, 0, 1.0, vcc
	v_cmp_eq_u32_e32 vcc, v202, v200
	v_pk_fma_f32 v[38:39], v[244:245], v[38:39], v[44:45] op_sel_hi:[0,1,1] neg_lo:[1,0,0] neg_hi:[1,0,0]
	v_cvt_pk_bf16_f32 v38, v38, v39
	v_cndmask_b32_e64 v45, 0, 1.0, vcc
	v_cmp_eq_u32_e32 vcc, v203, v200
	s_nop 1
	v_cndmask_b32_e64 v44, 0, 1.0, vcc
	v_pk_fma_f32 v[40:41], v[244:245], v[40:41], v[44:45] op_sel_hi:[0,1,1] neg_lo:[1,0,0] neg_hi:[1,0,0]
	v_cvt_pk_bf16_f32 v39, v40, v41
	ds_write_b64 v186, v[38:39] offset:3264
	v_cmp_eq_u32_e32 vcc, v133, v201
	s_nop 1
	v_cndmask_b32_e64 v40, 0, 1.0, vcc
	v_cmp_eq_u32_e32 vcc, v135, v201
	s_nop 1
	v_cndmask_b32_e64 v41, 0, 1.0, vcc
	v_cmp_eq_u32_e32 vcc, v202, v201
	v_pk_fma_f32 v[34:35], v[246:247], v[34:35], v[40:41] op_sel_hi:[0,1,1] neg_lo:[1,0,0] neg_hi:[1,0,0]
	v_cvt_pk_bf16_f32 v34, v34, v35
	v_cndmask_b32_e64 v41, 0, 1.0, vcc
	v_cmp_eq_u32_e32 vcc, v203, v201
	s_nop 1
	v_cndmask_b32_e64 v40, 0, 1.0, vcc
	v_pk_fma_f32 v[36:37], v[246:247], v[36:37], v[40:41] op_sel_hi:[0,1,1] neg_lo:[1,0,0] neg_hi:[1,0,0]
	v_cvt_pk_bf16_f32 v35, v36, v37
	ds_write_b64 v186, v[34:35] offset:3808
	ds_read_b32 v232, v187 offset:0
	ds_read_b32 v234, v187 offset:8
	ds_read_b32 v236, v187 offset:16
	ds_read_b32 v238, v187 offset:24
	ds_read_b32 v240, v187 offset:32
	ds_read_b32 v242, v187 offset:40
	ds_read_b32 v244, v187 offset:48
	ds_read_b32 v246, v187 offset:56
	ds_read_b128 v[34:37], v1
	ds_read_b128 v[38:41], v1 offset:64
	ds_read_b128 v[42:45], v1 offset:128
	ds_read_b128 v[46:49], v1 offset:192
	v_mov_b32_e32 v106, v189
	s_waitcnt vmcnt(15)
	s_waitcnt vmcnt(14)
	s_waitcnt vmcnt(13)
	s_waitcnt vmcnt(12)
	s_waitcnt vmcnt(11)
	s_waitcnt vmcnt(10)
	s_waitcnt vmcnt(9)
	s_waitcnt vmcnt(8)
	v_add_u32_e32 v107, 1, v106
	v_cmp_eq_u32_e32 vcc, v106, v132
	v_add_u32_e32 v108, 3, v106
	v_add_u32_e32 v109, 2, v106
	v_cndmask_b32_e64 v84, 0, 1.0, vcc
	v_cmp_eq_u32_e32 vcc, v107, v132
	s_nop 1
	v_cndmask_b32_e64 v85, 0, 1.0, vcc
	v_cmp_eq_u32_e32 vcc, v108, v132
	s_waitcnt lgkmcnt(0)
	v_pk_fma_f32 v[94:95], v[232:233], v[118:119], v[84:85] op_sel_hi:[0,1,1] neg_lo:[1,0,0] neg_hi:[1,0,0]
	v_cvt_pk_bf16_f32 v94, v94, v95
	v_cndmask_b32_e64 v97, 0, 1.0, vcc
	v_cmp_eq_u32_e32 vcc, v109, v132
	s_nop 1
	v_cndmask_b32_e64 v96, 0, 1.0, vcc
	v_pk_fma_f32 v[82:83], v[232:233], v[120:121], v[96:97] op_sel_hi:[0,1,1] neg_lo:[1,0,0] neg_hi:[1,0,0]
	v_cvt_pk_bf16_f32 v95, v82, v83
	ds_write_b64 v186, v[94:95]
	v_cmp_eq_u32_e32 vcc, v106, v193
	s_nop 1
	v_cndmask_b32_e64 v94, 0, 1.0, vcc
	v_cmp_eq_u32_e32 vcc, v107, v193
	s_nop 1
	v_cndmask_b32_e64 v95, 0, 1.0, vcc
	v_cmp_eq_u32_e32 vcc, v108, v193
	v_pk_fma_f32 v[94:95], v[234:235], v[110:111], v[94:95] op_sel_hi:[0,1,1] neg_lo:[1,0,0] neg_hi:[1,0,0]
	v_cvt_pk_bf16_f32 v94, v94, v95
	v_cndmask_b32_e64 v85, 0, 1.0, vcc
	v_pk_fma_f32 v[82:83], v[234:235], v[112:113], v[84:85] op_sel_hi:[0,1,1] neg_lo:[1,0,0] neg_hi:[1,0,0]
	v_cvt_pk_bf16_f32 v95, v82, v83
	ds_write_b64 v186, v[94:95] offset:544
	v_cmp_eq_u32_e32 vcc, v106, v192
	s_nop 1
	v_cndmask_b32_e64 v84, 0, 1.0, vcc
	v_cmp_eq_u32_e32 vcc, v107, v192
	s_nop 1
	v_cndmask_b32_e64 v85, 0, 1.0, vcc
	v_cmp_eq_u32_e32 vcc, v108, v192
	v_pk_fma_f32 v[84:85], v[236:237], v[98:99], v[84:85] op_sel_hi:[0,1,1] neg_lo:[1,0,0] neg_hi:[1,0,0]
	v_cvt_pk_bf16_f32 v84, v84, v85
	v_cndmask_b32_e64 v95, 0, 1.0, vcc
	v_cmp_eq_u32_e32 vcc, v109, v192
	s_nop 1
	v_cndmask_b32_e64 v94, 0, 1.0, vcc
	v_pk_fma_f32 v[82:83], v[236:237], v[100:101], v[94:95] op_sel_hi:[0,1,1] neg_lo:[1,0,0] neg_hi:[1,0,0]
	v_cvt_pk_bf16_f32 v85, v82, v83
	ds_write_b64 v186, v[84:85] offset:1088
	v_cmp_eq_u32_e32 vcc, v106, v190
	s_nop 1
	v_cndmask_b32_e64 v84, 0, 1.0, vcc
	v_cmp_eq_u32_e32 vcc, v107, v190
	s_nop 1
	v_cndmask_b32_e64 v85, 0, 1.0, vcc
	v_cmp_eq_u32_e32 vcc, v108, v190
	v_pk_fma_f32 v[84:85], v[238:239], v[86:87], v[84:85] op_sel_hi:[0,1,1] neg_lo:[1,0,0] neg_hi:[1,0,0]
	v_cvt_pk_bf16_f32 v84, v84, v85
	v_cndmask_b32_e64 v87, 0, 1.0, vcc
	v_cmp_eq_u32_e32 vcc, v109, v190
	s_nop 1
	v_cndmask_b32_e64 v86, 0, 1.0, vcc
	v_pk_fma_f32 v[82:83], v[238:239], v[88:89], v[86:87] op_sel_hi:[0,1,1] neg_lo:[1,0,0] neg_hi:[1,0,0]
	v_cvt_pk_bf16_f32 v85, v82, v83
	ds_write_b64 v186, v[84:85] offset:1632
	v_cmp_eq_u32_e32 vcc, v106, v149
	s_nop 1
	v_cndmask_b32_e64 v84, 0, 1.0, vcc
	v_cmp_eq_u32_e32 vcc, v107, v149
	s_nop 1
	v_cndmask_b32_e64 v85, 0, 1.0, vcc
	v_cmp_eq_u32_e32 vcc, v108, v149
	v_pk_fma_f32 v[62:63], v[240:241], v[62:63], v[84:85] op_sel_hi:[0,1,1] neg_lo:[1,0,0] neg_hi:[1,0,0]
	v_cvt_pk_bf16_f32 v62, v62, v63
	v_cndmask_b32_e64 v85, 0, 1.0, vcc
	v_cmp_eq_u32_e32 vcc, v109, v149
	s_nop 1
	v_cndmask_b32_e64 v84, 0, 1.0, vcc
	v_pk_fma_f32 v[64:65], v[240:241], v[64:65], v[84:85] op_sel_hi:[0,1,1] neg_lo:[1,0,0] neg_hi:[1,0,0]
	v_cvt_pk_bf16_f32 v63, v64, v65
	ds_write_b64 v186, v[62:63] offset:2176
	v_cmp_eq_u32_e32 vcc, v106, v148
	s_nop 1
	v_cndmask_b32_e64 v64, 0, 1.0, vcc
	v_cmp_eq_u32_e32 vcc, v107, v148
	s_nop 1
	v_cndmask_b32_e64 v65, 0, 1.0, vcc
	v_cmp_eq_u32_e32 vcc, v108, v148
	v_pk_fma_f32 v[58:59], v[242:243], v[58:59], v[64:65] op_sel_hi:[0,1,1] neg_lo:[1,0,0] neg_hi:[1,0,0]
	v_cvt_pk_bf16_f32 v58, v58, v59
	v_cndmask_b32_e64 v65, 0, 1.0, vcc
	v_cmp_eq_u32_e32 vcc, v109, v148
	s_nop 1
	v_cndmask_b32_e64 v64, 0, 1.0, vcc
	v_pk_fma_f32 v[60:61], v[242:243], v[60:61], v[64:65] op_sel_hi:[0,1,1] neg_lo:[1,0,0] neg_hi:[1,0,0]
	v_cvt_pk_bf16_f32 v59, v60, v61
	ds_write_b64 v186, v[58:59] offset:2720
	v_cmp_eq_u32_e32 vcc, v106, v147
	s_nop 1
	v_cndmask_b32_e64 v60, 0, 1.0, vcc
	v_cmp_eq_u32_e32 vcc, v107, v147
	s_nop 1
	v_cndmask_b32_e64 v61, 0, 1.0, vcc
	v_cmp_eq_u32_e32 vcc, v108, v147
	v_pk_fma_f32 v[54:55], v[244:245], v[54:55], v[60:61] op_sel_hi:[0,1,1] neg_lo:[1,0,0] neg_hi:[1,0,0]
	v_cvt_pk_bf16_f32 v54, v54, v55
	v_cndmask_b32_e64 v61, 0, 1.0, vcc
	v_cmp_eq_u32_e32 vcc, v109, v147
	s_nop 1
	v_cndmask_b32_e64 v60, 0, 1.0, vcc
	v_pk_fma_f32 v[56:57], v[244:245], v[56:57], v[60:61] op_sel_hi:[0,1,1] neg_lo:[1,0,0] neg_hi:[1,0,0]
	v_cvt_pk_bf16_f32 v55, v56, v57
	ds_write_b64 v186, v[54:55] offset:3264
	v_cmp_eq_u32_e32 vcc, v106, v146
	s_nop 1
	v_cndmask_b32_e64 v56, 0, 1.0, vcc
	v_cmp_eq_u32_e32 vcc, v107, v146
	s_nop 1
	v_cndmask_b32_e64 v57, 0, 1.0, vcc
	v_cmp_eq_u32_e32 vcc, v108, v146
	v_pk_fma_f32 v[50:51], v[246:247], v[50:51], v[56:57] op_sel_hi:[0,1,1] neg_lo:[1,0,0] neg_hi:[1,0,0]
	v_cvt_pk_bf16_f32 v50, v50, v51
	v_cndmask_b32_e64 v57, 0, 1.0, vcc
	v_cmp_eq_u32_e32 vcc, v109, v146
	s_nop 1
	v_cndmask_b32_e64 v56, 0, 1.0, vcc
	v_pk_fma_f32 v[52:53], v[246:247], v[52:53], v[56:57] op_sel_hi:[0,1,1] neg_lo:[1,0,0] neg_hi:[1,0,0]
	v_cvt_pk_bf16_f32 v51, v52, v53
	ds_write_b64 v186, v[50:51] offset:3808
	ds_read_b32 v232, v187 offset:64
	ds_read_b32 v234, v187 offset:72
	ds_read_b32 v236, v187 offset:80
	ds_read_b32 v238, v187 offset:88
	ds_read_b32 v240, v187 offset:96
	ds_read_b32 v242, v187 offset:104
	ds_read_b32 v244, v187 offset:112
	ds_read_b32 v246, v187 offset:120
	ds_read_b128 v[50:53], v1
	ds_read_b128 v[54:57], v1 offset:64
	ds_read_b128 v[58:61], v1 offset:128
	ds_read_b128 v[62:65], v1 offset:192
	v_lshl_add_u64 v[82:83], v[168:169], 0, s[8:9]
	v_lshl_add_u64 v[84:85], v[170:171], 0, s[8:9]
	v_lshl_add_u64 v[86:87], v[172:173], 0, s[8:9]
	v_lshl_add_u64 v[88:89], v[174:175], 0, s[8:9]
	v_lshl_add_u64 v[94:95], v[176:177], 0, s[8:9]
	v_lshl_add_u64 v[96:97], v[178:179], 0, s[8:9]
	v_lshl_add_u64 v[122:123], v[180:181], 0, s[8:9]
	v_lshl_add_u64 v[124:125], v[182:183], 0, s[8:9]
	global_load_dwordx4 v[134:137], v[82:83], off nt
	global_load_dwordx4 v[118:121], v[84:85], off nt
	global_load_dwordx4 v[110:113], v[86:87], off nt
	global_load_dwordx4 v[106:109], v[88:89], off nt
	global_load_dwordx4 v[98:101], v[94:95], off nt
	s_nop 0
	global_load_dwordx4 v[94:97], v[96:97], off nt
	s_nop 0
	global_load_dwordx4 v[86:89], v[122:123], off nt
	global_load_dwordx4 v[82:85], v[124:125], off nt
	v_mov_b32_e32 v132, v189
	s_waitcnt vmcnt(15)
	s_waitcnt vmcnt(14)
	s_waitcnt vmcnt(13)
	s_waitcnt vmcnt(12)
	s_waitcnt vmcnt(11)
	s_waitcnt vmcnt(10)
	s_waitcnt vmcnt(9)
	s_waitcnt vmcnt(8)
	v_add_u32_e32 v133, 1, v132
	v_cmp_eq_u32_e32 vcc, v132, v138
	v_add_u32_e32 v146, 3, v132
	v_add_u32_e32 v147, 2, v132
	v_cndmask_b32_e64 v124, 0, 1.0, vcc
	v_cmp_eq_u32_e32 vcc, v133, v138
	s_nop 1
	v_cndmask_b32_e64 v125, 0, 1.0, vcc
	v_cmp_eq_u32_e32 vcc, v146, v138
	s_waitcnt lgkmcnt(0)
	v_pk_fma_f32 v[124:125], v[232:233], v[126:127], v[124:125] op_sel_hi:[0,1,1] neg_lo:[1,0,0] neg_hi:[1,0,0]
	v_cvt_pk_bf16_f32 v124, v124, v125
	v_cndmask_b32_e64 v127, 0, 1.0, vcc
	v_cmp_eq_u32_e32 vcc, v147, v138
	s_nop 1
	v_cndmask_b32_e64 v126, 0, 1.0, vcc
	v_pk_fma_f32 v[122:123], v[232:233], v[128:129], v[126:127] op_sel_hi:[0,1,1] neg_lo:[1,0,0] neg_hi:[1,0,0]
	v_cvt_pk_bf16_f32 v125, v122, v123
	ds_write_b64 v186, v[124:125]
	v_cmp_eq_u32_e32 vcc, v132, v139
	s_nop 1
	v_cndmask_b32_e64 v124, 0, 1.0, vcc
	v_cmp_eq_u32_e32 vcc, v133, v139
	s_nop 1
	v_cndmask_b32_e64 v125, 0, 1.0, vcc
	v_cmp_eq_u32_e32 vcc, v146, v139
	v_pk_fma_f32 v[114:115], v[234:235], v[114:115], v[124:125] op_sel_hi:[0,1,1] neg_lo:[1,0,0] neg_hi:[1,0,0]
	v_cvt_pk_bf16_f32 v114, v114, v115
	v_cndmask_b32_e64 v125, 0, 1.0, vcc
	v_cmp_eq_u32_e32 vcc, v147, v139
	s_nop 1
	v_cndmask_b32_e64 v124, 0, 1.0, vcc
	v_pk_fma_f32 v[116:117], v[234:235], v[116:117], v[124:125] op_sel_hi:[0,1,1] neg_lo:[1,0,0] neg_hi:[1,0,0]
	v_cvt_pk_bf16_f32 v115, v116, v117
	ds_write_b64 v186, v[114:115] offset:544
	v_cmp_eq_u32_e32 vcc, v132, v140
	s_nop 1
	v_cndmask_b32_e64 v116, 0, 1.0, vcc
	v_cmp_eq_u32_e32 vcc, v133, v140
	s_nop 1
	v_cndmask_b32_e64 v117, 0, 1.0, vcc
	v_cmp_eq_u32_e32 vcc, v146, v140
	v_pk_fma_f32 v[102:103], v[236:237], v[102:103], v[116:117] op_sel_hi:[0,1,1] neg_lo:[1,0,0] neg_hi:[1,0,0]
	v_cvt_pk_bf16_f32 v102, v102, v103
	v_cndmask_b32_e64 v117, 0, 1.0, vcc
	v_cmp_eq_u32_e32 vcc, v147, v140
	s_nop 1
	v_cndmask_b32_e64 v116, 0, 1.0, vcc
	v_pk_fma_f32 v[104:105], v[236:237], v[104:105], v[116:117] op_sel_hi:[0,1,1] neg_lo:[1,0,0] neg_hi:[1,0,0]
	v_cvt_pk_bf16_f32 v103, v104, v105
	ds_write_b64 v186, v[102:103] offset:1088
	v_cmp_eq_u32_e32 vcc, v132, v141
	s_nop 1
	v_cndmask_b32_e64 v104, 0, 1.0, vcc
	v_cmp_eq_u32_e32 vcc, v133, v141
	s_nop 1
	v_cndmask_b32_e64 v105, 0, 1.0, vcc
	v_cmp_eq_u32_e32 vcc, v146, v141
	v_pk_fma_f32 v[90:91], v[238:239], v[90:91], v[104:105] op_sel_hi:[0,1,1] neg_lo:[1,0,0] neg_hi:[1,0,0]
	v_cvt_pk_bf16_f32 v90, v90, v91
	v_cndmask_b32_e64 v105, 0, 1.0, vcc
	v_cmp_eq_u32_e32 vcc, v147, v141
	s_nop 1
	v_cndmask_b32_e64 v104, 0, 1.0, vcc
	v_pk_fma_f32 v[92:93], v[238:239], v[92:93], v[104:105] op_sel_hi:[0,1,1] neg_lo:[1,0,0] neg_hi:[1,0,0]
	v_cvt_pk_bf16_f32 v91, v92, v93
	ds_write_b64 v186, v[90:91] offset:1632
	v_cmp_eq_u32_e32 vcc, v132, v142
	s_nop 1
	v_cndmask_b32_e64 v92, 0, 1.0, vcc
	v_cmp_eq_u32_e32 vcc, v133, v142
	s_nop 1
	v_cndmask_b32_e64 v93, 0, 1.0, vcc
	v_cmp_eq_u32_e32 vcc, v146, v142
	v_pk_fma_f32 v[78:79], v[240:241], v[78:79], v[92:93] op_sel_hi:[0,1,1] neg_lo:[1,0,0] neg_hi:[1,0,0]
	v_cvt_pk_bf16_f32 v78, v78, v79
	v_cndmask_b32_e64 v93, 0, 1.0, vcc
	v_cmp_eq_u32_e32 vcc, v147, v142
	s_nop 1
	v_cndmask_b32_e64 v92, 0, 1.0, vcc
	v_pk_fma_f32 v[80:81], v[240:241], v[80:81], v[92:93] op_sel_hi:[0,1,1] neg_lo:[1,0,0] neg_hi:[1,0,0]
	v_cvt_pk_bf16_f32 v79, v80, v81
	ds_write_b64 v186, v[78:79] offset:2176
	v_cmp_eq_u32_e32 vcc, v132, v143
	s_nop 1
	v_cndmask_b32_e64 v80, 0, 1.0, vcc
	v_cmp_eq_u32_e32 vcc, v133, v143
	s_nop 1
	v_cndmask_b32_e64 v81, 0, 1.0, vcc
	v_cmp_eq_u32_e32 vcc, v146, v143
	v_pk_fma_f32 v[74:75], v[242:243], v[74:75], v[80:81] op_sel_hi:[0,1,1] neg_lo:[1,0,0] neg_hi:[1,0,0]
	v_cvt_pk_bf16_f32 v74, v74, v75
	v_cndmask_b32_e64 v81, 0, 1.0, vcc
	v_cmp_eq_u32_e32 vcc, v147, v143
	s_nop 1
	v_cndmask_b32_e64 v80, 0, 1.0, vcc
	v_pk_fma_f32 v[76:77], v[242:243], v[76:77], v[80:81] op_sel_hi:[0,1,1] neg_lo:[1,0,0] neg_hi:[1,0,0]
	v_cvt_pk_bf16_f32 v75, v76, v77
	ds_write_b64 v186, v[74:75] offset:2720
	v_cmp_eq_u32_e32 vcc, v132, v144
	s_nop 1
	v_cndmask_b32_e64 v76, 0, 1.0, vcc
	v_cmp_eq_u32_e32 vcc, v133, v144
	s_nop 1
	v_cndmask_b32_e64 v77, 0, 1.0, vcc
	v_cmp_eq_u32_e32 vcc, v146, v144
	v_pk_fma_f32 v[70:71], v[244:245], v[70:71], v[76:77] op_sel_hi:[0,1,1] neg_lo:[1,0,0] neg_hi:[1,0,0]
	v_cvt_pk_bf16_f32 v70, v70, v71
	v_cndmask_b32_e64 v77, 0, 1.0, vcc
	v_cmp_eq_u32_e32 vcc, v147, v144
	s_nop 1
	v_cndmask_b32_e64 v76, 0, 1.0, vcc
	v_pk_fma_f32 v[72:73], v[244:245], v[72:73], v[76:77] op_sel_hi:[0,1,1] neg_lo:[1,0,0] neg_hi:[1,0,0]
	v_cvt_pk_bf16_f32 v71, v72, v73
	ds_write_b64 v186, v[70:71] offset:3264
	v_cmp_eq_u32_e32 vcc, v132, v145
	s_nop 1
	v_cndmask_b32_e64 v72, 0, 1.0, vcc
	v_cmp_eq_u32_e32 vcc, v133, v145
	s_nop 1
	v_cndmask_b32_e64 v73, 0, 1.0, vcc
	v_cmp_eq_u32_e32 vcc, v146, v145
	v_pk_fma_f32 v[66:67], v[246:247], v[66:67], v[72:73] op_sel_hi:[0,1,1] neg_lo:[1,0,0] neg_hi:[1,0,0]
	v_cvt_pk_bf16_f32 v66, v66, v67
	v_cndmask_b32_e64 v73, 0, 1.0, vcc
	v_cmp_eq_u32_e32 vcc, v147, v145
	s_nop 1
	v_cndmask_b32_e64 v72, 0, 1.0, vcc
	v_pk_fma_f32 v[68:69], v[246:247], v[68:69], v[72:73] op_sel_hi:[0,1,1] neg_lo:[1,0,0] neg_hi:[1,0,0]
	v_cvt_pk_bf16_f32 v67, v68, v69
	ds_write_b64 v186, v[66:67] offset:3808
	ds_read_b32 v232, v187 offset:128
	ds_read_b32 v234, v187 offset:136
	ds_read_b32 v236, v187 offset:144
	ds_read_b32 v238, v187 offset:152
	ds_read_b32 v240, v187 offset:160
	ds_read_b32 v242, v187 offset:168
	ds_read_b32 v244, v187 offset:176
	ds_read_b32 v246, v187 offset:184
	ds_read_b128 v[66:69], v1
	ds_read_b128 v[70:73], v1 offset:64
	ds_read_b128 v[74:77], v1 offset:128
	ds_read_b128 v[78:81], v1 offset:192
	v_lshl_add_u64 v[90:91], v[130:131], 0, s[0:1]
	v_add_co_u32_e32 v92, vcc, s7, v90
	s_nop 1
	v_addc_co_u32_e32 v93, vcc, 0, v91, vcc
	global_load_dwordx4 v[146:149], v[90:91], off nt
	global_load_dwordx4 v[142:145], v[92:93], off nt
	v_add_co_u32_e32 v92, vcc, s36, v90
	s_nop 1
	v_addc_co_u32_e32 v93, vcc, 0, v91, vcc
	v_add_co_u32_e32 v102, vcc, s37, v90
	s_nop 1
	v_addc_co_u32_e32 v103, vcc, 0, v91, vcc
	global_load_dwordx4 v[138:141], v[92:93], off nt
	global_load_dwordx4 v[130:133], v[102:103], off nt
	v_add_co_u32_e32 v92, vcc, s38, v90
	s_nop 1
	v_addc_co_u32_e32 v93, vcc, 0, v91, vcc
	v_add_co_u32_e32 v102, vcc, s39, v90
	s_nop 1
	v_addc_co_u32_e32 v103, vcc, 0, v91, vcc
	global_load_dwordx4 v[126:129], v[92:93], off nt
	global_load_dwordx4 v[122:125], v[102:103], off nt
	v_add_co_u32_e32 v92, vcc, s41, v90
	s_nop 1
	v_addc_co_u32_e32 v93, vcc, 0, v91, vcc
	v_add_co_u32_e32 v90, vcc, s42, v90
	s_nop 1
	v_addc_co_u32_e32 v91, vcc, 0, v91, vcc
	global_load_dwordx4 v[114:117], v[92:93], off nt
	global_load_dwordx4 v[102:105], v[90:91], off nt
	s_waitcnt vmcnt(15)
	s_waitcnt vmcnt(14)
	s_waitcnt vmcnt(13)
	s_waitcnt vmcnt(12)
	s_waitcnt vmcnt(11)
	s_waitcnt vmcnt(10)
	s_waitcnt vmcnt(9)
	s_waitcnt vmcnt(8)
	v_add_u32_e32 v190, 1, v189
	v_cmp_eq_u32_e32 vcc, v189, v194
	v_add_u32_e32 v192, 3, v189
	v_add_u32_e32 v193, 2, v189
	v_cndmask_b32_e64 v92, 0, 1.0, vcc
	v_cmp_eq_u32_e32 vcc, v190, v194
	s_nop 1
	v_cndmask_b32_e64 v93, 0, 1.0, vcc
	v_cmp_eq_u32_e32 vcc, v192, v194
	s_waitcnt lgkmcnt(0)
	v_pk_fma_f32 v[92:93], v[232:233], v[134:135], v[92:93] op_sel_hi:[0,1,1] neg_lo:[1,0,0] neg_hi:[1,0,0]
	v_cvt_pk_bf16_f32 v92, v92, v93
	v_cndmask_b32_e64 v135, 0, 1.0, vcc
	v_cmp_eq_u32_e32 vcc, v193, v194
	s_nop 1
	v_cndmask_b32_e64 v134, 0, 1.0, vcc
	v_pk_fma_f32 v[90:91], v[232:233], v[136:137], v[134:135] op_sel_hi:[0,1,1] neg_lo:[1,0,0] neg_hi:[1,0,0]
	v_cvt_pk_bf16_f32 v93, v90, v91
	ds_write_b64 v186, v[92:93]
	v_cmp_eq_u32_e32 vcc, v189, v195
	s_nop 1
	v_cndmask_b32_e64 v92, 0, 1.0, vcc
	v_cmp_eq_u32_e32 vcc, v190, v195
	s_nop 1
	v_cndmask_b32_e64 v93, 0, 1.0, vcc
	v_cmp_eq_u32_e32 vcc, v192, v195
	v_pk_fma_f32 v[92:93], v[234:235], v[118:119], v[92:93] op_sel_hi:[0,1,1] neg_lo:[1,0,0] neg_hi:[1,0,0]
	v_cvt_pk_bf16_f32 v92, v92, v93
	v_cndmask_b32_e64 v119, 0, 1.0, vcc
	v_cmp_eq_u32_e32 vcc, v193, v195
	s_nop 1
	v_cndmask_b32_e64 v118, 0, 1.0, vcc
	v_pk_fma_f32 v[90:91], v[234:235], v[120:121], v[118:119] op_sel_hi:[0,1,1] neg_lo:[1,0,0] neg_hi:[1,0,0]
	v_cvt_pk_bf16_f32 v93, v90, v91
	ds_write_b64 v186, v[92:93] offset:544
	v_cmp_eq_u32_e32 vcc, v189, v196
	s_nop 1
	v_cndmask_b32_e64 v92, 0, 1.0, vcc
	v_cmp_eq_u32_e32 vcc, v190, v196
	s_nop 1
	v_cndmask_b32_e64 v93, 0, 1.0, vcc
	v_cmp_eq_u32_e32 vcc, v192, v196
	v_pk_fma_f32 v[92:93], v[236:237], v[110:111], v[92:93] op_sel_hi:[0,1,1] neg_lo:[1,0,0] neg_hi:[1,0,0]
	v_cvt_pk_bf16_f32 v92, v92, v93
	v_cndmask_b32_e64 v111, 0, 1.0, vcc
	v_cmp_eq_u32_e32 vcc, v193, v196
	s_nop 1
	v_cndmask_b32_e64 v110, 0, 1.0, vcc
	v_pk_fma_f32 v[90:91], v[236:237], v[112:113], v[110:111] op_sel_hi:[0,1,1] neg_lo:[1,0,0] neg_hi:[1,0,0]
	v_cvt_pk_bf16_f32 v93, v90, v91
	ds_write_b64 v186, v[92:93] offset:1088
	v_cmp_eq_u32_e32 vcc, v189, v197
	s_nop 1
	v_cndmask_b32_e64 v92, 0, 1.0, vcc
	v_cmp_eq_u32_e32 vcc, v190, v197
	s_nop 1
	v_cndmask_b32_e64 v93, 0, 1.0, vcc
	v_cmp_eq_u32_e32 vcc, v192, v197
	v_pk_fma_f32 v[92:93], v[238:239], v[106:107], v[92:93] op_sel_hi:[0,1,1] neg_lo:[1,0,0] neg_hi:[1,0,0]
	v_cvt_pk_bf16_f32 v92, v92, v93
	v_cndmask_b32_e64 v107, 0, 1.0, vcc
	v_cmp_eq_u32_e32 vcc, v193, v197
	s_nop 1
	v_cndmask_b32_e64 v106, 0, 1.0, vcc
	v_pk_fma_f32 v[90:91], v[238:239], v[108:109], v[106:107] op_sel_hi:[0,1,1] neg_lo:[1,0,0] neg_hi:[1,0,0]
	v_cvt_pk_bf16_f32 v93, v90, v91
	ds_write_b64 v186, v[92:93] offset:1632
	v_cmp_eq_u32_e32 vcc, v189, v198
	s_nop 1
	v_cndmask_b32_e64 v92, 0, 1.0, vcc
	v_cmp_eq_u32_e32 vcc, v190, v198
	s_nop 1
	v_cndmask_b32_e64 v93, 0, 1.0, vcc
	v_cmp_eq_u32_e32 vcc, v192, v198
	v_pk_fma_f32 v[92:93], v[240:241], v[98:99], v[92:93] op_sel_hi:[0,1,1] neg_lo:[1,0,0] neg_hi:[1,0,0]
	v_cvt_pk_bf16_f32 v92, v92, v93
	v_cndmask_b32_e64 v99, 0, 1.0, vcc
	v_cmp_eq_u32_e32 vcc, v193, v198
	s_nop 1
	v_cndmask_b32_e64 v98, 0, 1.0, vcc
	v_pk_fma_f32 v[90:91], v[240:241], v[100:101], v[98:99] op_sel_hi:[0,1,1] neg_lo:[1,0,0] neg_hi:[1,0,0]
	v_cvt_pk_bf16_f32 v93, v90, v91
	ds_write_b64 v186, v[92:93] offset:2176
	v_cmp_eq_u32_e32 vcc, v189, v199
	s_nop 1
	v_cndmask_b32_e64 v92, 0, 1.0, vcc
	v_cmp_eq_u32_e32 vcc, v190, v199
	s_nop 1
	v_cndmask_b32_e64 v93, 0, 1.0, vcc
	v_cmp_eq_u32_e32 vcc, v192, v199
	v_pk_fma_f32 v[92:93], v[242:243], v[94:95], v[92:93] op_sel_hi:[0,1,1] neg_lo:[1,0,0] neg_hi:[1,0,0]
	v_cvt_pk_bf16_f32 v92, v92, v93
	v_cndmask_b32_e64 v95, 0, 1.0, vcc
	v_cmp_eq_u32_e32 vcc, v193, v199
	s_nop 1
	v_cndmask_b32_e64 v94, 0, 1.0, vcc
	v_pk_fma_f32 v[90:91], v[242:243], v[96:97], v[94:95] op_sel_hi:[0,1,1] neg_lo:[1,0,0] neg_hi:[1,0,0]
	v_cvt_pk_bf16_f32 v93, v90, v91
	ds_write_b64 v186, v[92:93] offset:2720
	v_cmp_eq_u32_e32 vcc, v189, v200
	s_nop 1
	v_cndmask_b32_e64 v92, 0, 1.0, vcc
	v_cmp_eq_u32_e32 vcc, v190, v200
	s_nop 1
	v_cndmask_b32_e64 v93, 0, 1.0, vcc
	v_cmp_eq_u32_e32 vcc, v192, v200
	v_pk_fma_f32 v[86:87], v[244:245], v[86:87], v[92:93] op_sel_hi:[0,1,1] neg_lo:[1,0,0] neg_hi:[1,0,0]
	v_cvt_pk_bf16_f32 v86, v86, v87
	v_cndmask_b32_e64 v93, 0, 1.0, vcc
	v_cmp_eq_u32_e32 vcc, v193, v200
	s_nop 1
	v_cndmask_b32_e64 v92, 0, 1.0, vcc
	v_pk_fma_f32 v[88:89], v[244:245], v[88:89], v[92:93] op_sel_hi:[0,1,1] neg_lo:[1,0,0] neg_hi:[1,0,0]
	v_cvt_pk_bf16_f32 v87, v88, v89
	ds_write_b64 v186, v[86:87] offset:3264
	v_cmp_eq_u32_e32 vcc, v189, v201
	s_nop 1
	v_cndmask_b32_e64 v88, 0, 1.0, vcc
	v_cmp_eq_u32_e32 vcc, v190, v201
	s_nop 1
	v_cndmask_b32_e64 v89, 0, 1.0, vcc
	v_cmp_eq_u32_e32 vcc, v192, v201
	v_pk_fma_f32 v[82:83], v[246:247], v[82:83], v[88:89] op_sel_hi:[0,1,1] neg_lo:[1,0,0] neg_hi:[1,0,0]
	v_cvt_pk_bf16_f32 v82, v82, v83
	v_cndmask_b32_e64 v89, 0, 1.0, vcc
	v_cmp_eq_u32_e32 vcc, v193, v201
	s_nop 1
	v_cndmask_b32_e64 v88, 0, 1.0, vcc
	v_pk_fma_f32 v[84:85], v[246:247], v[84:85], v[88:89] op_sel_hi:[0,1,1] neg_lo:[1,0,0] neg_hi:[1,0,0]
	v_cvt_pk_bf16_f32 v83, v84, v85
	ds_write_b64 v186, v[82:83] offset:3808
	ds_read_b32 v232, v187 offset:0
	ds_read_b32 v234, v187 offset:8
	ds_read_b32 v236, v187 offset:16
	ds_read_b32 v238, v187 offset:24
	ds_read_b32 v240, v187 offset:32
	ds_read_b32 v242, v187 offset:40
	ds_read_b32 v244, v187 offset:48
	ds_read_b32 v246, v187 offset:56
	ds_read_b128 v[82:85], v1
	ds_read_b128 v[86:89], v1 offset:64
	ds_read_b128 v[90:93], v1 offset:128
	ds_read_b128 v[94:97], v1 offset:192
	v_lshl_add_u64 v[98:99], v[150:151], 0, s[0:1]
	v_lshl_add_u64 v[192:193], v[164:165], 0, s[0:1]
	v_lshl_add_u64 v[196:197], v[166:167], 0, s[0:1]
	v_lshl_add_u64 v[100:101], v[152:153], 0, s[0:1]
	v_lshl_add_u64 v[106:107], v[156:157], 0, s[0:1]
	v_lshl_add_u64 v[108:109], v[158:159], 0, s[0:1]
	v_lshl_add_u64 v[110:111], v[160:161], 0, s[0:1]
	v_lshl_add_u64 v[112:113], v[162:163], 0, s[0:1]
	global_load_dwordx4 v[118:121], v[98:99], off nt
	global_load_dwordx4 v[134:137], v[100:101], off nt
	global_load_dwordx4 v[150:153], v[106:107], off nt
	global_load_dwordx4 v[156:159], v[108:109], off nt
	global_load_dwordx4 v[160:163], v[110:111], off nt
	global_load_dwordx4 v[164:167], v[112:113], off nt
	s_nop 0
	global_load_dwordx4 v[192:195], v[192:193], off nt
	s_nop 0
	global_load_dwordx4 v[196:199], v[196:197], off nt
	v_mov_b32_e32 v98, v188
	s_waitcnt vmcnt(15)
	s_waitcnt vmcnt(14)
	s_waitcnt vmcnt(13)
	s_waitcnt vmcnt(12)
	s_waitcnt vmcnt(11)
	s_waitcnt vmcnt(10)
	s_waitcnt vmcnt(9)
	s_waitcnt vmcnt(8)
	s_waitcnt lgkmcnt(0)
	v_pk_fma_f32 v[100:101], v[232:233], v[146:147], 0 op_sel_hi:[0,1,0] neg_lo:[1,0,0] neg_hi:[1,0,0]
	v_pk_fma_f32 v[98:99], v[232:233], v[148:149], 0 op_sel_hi:[0,1,0] neg_lo:[1,0,0] neg_hi:[1,0,0]
	v_cvt_pk_bf16_f32 v100, v100, v101
	v_cvt_pk_bf16_f32 v101, v98, v99
	ds_write_b64 v186, v[100:101]
	v_pk_fma_f32 v[100:101], v[234:235], v[142:143], 0 op_sel_hi:[0,1,0] neg_lo:[1,0,0] neg_hi:[1,0,0]
	v_pk_fma_f32 v[98:99], v[234:235], v[144:145], 0 op_sel_hi:[0,1,0] neg_lo:[1,0,0] neg_hi:[1,0,0]
	v_cvt_pk_bf16_f32 v100, v100, v101
	v_cvt_pk_bf16_f32 v101, v98, v99
	ds_write_b64 v186, v[100:101] offset:544
	v_pk_fma_f32 v[100:101], v[236:237], v[138:139], 0 op_sel_hi:[0,1,0] neg_lo:[1,0,0] neg_hi:[1,0,0]
	v_pk_fma_f32 v[98:99], v[236:237], v[140:141], 0 op_sel_hi:[0,1,0] neg_lo:[1,0,0] neg_hi:[1,0,0]
	v_cvt_pk_bf16_f32 v100, v100, v101
	v_cvt_pk_bf16_f32 v101, v98, v99
	ds_write_b64 v186, v[100:101] offset:1088
	v_pk_fma_f32 v[100:101], v[238:239], v[130:131], 0 op_sel_hi:[0,1,0] neg_lo:[1,0,0] neg_hi:[1,0,0]
	v_pk_fma_f32 v[98:99], v[238:239], v[132:133], 0 op_sel_hi:[0,1,0] neg_lo:[1,0,0] neg_hi:[1,0,0]
	v_cvt_pk_bf16_f32 v100, v100, v101
	v_cvt_pk_bf16_f32 v101, v98, v99
	ds_write_b64 v186, v[100:101] offset:1632
	v_pk_fma_f32 v[100:101], v[240:241], v[126:127], 0 op_sel_hi:[0,1,0] neg_lo:[1,0,0] neg_hi:[1,0,0]
	v_pk_fma_f32 v[98:99], v[240:241], v[128:129], 0 op_sel_hi:[0,1,0] neg_lo:[1,0,0] neg_hi:[1,0,0]
	v_cvt_pk_bf16_f32 v100, v100, v101
	v_cvt_pk_bf16_f32 v101, v98, v99
	ds_write_b64 v186, v[100:101] offset:2176
	v_pk_fma_f32 v[100:101], v[242:243], v[122:123], 0 op_sel_hi:[0,1,0] neg_lo:[1,0,0] neg_hi:[1,0,0]
	v_pk_fma_f32 v[98:99], v[242:243], v[124:125], 0 op_sel_hi:[0,1,0] neg_lo:[1,0,0] neg_hi:[1,0,0]
	v_cvt_pk_bf16_f32 v100, v100, v101
	v_cvt_pk_bf16_f32 v101, v98, v99
	ds_write_b64 v186, v[100:101] offset:2720
	v_pk_fma_f32 v[100:101], v[244:245], v[114:115], 0 op_sel_hi:[0,1,0] neg_lo:[1,0,0] neg_hi:[1,0,0]
	v_pk_fma_f32 v[98:99], v[244:245], v[116:117], 0 op_sel_hi:[0,1,0] neg_lo:[1,0,0] neg_hi:[1,0,0]
	v_cvt_pk_bf16_f32 v100, v100, v101
	v_cvt_pk_bf16_f32 v101, v98, v99
	ds_write_b64 v186, v[100:101] offset:3264
	v_pk_fma_f32 v[100:101], v[246:247], v[102:103], 0 op_sel_hi:[0,1,0] neg_lo:[1,0,0] neg_hi:[1,0,0]
	v_pk_fma_f32 v[98:99], v[246:247], v[104:105], 0 op_sel_hi:[0,1,0] neg_lo:[1,0,0] neg_hi:[1,0,0]
	v_cvt_pk_bf16_f32 v100, v100, v101
	v_cvt_pk_bf16_f32 v101, v98, v99
	ds_write_b64 v186, v[100:101] offset:3808
	ds_read_b32 v232, v187 offset:64
	ds_read_b32 v234, v187 offset:72
	ds_read_b32 v236, v187 offset:80
	ds_read_b32 v238, v187 offset:88
	ds_read_b32 v240, v187 offset:96
	ds_read_b32 v242, v187 offset:104
	ds_read_b32 v244, v187 offset:112
	ds_read_b32 v246, v187 offset:120
	ds_read_b128 v[98:101], v1
	ds_read_b128 v[102:105], v1 offset:64
	ds_read_b128 v[106:109], v1 offset:128
	ds_read_b128 v[110:113], v1 offset:192
	v_lshl_add_u64 v[114:115], v[168:169], 0, s[0:1]
	v_lshl_add_u64 v[126:127], v[176:177], 0, s[0:1]
	v_lshl_add_u64 v[176:177], v[180:181], 0, s[0:1]
	v_lshl_add_u64 v[180:181], v[182:183], 0, s[0:1]
	v_lshl_add_u64 v[116:117], v[170:171], 0, s[0:1]
	v_lshl_add_u64 v[122:123], v[172:173], 0, s[0:1]
	v_lshl_add_u64 v[124:125], v[174:175], 0, s[0:1]
	v_lshl_add_u64 v[128:129], v[178:179], 0, s[0:1]
	global_load_dwordx4 v[130:133], v[114:115], off nt
	global_load_dwordx4 v[138:141], v[116:117], off nt
	global_load_dwordx4 v[142:145], v[122:123], off nt
	global_load_dwordx4 v[146:149], v[124:125], off nt
	global_load_dwordx4 v[168:171], v[126:127], off nt
	global_load_dwordx4 v[172:175], v[128:129], off nt
	s_nop 0
	global_load_dwordx4 v[176:179], v[176:177], off nt
	s_nop 0
	global_load_dwordx4 v[180:183], v[180:181], off nt
	v_mov_b32_e32 v114, v188
	s_waitcnt vmcnt(15)
	s_waitcnt vmcnt(14)
	s_waitcnt vmcnt(13)
	s_waitcnt vmcnt(12)
	s_waitcnt vmcnt(11)
	s_waitcnt vmcnt(10)
	s_waitcnt vmcnt(9)
	s_waitcnt vmcnt(8)
	s_waitcnt lgkmcnt(0)
	v_pk_fma_f32 v[116:117], v[232:233], v[118:119], 0 op_sel_hi:[0,1,0] neg_lo:[1,0,0] neg_hi:[1,0,0]
	v_pk_fma_f32 v[114:115], v[232:233], v[120:121], 0 op_sel_hi:[0,1,0] neg_lo:[1,0,0] neg_hi:[1,0,0]
	v_cvt_pk_bf16_f32 v116, v116, v117
	v_cvt_pk_bf16_f32 v117, v114, v115
	ds_write_b64 v186, v[116:117]
	v_pk_fma_f32 v[116:117], v[234:235], v[134:135], 0 op_sel_hi:[0,1,0] neg_lo:[1,0,0] neg_hi:[1,0,0]
	v_pk_fma_f32 v[114:115], v[234:235], v[136:137], 0 op_sel_hi:[0,1,0] neg_lo:[1,0,0] neg_hi:[1,0,0]
	v_cvt_pk_bf16_f32 v116, v116, v117
	v_cvt_pk_bf16_f32 v117, v114, v115
	ds_write_b64 v186, v[116:117] offset:544
	v_pk_fma_f32 v[116:117], v[236:237], v[150:151], 0 op_sel_hi:[0,1,0] neg_lo:[1,0,0] neg_hi:[1,0,0]
	v_pk_fma_f32 v[114:115], v[236:237], v[152:153], 0 op_sel_hi:[0,1,0] neg_lo:[1,0,0] neg_hi:[1,0,0]
	v_cvt_pk_bf16_f32 v116, v116, v117
	v_cvt_pk_bf16_f32 v117, v114, v115
	ds_write_b64 v186, v[116:117] offset:1088
	v_pk_fma_f32 v[116:117], v[238:239], v[156:157], 0 op_sel_hi:[0,1,0] neg_lo:[1,0,0] neg_hi:[1,0,0]
	v_pk_fma_f32 v[114:115], v[238:239], v[158:159], 0 op_sel_hi:[0,1,0] neg_lo:[1,0,0] neg_hi:[1,0,0]
	v_cvt_pk_bf16_f32 v116, v116, v117
	v_cvt_pk_bf16_f32 v117, v114, v115
	ds_write_b64 v186, v[116:117] offset:1632
	v_pk_fma_f32 v[116:117], v[240:241], v[160:161], 0 op_sel_hi:[0,1,0] neg_lo:[1,0,0] neg_hi:[1,0,0]
	v_pk_fma_f32 v[114:115], v[240:241], v[162:163], 0 op_sel_hi:[0,1,0] neg_lo:[1,0,0] neg_hi:[1,0,0]
	v_cvt_pk_bf16_f32 v116, v116, v117
	v_cvt_pk_bf16_f32 v117, v114, v115
	ds_write_b64 v186, v[116:117] offset:2176
	v_pk_fma_f32 v[116:117], v[242:243], v[164:165], 0 op_sel_hi:[0,1,0] neg_lo:[1,0,0] neg_hi:[1,0,0]
	v_pk_fma_f32 v[114:115], v[242:243], v[166:167], 0 op_sel_hi:[0,1,0] neg_lo:[1,0,0] neg_hi:[1,0,0]
	v_cvt_pk_bf16_f32 v116, v116, v117
	v_cvt_pk_bf16_f32 v117, v114, v115
	ds_write_b64 v186, v[116:117] offset:2720
	v_pk_fma_f32 v[116:117], v[244:245], v[192:193], 0 op_sel_hi:[0,1,0] neg_lo:[1,0,0] neg_hi:[1,0,0]
	v_pk_fma_f32 v[114:115], v[244:245], v[194:195], 0 op_sel_hi:[0,1,0] neg_lo:[1,0,0] neg_hi:[1,0,0]
	v_cvt_pk_bf16_f32 v116, v116, v117
	v_cvt_pk_bf16_f32 v117, v114, v115
	ds_write_b64 v186, v[116:117] offset:3264
	v_pk_fma_f32 v[116:117], v[246:247], v[196:197], 0 op_sel_hi:[0,1,0] neg_lo:[1,0,0] neg_hi:[1,0,0]
	v_pk_fma_f32 v[114:115], v[246:247], v[198:199], 0 op_sel_hi:[0,1,0] neg_lo:[1,0,0] neg_hi:[1,0,0]
	v_cvt_pk_bf16_f32 v116, v116, v117
	v_cvt_pk_bf16_f32 v117, v114, v115
	ds_write_b64 v186, v[116:117] offset:3808
	ds_read_b32 v232, v187 offset:128
	ds_read_b32 v234, v187 offset:136
	ds_read_b32 v236, v187 offset:144
	ds_read_b32 v238, v187 offset:152
	ds_read_b32 v240, v187 offset:160
	ds_read_b32 v242, v187 offset:168
	ds_read_b32 v244, v187 offset:176
	ds_read_b32 v246, v187 offset:184
	ds_read_b128 v[114:117], v1
	ds_read_b128 v[118:121], v1 offset:64
	ds_read_b128 v[122:125], v1 offset:128
	ds_read_b128 v[126:129], v1 offset:192
	s_waitcnt vmcnt(7)
	s_waitcnt vmcnt(6)
	s_waitcnt vmcnt(5)
	s_waitcnt vmcnt(4)
	s_waitcnt vmcnt(3)
	s_waitcnt vmcnt(2)
	s_waitcnt vmcnt(1)
	s_waitcnt vmcnt(0)
	s_waitcnt lgkmcnt(0)
	v_pk_fma_f32 v[130:131], v[232:233], v[130:131], 0 op_sel_hi:[0,1,0] neg_lo:[1,0,0] neg_hi:[1,0,0]
	v_pk_fma_f32 v[132:133], v[232:233], v[132:133], 0 op_sel_hi:[0,1,0] neg_lo:[1,0,0] neg_hi:[1,0,0]
	v_cvt_pk_bf16_f32 v130, v130, v131
	v_cvt_pk_bf16_f32 v131, v132, v133
	ds_write_b64 v186, v[130:131]
	v_pk_fma_f32 v[132:133], v[234:235], v[138:139], 0 op_sel_hi:[0,1,0] neg_lo:[1,0,0] neg_hi:[1,0,0]
	v_pk_fma_f32 v[130:131], v[234:235], v[140:141], 0 op_sel_hi:[0,1,0] neg_lo:[1,0,0] neg_hi:[1,0,0]
	v_cvt_pk_bf16_f32 v132, v132, v133
	v_cvt_pk_bf16_f32 v133, v130, v131
	ds_write_b64 v186, v[132:133] offset:544
	v_pk_fma_f32 v[132:133], v[236:237], v[142:143], 0 op_sel_hi:[0,1,0] neg_lo:[1,0,0] neg_hi:[1,0,0]
	v_pk_fma_f32 v[130:131], v[236:237], v[144:145], 0 op_sel_hi:[0,1,0] neg_lo:[1,0,0] neg_hi:[1,0,0]
	v_cvt_pk_bf16_f32 v132, v132, v133
	v_cvt_pk_bf16_f32 v133, v130, v131
	ds_write_b64 v186, v[132:133] offset:1088
	v_pk_fma_f32 v[132:133], v[238:239], v[146:147], 0 op_sel_hi:[0,1,0] neg_lo:[1,0,0] neg_hi:[1,0,0]
	v_pk_fma_f32 v[130:131], v[238:239], v[148:149], 0 op_sel_hi:[0,1,0] neg_lo:[1,0,0] neg_hi:[1,0,0]
	v_cvt_pk_bf16_f32 v132, v132, v133
	v_cvt_pk_bf16_f32 v133, v130, v131
	ds_write_b64 v186, v[132:133] offset:1632
	v_pk_fma_f32 v[132:133], v[240:241], v[168:169], 0 op_sel_hi:[0,1,0] neg_lo:[1,0,0] neg_hi:[1,0,0]
	v_pk_fma_f32 v[130:131], v[240:241], v[170:171], 0 op_sel_hi:[0,1,0] neg_lo:[1,0,0] neg_hi:[1,0,0]
	v_cvt_pk_bf16_f32 v132, v132, v133
	v_cvt_pk_bf16_f32 v133, v130, v131
	ds_write_b64 v186, v[132:133] offset:2176
	v_pk_fma_f32 v[132:133], v[242:243], v[172:173], 0 op_sel_hi:[0,1,0] neg_lo:[1,0,0] neg_hi:[1,0,0]
	v_pk_fma_f32 v[130:131], v[242:243], v[174:175], 0 op_sel_hi:[0,1,0] neg_lo:[1,0,0] neg_hi:[1,0,0]
	v_cvt_pk_bf16_f32 v132, v132, v133
	v_cvt_pk_bf16_f32 v133, v130, v131
	ds_write_b64 v186, v[132:133] offset:2720
	v_pk_fma_f32 v[132:133], v[244:245], v[176:177], 0 op_sel_hi:[0,1,0] neg_lo:[1,0,0] neg_hi:[1,0,0]
	v_pk_fma_f32 v[130:131], v[244:245], v[178:179], 0 op_sel_hi:[0,1,0] neg_lo:[1,0,0] neg_hi:[1,0,0]
	v_cvt_pk_bf16_f32 v132, v132, v133
	v_cvt_pk_bf16_f32 v133, v130, v131
	ds_write_b64 v186, v[132:133] offset:3264
	v_pk_fma_f32 v[132:133], v[246:247], v[180:181], 0 op_sel_hi:[0,1,0] neg_lo:[1,0,0] neg_hi:[1,0,0]
	v_pk_fma_f32 v[130:131], v[246:247], v[182:183], 0 op_sel_hi:[0,1,0] neg_lo:[1,0,0] neg_hi:[1,0,0]
	v_cvt_pk_bf16_f32 v132, v132, v133
	v_cvt_pk_bf16_f32 v133, v130, v131
	ds_write_b64 v186, v[132:133] offset:3808
	ds_read_b128 v[130:133], v1
	ds_read_b128 v[134:137], v1 offset:64
	ds_read_b128 v[138:141], v1 offset:128
	ds_read_b128 v[142:145], v1 offset:192
	s_ashr_i32 s7, s6, 31
	s_lshl_b64 s[0:1], s[6:7], 2
	s_add_u32 s0, s4, s0
	s_addc_u32 s1, s5, s1
	v_lshlrev_b32_e32 v1, 4, v0
	s_add_i32 s20, s34, 1
	s_add_i32 s34, s34, -1
	v_or_b32_e32 v153, s10, v206
	s_xor_b32 s26, s3, 2
	s_lshl_b64 s[10:11], s[10:11], 3
	s_and_b32 s20, s20, 3
	s_and_b32 s27, s34, 3
	s_add_u32 s10, s14, s10
	s_addc_u32 s11, s15, s11
	s_lshl_b32 s42, s35, 2
	s_add_i32 s41, s42, 0x26a20
	s_add_i32 s42, s42, 0x26a00
	v_lshlrev_b32_e32 v190, 3, v206
	s_cmp_eq_u32 s35, 3
	v_lshlrev_b32_e32 v150, 3, v0
	v_and_b32_e32 v151, 1, v0
	v_lshl_add_u64 v[0:1], v[154:155], 3, s[14:15]
	v_lshl_add_u64 v[192:193], s[10:11], 0, v[190:191]
	s_cselect_b64 s[10:11], -1, 0
	s_lshl_b32 s14, s3, 2
	s_add_u32 s24, s16, s14
	v_or_b32_e32 v155, 0x20000, v150
	v_add_u32_e32 v156, 0x20880, v150
	v_lshlrev_b32_e32 v150, 1, v153
	s_addc_u32 s25, s17, 0
	s_lshl_b32 s43, s3, 9
	v_lshl_add_u32 v212, s26, 9, v150
	s_lshl_b32 s15, s26, 8
	s_add_i32 s26, s43, 0x200
	v_mov_b32_e32 v152, 0x880
	v_cmp_lt_u32_e64 s[0:1], 15, v206
	v_cmp_eq_u32_e32 vcc, 1, v151
	s_and_b32 s45, s26, 0x600
	s_add_i32 s26, s43, 0x500
	v_cndmask_b32_e32 v211, 0, v152, vcc
	s_and_b32 s56, s26, 0x700
	s_add_i32 s26, s43, 0x540
	v_lshl_add_u32 v213, s20, 9, v150
	v_lshl_add_u32 v214, s27, 9, v150
	s_and_b32 s57, s26, 0x740
	s_add_i32 s26, s43, 0x580
	s_and_b32 s58, s26, 0x780
	s_add_i32 s26, s43, 0x5c0
	s_and_b32 s59, s26, 0x7c0
	s_add_i32 s26, s43, 0x600
	s_and_b32 s60, s26, 0x600
	s_add_i32 s26, s43, 0x640
	s_and_b32 s61, s26, 0x640
	s_add_i32 s26, s43, 0x680
	s_and_b32 s62, s26, 0x680
	s_add_i32 s26, s43, 0x6c0
	s_and_b32 s63, s26, 0x6c0
	s_add_i32 s26, s43, 0x700
	s_and_b32 s64, s26, 0x700
	s_add_i32 s26, s43, 0x740
	s_and_b32 s65, s26, 0x740
	s_add_i32 s26, s43, 0x780
	s_lshl_b32 s14, s27, 8
	s_lshl_b32 s20, s20, 8
	s_add_i32 s27, s43, 0x240
	s_add_i32 s28, s43, 0x280
	s_add_i32 s29, s43, 0x2c0
	s_add_i32 s30, s43, 0x300
	s_add_i32 s31, s43, 0x340
	s_add_i32 s34, s43, 0x380
	s_add_i32 s35, s43, 0x3c0
	s_add_i32 s36, s43, 0x440
	s_add_i32 s37, s43, 0x480
	s_add_i32 s38, s43, 0x4c0
	s_and_b32 s66, s26, 0x780
	s_add_i32 s26, s43, 0x7c0
	s_mul_hi_i32 s23, s18, 0x65
	s_mul_i32 s22, s18, 0x65
	v_cmp_eq_u32_e64 s[4:5], 1, v185
	v_cmp_eq_u32_e64 s[6:7], 2, v185
	v_cmp_eq_u32_e64 s[8:9], 63, v206
	s_xor_b32 s44, s43, 0x400
	s_and_b32 s46, s27, 0x640
	s_and_b32 s47, s28, 0x680
	s_waitcnt lgkmcnt(0)
	v_mov_b32_e32 v146, 0x20000
	s_and_b32 s48, s29, 0x6c0
	s_and_b32 s49, s30, 0x700
	s_and_b32 s50, s31, 0x740
	s_and_b32 s51, s34, 0x780
	s_and_b32 s52, s35, 0x7c0
	s_and_b32 s53, s36, 0x640
	s_and_b32 s54, s37, 0x680
	s_and_b32 s55, s38, 0x6c0
	s_and_b32 s67, s26, 0x7c0
	s_and_b64 s[26:27], s[10:11], s[12:13]
	v_lshl_add_u32 v215, v154, 1, v146
	v_mov_b32_e32 v216, 1
	s_lshl_b32 s28, s14, 3
	s_lshl_b32 s30, s15, 3
	s_lshl_b32 s34, s20, 3
	s_movk_i32 s68, 0x7fff
	s_mov_b32 s69, 0
	v_and_b32_e32 v220, 24, v206
	v_lshlrev_b32_e32 v220, 2, v220
	v_and_b32_e32 v221, 2, v206
	v_lshl_or_b32 v220, v221, 3, v220
	v_and_b32_e32 v221, 32, v206
	v_lshrrev_b32_e32 v221, 2, v221
	v_or_b32_e32 v220, v220, v221
	v_and_b32_e32 v221, 4, v206
	v_or_b32_e32 v220, v220, v221
	v_and_b32_e32 v221, 1, v206
	v_lshl_or_b32 v220, v221, 1, v220
	v_mov_b32_e32 v220, v254
	s_lshr_b32 s76, s19, 8
	s_add_i32 s76, s76, 0x20000
	v_add_u32_e32 v220, s76, v220
	v_add_u32_e32 v225, s45, v220
	v_add_u32_e32 v226, s44, v220
	v_add_u32_e32 v227, s60, v220
	v_add_u32_e32 v228, s43, v220
	v_and_b32_e32 v221, 1, v206
	v_mul_u32_u24_e32 v221, 0x880, v221
	v_lshrrev_b32_e32 v220, 4, v206
	v_lshl_add_u32 v221, v220, 5, v221
	v_and_b32_e32 v220, 2, v206
	v_lshl_add_u32 v221, v220, 3, v221
	v_add_u32_e32 v222, 0x20000, v221
	v_cmp_ne_u32_e32 vcc, 0, v220
	v_mov_b32_e32 v220, 0x44444444
	v_mov_b32_e32 v221, 0xeeeeeeee
	s_nop 1
	v_cndmask_b32_e32 v223, v220, v221, vcc
	v_cmp_lt_u32_e64 s[74:75], 47, v206
	s_lshr_b32 s82, s19, 15
	s_mul_i32 s83, s82, 0x1100
	s_add_i32 s83, s83, 0x22200
	v_lshl_add_u32 v254, v206, 2, s83
	v_mov_b32_e32 v220, s41
	s_nop 1
	v_cndmask_b32_e64 v254, v254, v220, s[12:13]
	v_mov_b32_e32 v224, v184
	s_mov_b32 s86, 0x55555555
	s_mov_b32 s87, 0x55555555
	s_lshr_b32 s78, s19, 15
	s_lshl_b32 s79, s78, 11
	v_add_u32_e32 v255, s79, v224
	ds_read_b128 v[166:169], v224 offset:0
	ds_read_b128 v[170:173], v224 offset:1024
	ds_read_b128 v[174:177], v224 offset:2048
	ds_read_b128 v[178:181], v224 offset:3072
	ds_read_b128 v[182:185], v224 offset:4096
	ds_read_b128 v[186:189], v224 offset:5120
	s_mov_b32 s20, 0
